# speedup vs baseline: 1.0083x; 1.0011x over previous
_Z4k_k2ILb0EEvPKDF16_S1_PKfS3_S3_S1_S1_PfS3_S3_S1_PDF16_PKiS4_S4_:
	s_load_dwordx2 s[24:25], s[0:1], 0x58
	s_load_dwordx8 s[4:11], s[0:1], 0x38
	s_load_dwordx4 s[20:23], s[0:1], 0x0
	s_load_dwordx8 s[12:19], s[0:1], 0x18
	s_load_dwordx2 s[54:55], s[0:1], 0x10
	s_lshl_b32 s3, s2, 5
	s_and_b32 s3, s3, 0xe0
	s_lshr_b32 s26, s2, 3
	s_or_b32 s3, s3, s26
	s_movk_i32 s26, 0x100
	s_lshl_b32 s28, s3, 5
	v_cmp_gt_u32_e32 vcc, s26, v0
	v_mov_b32_e32 v67, 0
	v_lshlrev_b32_e32 v66, 4, v0
	s_lshl_b32 s0, s3, 1
	s_and_b32 s26, s0, 0xffffffe
	s_mov_b32 s27, 0
	s_waitcnt lgkmcnt(0)
	v_lshl_add_u64 v[2:3], s[16:17], 0, v[66:67]
	s_lshl_b64 s[0:1], s[26:27], 13
	s_or_b32 s26, s26, 1
	v_lshl_add_u64 v[4:5], v[2:3], 0, s[0:1]
	s_lshl_b64 s[0:1], s[26:27], 13
	v_lshl_add_u64 v[2:3], v[2:3], 0, s[0:1]
	global_load_dwordx4 v[68:71], v[4:5], off
	global_load_dwordx4 v[72:75], v[2:3], off
	v_lshl_add_u64 v[2:3], s[12:13], 0, v[66:67]
	s_movk_i32 s29, 0x2000
	v_add_co_u32_e32 v4, vcc, s29, v2
	s_movk_i32 s52, 0x4000
	s_nop 0
	v_addc_co_u32_e32 v5, vcc, 0, v3, vcc
	v_add_co_u32_e32 v18, vcc, s52, v2
	s_movk_i32 s33, 0x6000
	s_nop 0
	v_addc_co_u32_e32 v19, vcc, 0, v3, vcc
	s_lshl_b32 s26, s3, 2
	global_load_dwordx4 v[14:17], v66, s[12:13]
	global_load_dwordx4 v[10:13], v[4:5], off
	global_load_dwordx4 v[6:9], v[18:19], off
	v_add_co_u32_e32 v18, vcc, s33, v2
	s_add_u32 s0, s24, 0x800000
	s_nop 0
	v_addc_co_u32_e32 v19, vcc, 0, v3, vcc
	s_addc_u32 s1, s25, 0
	s_lshl_b64 s[12:13], s[26:27], 13
	v_lshlrev_b32_e32 v20, 2, v0
	global_load_dwordx4 v[2:5], v[18:19], off
	global_load_dword v1, v20, s[14:15]
	v_or_b32_e32 v18, s12, v66
	v_mov_b32_e32 v19, s13
	s_or_b32 s12, s26, 1
	s_mov_b32 s13, s27
	s_lshl_b64 s[12:13], s[12:13], 13
	v_lshl_add_u64 v[76:77], s[22:23], 0, v[18:19]
	v_lshl_add_u64 v[78:79], s[20:21], 0, v[18:19]
	v_lshl_add_u64 v[80:81], s[0:1], 0, v[18:19]
	v_or_b32_e32 v18, s12, v66
	v_mov_b32_e32 v19, s13
	s_or_b32 s12, s26, 2
	s_mov_b32 s13, s27
	s_lshl_b64 s[12:13], s[12:13], 13
	s_or_b32 s26, s26, 3
	v_lshl_add_u64 v[82:83], s[22:23], 0, v[18:19]
	v_lshl_add_u64 v[84:85], s[20:21], 0, v[18:19]
	v_lshl_add_u64 v[86:87], s[0:1], 0, v[18:19]
	v_or_b32_e32 v18, s12, v66
	v_mov_b32_e32 v19, s13
	s_lshl_b64 s[12:13], s[26:27], 13
	v_lshl_add_u64 v[88:89], s[22:23], 0, v[18:19]
	v_lshl_add_u64 v[90:91], s[20:21], 0, v[18:19]
	v_lshl_add_u64 v[92:93], s[0:1], 0, v[18:19]
	v_or_b32_e32 v18, s12, v66
	v_mov_b32_e32 v19, s13
	v_lshl_add_u64 v[94:95], s[22:23], 0, v[18:19]
	v_lshl_add_u64 v[96:97], s[20:21], 0, v[18:19]
	v_lshl_add_u64 v[98:99], s[0:1], 0, v[18:19]
	global_load_dwordx4 v[62:65], v[76:77], off
	global_load_dwordx4 v[54:57], v[78:79], off
	global_load_dwordx4 v[58:61], v[80:81], off
	v_mov_b64_e32 v[212:213], v[82:83]
	v_mov_b64_e32 v[214:215], v[84:85]
	v_mov_b64_e32 v[216:217], v[86:87]
	v_mov_b64_e32 v[218:219], v[88:89]
	v_mov_b64_e32 v[220:221], v[90:91]
	v_mov_b64_e32 v[222:223], v[92:93]
	v_mov_b64_e32 v[224:225], v[94:95]
	v_mov_b64_e32 v[226:227], v[96:97]
	v_mov_b64_e32 v[228:229], v[98:99]
	s_lshl_b32 s30, s28, 7
	s_add_u32 s54, s54, s30
	s_addc_u32 s55, s55, 0
	s_load_dwordx16 s[36:51], s[54:55], 0x0
	s_load_dwordx16 s[72:87], s[54:55], 0x40
	s_load_dwordx16 s[56:71], s[54:55], 0x80
	s_load_dwordx8 s[88:95], s[54:55], 0xc0
	s_load_dwordx4 s[96:99], s[54:55], 0xe0
	s_load_dwordx4 s[20:23], s[54:55], 0xf0
	v_lshrrev_b32_e32 v196, 6, v0
	s_nop 1
	v_readfirstlane_b32 s16, v196
	s_nop 3
	s_lshl_b32 s16, s16, 9
	s_add_u32 s16, s54, s16
	s_addc_u32 s17, s55, 0
	s_load_dword s30, s[16:17], 0x0
	s_load_dword s30, s[16:17], 0x40
	s_load_dword s30, s[16:17], 0x80
	s_load_dword s30, s[16:17], 0xc0
	s_load_dword s30, s[16:17], 0x100
	s_load_dword s30, s[16:17], 0x140
	s_load_dword s30, s[16:17], 0x180
	s_load_dword s30, s[16:17], 0x1c0
	s_waitcnt vmcnt(9)
	v_cvt_f32_f16_e32 v134, v68
	v_cvt_f32_f16_sdwa v135, v68 dst_sel:DWORD dst_unused:UNUSED_PAD src0_sel:WORD_1
	v_cvt_f32_f16_e32 v136, v69
	v_cvt_f32_f16_sdwa v137, v69 dst_sel:DWORD dst_unused:UNUSED_PAD src0_sel:WORD_1
	v_cvt_f32_f16_e32 v138, v70
	v_cvt_f32_f16_sdwa v139, v70 dst_sel:DWORD dst_unused:UNUSED_PAD src0_sel:WORD_1
	v_cvt_f32_f16_e32 v140, v71
	v_cvt_f32_f16_sdwa v141, v71 dst_sel:DWORD dst_unused:UNUSED_PAD src0_sel:WORD_1
	s_waitcnt vmcnt(8)
	v_cvt_f32_f16_e32 v142, v72
	v_cvt_f32_f16_sdwa v143, v72 dst_sel:DWORD dst_unused:UNUSED_PAD src0_sel:WORD_1
	v_cvt_f32_f16_e32 v144, v73
	v_cvt_f32_f16_sdwa v145, v73 dst_sel:DWORD dst_unused:UNUSED_PAD src0_sel:WORD_1
	v_cvt_f32_f16_e32 v146, v74
	v_cvt_f32_f16_sdwa v147, v74 dst_sel:DWORD dst_unused:UNUSED_PAD src0_sel:WORD_1
	v_cvt_f32_f16_e32 v148, v75
	v_cvt_f32_f16_sdwa v149, v75 dst_sel:DWORD dst_unused:UNUSED_PAD src0_sel:WORD_1
	s_waitcnt lgkmcnt(0)
	v_lshlrev_b32_e32 v68, 1, v0
	s_waitcnt vmcnt(2)
	v_cvt_f32_f16_e32 v150, v62
	s_waitcnt vmcnt(1)
	v_pk_mul_f32 v[154:155], v[150:151], v[14:15] op_sel_hi:[0,1]
	v_exp_f32_e32 v154, v154
	v_exp_f32_e32 v155, v155
	v_pk_mul_f32 v[156:157], v[150:151], v[16:17] op_sel_hi:[0,1]
	v_exp_f32_e32 v156, v156
	v_exp_f32_e32 v157, v157
	v_fma_mix_f32 v152, v150, v54, 0 op_sel_hi:[0,1,0]
	v_pk_mul_f32 v[134:135], v[154:155], v[134:135]
	v_pk_fma_f32 v[134:135], v[152:153], s[36:37], v[134:135] op_sel_hi:[0, 1, 1]
	v_pk_fma_f32 v[70:71], s[72:73], v[134:135], 0 op_sel_hi:[1, 1, 0]
	v_pk_mul_f32 v[86:87], v[156:157], v[136:137]
	s_nop 0
	v_pk_fma_f32 v[136:137], v[152:153], s[38:39], v[86:87] op_sel_hi:[0, 1, 1]
	v_pk_mul_f32 v[72:73], v[150:151], v[10:11] op_sel_hi:[0,1]
	v_exp_f32_e32 v72, v72
	v_exp_f32_e32 v73, v73
	v_pk_mul_f32 v[86:87], v[150:151], v[12:13] op_sel_hi:[0,1]
	v_exp_f32_e32 v86, v86
	v_exp_f32_e32 v87, v87
	v_pk_mul_f32 v[72:73], v[72:73], v[138:139]
	v_pk_fma_f32 v[70:71], s[74:75], v[136:137], v[70:71]
	v_pk_fma_f32 v[138:139], v[152:153], s[40:41], v[72:73] op_sel_hi:[0, 1, 1]
	v_pk_mul_f32 v[72:73], v[86:87], v[140:141]
	v_pk_mul_f32 v[74:75], v[150:151], v[8:9] op_sel_hi:[0,1]
	v_pk_fma_f32 v[140:141], v[152:153], s[42:43], v[72:73] op_sel_hi:[0, 1, 1]
	v_pk_mul_f32 v[72:73], v[150:151], v[6:7] op_sel_hi:[0,1]
	v_exp_f32_e32 v72, v72
	v_exp_f32_e32 v73, v73
	v_exp_f32_e32 v74, v74
	v_exp_f32_e32 v75, v75
	v_pk_fma_f32 v[70:71], s[76:77], v[138:139], v[70:71]
	v_pk_mul_f32 v[72:73], v[72:73], v[142:143]
	v_pk_fma_f32 v[70:71], s[78:79], v[140:141], v[70:71]
	v_pk_fma_f32 v[142:143], v[152:153], s[44:45], v[72:73] op_sel_hi:[0, 1, 1]
	v_pk_mul_f32 v[72:73], v[74:75], v[144:145]
	v_pk_mul_f32 v[74:75], v[150:151], v[4:5] op_sel_hi:[0,1]
	v_pk_fma_f32 v[144:145], v[152:153], s[46:47], v[72:73] op_sel_hi:[0, 1, 1]
	v_pk_mul_f32 v[72:73], v[150:151], v[2:3] op_sel_hi:[0,1]
	v_exp_f32_e32 v72, v72
	v_exp_f32_e32 v73, v73
	v_exp_f32_e32 v74, v74
	v_exp_f32_e32 v75, v75
	v_pk_fma_f32 v[70:71], s[80:81], v[142:143], v[70:71]
	v_pk_mul_f32 v[72:73], v[72:73], v[146:147]
	v_pk_fma_f32 v[70:71], s[82:83], v[144:145], v[70:71]
	v_pk_fma_f32 v[146:147], v[152:153], s[48:49], v[72:73] op_sel_hi:[0, 1, 1]
	v_pk_mul_f32 v[72:73], v[74:75], v[148:149]
	v_pk_fma_f32 v[70:71], s[84:85], v[146:147], v[70:71]
	v_pk_fma_f32 v[148:149], v[152:153], s[50:51], v[72:73] op_sel_hi:[0, 1, 1]
	v_pk_fma_f32 v[70:71], s[86:87], v[148:149], v[70:71]
	s_nop 0
	v_add_f32_e32 v69, v70, v71
	v_fma_mix_f32 v69, v1, v54, v69 op_sel_hi:[0,1,0]
	s_waitcnt vmcnt(0)
	v_fma_mixlo_f16 v69, v69, v58, 0 op_sel_hi:[0,1,0]
	ds_write_b16 v68, v69 offset:4096
	global_load_dwordx4 v[50:53], v[212:213], off
	global_load_dwordx4 v[42:45], v[214:215], off
	global_load_dwordx4 v[46:49], v[216:217], off
	global_load_dwordx4 v[38:41], v[218:219], off
	global_load_dwordx4 v[30:33], v[220:221], off
	global_load_dwordx4 v[34:37], v[222:223], off
	global_load_dwordx4 v[26:29], v[224:225], off
	global_load_dwordx4 v[18:21], v[226:227], off
	global_load_dwordx4 v[22:25], v[228:229], off
	s_waitcnt lgkmcnt(0)
	s_load_dwordx16 s[36:51], s[54:55], 0x100
	s_load_dwordx16 s[72:87], s[54:55], 0x140
	v_cvt_f32_f16_sdwa v62, v62 dst_sel:DWORD dst_unused:UNUSED_PAD src0_sel:WORD_1
	v_pk_mul_f32 v[152:153], v[62:63], v[14:15] op_sel_hi:[0,1]
	v_exp_f32_e32 v152, v152
	v_exp_f32_e32 v153, v153
	v_pk_mul_f32 v[154:155], v[62:63], v[16:17] op_sel_hi:[0,1]
	v_exp_f32_e32 v154, v154
	v_exp_f32_e32 v155, v155
	v_fma_mix_f32 v150, v62, v54, 0 op_sel:[0,1,0] op_sel_hi:[0,1,0]
	v_pk_mul_f32 v[134:135], v[152:153], v[134:135]
	v_pk_fma_f32 v[134:135], v[150:151], s[56:57], v[134:135] op_sel_hi:[0, 1, 1]
	v_pk_fma_f32 v[102:103], s[88:89], v[134:135], 0 op_sel_hi:[1, 1, 0]
	v_pk_mul_f32 v[118:119], v[154:155], v[136:137]
	s_nop 0
	v_pk_fma_f32 v[136:137], v[150:151], s[58:59], v[118:119] op_sel_hi:[0, 1, 1]
	v_pk_mul_f32 v[104:105], v[62:63], v[10:11] op_sel_hi:[0,1]
	v_exp_f32_e32 v104, v104
	v_exp_f32_e32 v105, v105
	v_pk_mul_f32 v[118:119], v[62:63], v[12:13] op_sel_hi:[0,1]
	v_exp_f32_e32 v118, v118
	v_exp_f32_e32 v119, v119
	v_pk_mul_f32 v[104:105], v[104:105], v[138:139]
	v_pk_fma_f32 v[102:103], s[90:91], v[136:137], v[102:103]
	v_pk_fma_f32 v[138:139], v[150:151], s[60:61], v[104:105] op_sel_hi:[0, 1, 1]
	v_pk_mul_f32 v[104:105], v[118:119], v[140:141]
	v_pk_mul_f32 v[106:107], v[62:63], v[8:9] op_sel_hi:[0,1]
	v_pk_fma_f32 v[140:141], v[150:151], s[62:63], v[104:105] op_sel_hi:[0, 1, 1]
	v_pk_mul_f32 v[104:105], v[62:63], v[6:7] op_sel_hi:[0,1]
	v_exp_f32_e32 v104, v104
	v_exp_f32_e32 v105, v105
	v_exp_f32_e32 v106, v106
	v_exp_f32_e32 v107, v107
	v_pk_fma_f32 v[102:103], s[92:93], v[138:139], v[102:103]
	v_pk_mul_f32 v[104:105], v[104:105], v[142:143]
	v_pk_fma_f32 v[102:103], s[94:95], v[140:141], v[102:103]
	v_pk_fma_f32 v[142:143], v[150:151], s[64:65], v[104:105] op_sel_hi:[0, 1, 1]
	v_pk_mul_f32 v[104:105], v[106:107], v[144:145]
	v_pk_mul_f32 v[106:107], v[62:63], v[4:5] op_sel_hi:[0,1]
	v_pk_fma_f32 v[144:145], v[150:151], s[66:67], v[104:105] op_sel_hi:[0, 1, 1]
	v_pk_mul_f32 v[104:105], v[62:63], v[2:3] op_sel_hi:[0,1]
	v_exp_f32_e32 v104, v104
	v_exp_f32_e32 v105, v105
	v_exp_f32_e32 v106, v106
	v_exp_f32_e32 v107, v107
	v_pk_fma_f32 v[102:103], s[96:97], v[142:143], v[102:103]
	v_pk_mul_f32 v[104:105], v[104:105], v[146:147]
	v_pk_fma_f32 v[102:103], s[98:99], v[144:145], v[102:103]
	v_pk_fma_f32 v[146:147], v[150:151], s[68:69], v[104:105] op_sel_hi:[0, 1, 1]
	v_pk_mul_f32 v[104:105], v[106:107], v[148:149]
	v_pk_fma_f32 v[102:103], s[20:21], v[146:147], v[102:103]
	v_pk_fma_f32 v[148:149], v[150:151], s[70:71], v[104:105] op_sel_hi:[0, 1, 1]
	v_pk_fma_f32 v[102:103], s[22:23], v[148:149], v[102:103]
	s_waitcnt lgkmcnt(0)
	s_load_dwordx16 s[56:71], s[54:55], 0x180
	s_load_dwordx8 s[88:95], s[54:55], 0x1c0
	s_load_dwordx4 s[96:99], s[54:55], 0x1e0
	s_load_dwordx4 s[20:23], s[54:55], 0x1f0
	s_nop 0
	v_add_f32_e32 v62, v102, v103
	v_fma_mix_f32 v54, v1, v54, v62 op_sel:[0,1,0] op_sel_hi:[0,1,0]
	v_fma_mixlo_f16 v54, v54, v58, 0 op_sel:[0,1,0] op_sel_hi:[0,1,0]
	ds_write_b16 v68, v54 offset:5136
	v_cvt_f32_f16_e32 v54, v63
	v_pk_mul_f32 v[150:151], v[54:55], v[14:15] op_sel_hi:[0,1]
	v_exp_f32_e32 v150, v150
	v_exp_f32_e32 v151, v151
	v_pk_mul_f32 v[152:153], v[54:55], v[16:17] op_sel_hi:[0,1]
	v_exp_f32_e32 v152, v152
	v_exp_f32_e32 v153, v153
	v_fma_mix_f32 v58, v54, v55, 0 op_sel_hi:[0,1,0]
	v_pk_mul_f32 v[134:135], v[150:151], v[134:135]
	v_pk_fma_f32 v[134:135], v[58:59], s[36:37], v[134:135] op_sel_hi:[0, 1, 1]
	v_pk_fma_f32 v[70:71], s[72:73], v[134:135], 0 op_sel_hi:[1, 1, 0]
	v_pk_mul_f32 v[86:87], v[152:153], v[136:137]
	s_nop 0
	v_pk_fma_f32 v[136:137], v[58:59], s[38:39], v[86:87] op_sel_hi:[0, 1, 1]
	v_pk_mul_f32 v[72:73], v[54:55], v[10:11] op_sel_hi:[0,1]
	v_exp_f32_e32 v72, v72
	v_exp_f32_e32 v73, v73
	v_pk_mul_f32 v[86:87], v[54:55], v[12:13] op_sel_hi:[0,1]
	v_exp_f32_e32 v86, v86
	v_exp_f32_e32 v87, v87
	v_pk_mul_f32 v[72:73], v[72:73], v[138:139]
	v_pk_fma_f32 v[70:71], s[74:75], v[136:137], v[70:71]
	v_pk_fma_f32 v[138:139], v[58:59], s[40:41], v[72:73] op_sel_hi:[0, 1, 1]
	v_pk_mul_f32 v[72:73], v[86:87], v[140:141]
	v_pk_mul_f32 v[74:75], v[54:55], v[8:9] op_sel_hi:[0,1]
	v_pk_fma_f32 v[140:141], v[58:59], s[42:43], v[72:73] op_sel_hi:[0, 1, 1]
	v_pk_mul_f32 v[72:73], v[54:55], v[6:7] op_sel_hi:[0,1]
	v_exp_f32_e32 v72, v72
	v_exp_f32_e32 v73, v73
	v_exp_f32_e32 v74, v74
	v_exp_f32_e32 v75, v75
	v_pk_fma_f32 v[70:71], s[76:77], v[138:139], v[70:71]
	v_pk_mul_f32 v[72:73], v[72:73], v[142:143]
	v_pk_fma_f32 v[70:71], s[78:79], v[140:141], v[70:71]
	v_pk_fma_f32 v[142:143], v[58:59], s[44:45], v[72:73] op_sel_hi:[0, 1, 1]
	v_pk_mul_f32 v[72:73], v[74:75], v[144:145]
	v_pk_mul_f32 v[74:75], v[54:55], v[4:5] op_sel_hi:[0,1]
	v_pk_fma_f32 v[144:145], v[58:59], s[46:47], v[72:73] op_sel_hi:[0, 1, 1]
	v_pk_mul_f32 v[72:73], v[54:55], v[2:3] op_sel_hi:[0,1]
	v_exp_f32_e32 v72, v72
	v_exp_f32_e32 v73, v73
	v_exp_f32_e32 v74, v74
	v_exp_f32_e32 v75, v75
	v_pk_fma_f32 v[70:71], s[80:81], v[142:143], v[70:71]
	v_pk_mul_f32 v[72:73], v[72:73], v[146:147]
	v_pk_fma_f32 v[70:71], s[82:83], v[144:145], v[70:71]
	v_pk_fma_f32 v[146:147], v[58:59], s[48:49], v[72:73] op_sel_hi:[0, 1, 1]
	v_pk_mul_f32 v[72:73], v[74:75], v[148:149]
	v_pk_fma_f32 v[70:71], s[84:85], v[146:147], v[70:71]
	v_pk_fma_f32 v[148:149], v[58:59], s[50:51], v[72:73] op_sel_hi:[0, 1, 1]
	v_pk_fma_f32 v[70:71], s[86:87], v[148:149], v[70:71]
	s_waitcnt lgkmcnt(0)
	s_load_dwordx16 s[36:51], s[54:55], 0x200
	s_load_dwordx16 s[72:87], s[54:55], 0x240
	s_nop 0
	v_add_f32_e32 v54, v70, v71
	v_fma_mix_f32 v54, v1, v55, v54 op_sel_hi:[0,1,0]
	v_fma_mixlo_f16 v54, v54, v59, 0 op_sel_hi:[0,1,0]
	ds_write_b16 v68, v54 offset:6176
	v_cvt_f32_f16_sdwa v54, v63 dst_sel:DWORD dst_unused:UNUSED_PAD src0_sel:WORD_1
	v_pk_mul_f32 v[62:63], v[54:55], v[14:15] op_sel_hi:[0,1]
	v_exp_f32_e32 v62, v62
	v_exp_f32_e32 v63, v63
	v_pk_mul_f32 v[150:151], v[54:55], v[16:17] op_sel_hi:[0,1]
	v_exp_f32_e32 v150, v150
	v_exp_f32_e32 v151, v151
	v_fma_mix_f32 v58, v54, v55, 0 op_sel:[0,1,0] op_sel_hi:[0,1,0]
	v_pk_mul_f32 v[62:63], v[62:63], v[134:135]
	v_pk_fma_f32 v[62:63], v[58:59], s[56:57], v[62:63] op_sel_hi:[0, 1, 1]
	v_pk_fma_f32 v[102:103], s[88:89], v[62:63], 0 op_sel_hi:[1, 1, 0]
	v_pk_mul_f32 v[118:119], v[150:151], v[136:137]
	s_nop 0
	v_pk_fma_f32 v[134:135], v[58:59], s[58:59], v[118:119] op_sel_hi:[0, 1, 1]
	v_pk_mul_f32 v[104:105], v[54:55], v[10:11] op_sel_hi:[0,1]
	v_exp_f32_e32 v104, v104
	v_exp_f32_e32 v105, v105
	v_pk_mul_f32 v[118:119], v[54:55], v[12:13] op_sel_hi:[0,1]
	v_exp_f32_e32 v118, v118
	v_exp_f32_e32 v119, v119
	v_pk_mul_f32 v[104:105], v[104:105], v[138:139]
	v_pk_fma_f32 v[102:103], s[90:91], v[134:135], v[102:103]
	v_pk_fma_f32 v[136:137], v[58:59], s[60:61], v[104:105] op_sel_hi:[0, 1, 1]
	v_pk_mul_f32 v[104:105], v[118:119], v[140:141]
	v_pk_mul_f32 v[106:107], v[54:55], v[8:9] op_sel_hi:[0,1]
	v_pk_fma_f32 v[138:139], v[58:59], s[62:63], v[104:105] op_sel_hi:[0, 1, 1]
	v_pk_mul_f32 v[104:105], v[54:55], v[6:7] op_sel_hi:[0,1]
	v_exp_f32_e32 v104, v104
	v_exp_f32_e32 v105, v105
	v_exp_f32_e32 v106, v106
	v_exp_f32_e32 v107, v107
	v_pk_fma_f32 v[102:103], s[92:93], v[136:137], v[102:103]
	v_pk_mul_f32 v[104:105], v[104:105], v[142:143]
	v_pk_fma_f32 v[102:103], s[94:95], v[138:139], v[102:103]
	v_pk_fma_f32 v[140:141], v[58:59], s[64:65], v[104:105] op_sel_hi:[0, 1, 1]
	v_pk_mul_f32 v[104:105], v[106:107], v[144:145]
	v_pk_mul_f32 v[106:107], v[54:55], v[4:5] op_sel_hi:[0,1]
	v_pk_fma_f32 v[142:143], v[58:59], s[66:67], v[104:105] op_sel_hi:[0, 1, 1]
	v_pk_mul_f32 v[104:105], v[54:55], v[2:3] op_sel_hi:[0,1]
	v_exp_f32_e32 v104, v104
	v_exp_f32_e32 v105, v105
	v_exp_f32_e32 v106, v106
	v_exp_f32_e32 v107, v107
	v_pk_fma_f32 v[102:103], s[96:97], v[140:141], v[102:103]
	v_pk_mul_f32 v[104:105], v[104:105], v[146:147]
	v_pk_fma_f32 v[102:103], s[98:99], v[142:143], v[102:103]
	v_pk_fma_f32 v[144:145], v[58:59], s[68:69], v[104:105] op_sel_hi:[0, 1, 1]
	v_pk_mul_f32 v[104:105], v[106:107], v[148:149]
	v_pk_fma_f32 v[102:103], s[20:21], v[144:145], v[102:103]
	v_pk_fma_f32 v[146:147], v[58:59], s[70:71], v[104:105] op_sel_hi:[0, 1, 1]
	v_pk_fma_f32 v[102:103], s[22:23], v[146:147], v[102:103]
	s_waitcnt lgkmcnt(0)
	s_load_dwordx16 s[56:71], s[54:55], 0x280
	s_load_dwordx8 s[88:95], s[54:55], 0x2c0
	s_load_dwordx4 s[96:99], s[54:55], 0x2e0
	s_load_dwordx4 s[20:23], s[54:55], 0x2f0
	s_nop 0
	v_add_f32_e32 v54, v102, v103
	v_fma_mix_f32 v54, v1, v55, v54 op_sel:[0,1,0] op_sel_hi:[0,1,0]
	v_fma_mixlo_f16 v54, v54, v59, 0 op_sel:[0,1,0] op_sel_hi:[0,1,0]
	ds_write_b16 v68, v54 offset:7216
	v_cvt_f32_f16_e32 v54, v64
	v_pk_mul_f32 v[148:149], v[54:55], v[14:15] op_sel_hi:[0,1]
	v_exp_f32_e32 v148, v148
	v_exp_f32_e32 v149, v149
	v_pk_mul_f32 v[150:151], v[54:55], v[16:17] op_sel_hi:[0,1]
	v_exp_f32_e32 v150, v150
	v_exp_f32_e32 v151, v151
	v_fma_mix_f32 v58, v54, v56, 0 op_sel_hi:[0,1,0]
	v_pk_mul_f32 v[62:63], v[148:149], v[62:63]
	v_pk_fma_f32 v[62:63], v[58:59], s[36:37], v[62:63] op_sel_hi:[0, 1, 1]
	v_pk_fma_f32 v[70:71], s[72:73], v[62:63], 0 op_sel_hi:[1, 1, 0]
	v_pk_mul_f32 v[86:87], v[150:151], v[134:135]
	s_nop 0
	v_pk_fma_f32 v[134:135], v[58:59], s[38:39], v[86:87] op_sel_hi:[0, 1, 1]
	v_pk_mul_f32 v[72:73], v[54:55], v[10:11] op_sel_hi:[0,1]
	v_exp_f32_e32 v72, v72
	v_exp_f32_e32 v73, v73
	v_pk_mul_f32 v[86:87], v[54:55], v[12:13] op_sel_hi:[0,1]
	v_exp_f32_e32 v86, v86
	v_exp_f32_e32 v87, v87
	v_pk_mul_f32 v[72:73], v[72:73], v[136:137]
	v_pk_fma_f32 v[70:71], s[74:75], v[134:135], v[70:71]
	v_pk_fma_f32 v[136:137], v[58:59], s[40:41], v[72:73] op_sel_hi:[0, 1, 1]
	v_pk_mul_f32 v[72:73], v[86:87], v[138:139]
	v_pk_mul_f32 v[74:75], v[54:55], v[8:9] op_sel_hi:[0,1]
	v_pk_fma_f32 v[138:139], v[58:59], s[42:43], v[72:73] op_sel_hi:[0, 1, 1]
	v_pk_mul_f32 v[72:73], v[54:55], v[6:7] op_sel_hi:[0,1]
	v_exp_f32_e32 v72, v72
	v_exp_f32_e32 v73, v73
	v_exp_f32_e32 v74, v74
	v_exp_f32_e32 v75, v75
	v_pk_fma_f32 v[70:71], s[76:77], v[136:137], v[70:71]
	v_pk_mul_f32 v[72:73], v[72:73], v[140:141]
	v_pk_fma_f32 v[70:71], s[78:79], v[138:139], v[70:71]
	v_pk_fma_f32 v[140:141], v[58:59], s[44:45], v[72:73] op_sel_hi:[0, 1, 1]
	v_pk_mul_f32 v[72:73], v[74:75], v[142:143]
	v_pk_fma_f32 v[70:71], s[80:81], v[140:141], v[70:71]
	v_pk_fma_f32 v[142:143], v[58:59], s[46:47], v[72:73] op_sel_hi:[0, 1, 1]
	v_pk_mul_f32 v[72:73], v[54:55], v[2:3] op_sel_hi:[0,1]
	v_exp_f32_e32 v72, v72
	v_exp_f32_e32 v73, v73
	v_pk_mul_f32 v[54:55], v[54:55], v[4:5] op_sel_hi:[0,1]
	v_exp_f32_e32 v54, v54
	v_exp_f32_e32 v55, v55
	v_pk_mul_f32 v[72:73], v[72:73], v[144:145]
	v_pk_fma_f32 v[70:71], s[82:83], v[142:143], v[70:71]
	v_pk_fma_f32 v[144:145], v[58:59], s[48:49], v[72:73] op_sel_hi:[0, 1, 1]
	v_pk_mul_f32 v[54:55], v[54:55], v[146:147]
	v_pk_fma_f32 v[70:71], s[84:85], v[144:145], v[70:71]
	v_pk_fma_f32 v[54:55], v[58:59], s[50:51], v[54:55] op_sel_hi:[0, 1, 1]
	v_pk_fma_f32 v[58:59], s[86:87], v[54:55], v[70:71]
	s_waitcnt lgkmcnt(0)
	s_load_dwordx16 s[36:51], s[54:55], 0x300
	s_load_dwordx16 s[72:87], s[54:55], 0x340
	s_nop 0
	v_add_f32_e32 v58, v58, v59
	v_fma_mix_f32 v58, v1, v56, v58 op_sel_hi:[0,1,0]
	v_fma_mixlo_f16 v58, v58, v60, 0 op_sel_hi:[0,1,0]
	ds_write_b16 v68, v58 offset:8256
	v_cvt_f32_f16_sdwa v58, v64 dst_sel:DWORD dst_unused:UNUSED_PAD src0_sel:WORD_1
	v_pk_mul_f32 v[146:147], v[58:59], v[14:15] op_sel_hi:[0,1]
	v_exp_f32_e32 v146, v146
	v_exp_f32_e32 v147, v147
	v_pk_mul_f32 v[148:149], v[58:59], v[16:17] op_sel_hi:[0,1]
	v_exp_f32_e32 v148, v148
	v_exp_f32_e32 v149, v149
	v_fma_mix_f32 v64, v58, v56, 0 op_sel:[0,1,0] op_sel_hi:[0,1,0]
	v_pk_mul_f32 v[62:63], v[146:147], v[62:63]
	v_pk_fma_f32 v[62:63], v[64:65], s[56:57], v[62:63] op_sel_hi:[0, 1, 1]
	v_pk_fma_f32 v[102:103], s[88:89], v[62:63], 0 op_sel_hi:[1, 1, 0]
	v_pk_mul_f32 v[118:119], v[148:149], v[134:135]
	s_nop 0
	v_pk_fma_f32 v[134:135], v[64:65], s[58:59], v[118:119] op_sel_hi:[0, 1, 1]
	v_pk_mul_f32 v[104:105], v[58:59], v[10:11] op_sel_hi:[0,1]
	v_exp_f32_e32 v104, v104
	v_exp_f32_e32 v105, v105
	v_pk_mul_f32 v[118:119], v[58:59], v[12:13] op_sel_hi:[0,1]
	v_exp_f32_e32 v118, v118
	v_exp_f32_e32 v119, v119
	v_pk_mul_f32 v[104:105], v[104:105], v[136:137]
	v_pk_fma_f32 v[102:103], s[90:91], v[134:135], v[102:103]
	v_pk_fma_f32 v[136:137], v[64:65], s[60:61], v[104:105] op_sel_hi:[0, 1, 1]
	v_pk_mul_f32 v[104:105], v[118:119], v[138:139]
	v_pk_mul_f32 v[106:107], v[58:59], v[8:9] op_sel_hi:[0,1]
	v_pk_fma_f32 v[138:139], v[64:65], s[62:63], v[104:105] op_sel_hi:[0, 1, 1]
	v_pk_mul_f32 v[104:105], v[58:59], v[6:7] op_sel_hi:[0,1]
	v_exp_f32_e32 v104, v104
	v_exp_f32_e32 v105, v105
	v_exp_f32_e32 v106, v106
	v_exp_f32_e32 v107, v107
	v_pk_fma_f32 v[102:103], s[92:93], v[136:137], v[102:103]
	v_pk_mul_f32 v[104:105], v[104:105], v[140:141]
	v_pk_fma_f32 v[102:103], s[94:95], v[138:139], v[102:103]
	v_pk_fma_f32 v[140:141], v[64:65], s[64:65], v[104:105] op_sel_hi:[0, 1, 1]
	v_pk_mul_f32 v[104:105], v[106:107], v[142:143]
	v_pk_fma_f32 v[102:103], s[96:97], v[140:141], v[102:103]
	v_pk_fma_f32 v[142:143], v[64:65], s[66:67], v[104:105] op_sel_hi:[0, 1, 1]
	v_pk_mul_f32 v[104:105], v[58:59], v[2:3] op_sel_hi:[0,1]
	v_exp_f32_e32 v104, v104
	v_exp_f32_e32 v105, v105
	v_pk_mul_f32 v[58:59], v[58:59], v[4:5] op_sel_hi:[0,1]
	v_exp_f32_e32 v58, v58
	v_exp_f32_e32 v59, v59
	v_pk_mul_f32 v[104:105], v[104:105], v[144:145]
	v_pk_fma_f32 v[102:103], s[98:99], v[142:143], v[102:103]
	v_pk_fma_f32 v[144:145], v[64:65], s[68:69], v[104:105] op_sel_hi:[0, 1, 1]
	v_pk_mul_f32 v[54:55], v[58:59], v[54:55]
	v_pk_fma_f32 v[102:103], s[20:21], v[144:145], v[102:103]
	v_pk_fma_f32 v[54:55], v[64:65], s[70:71], v[54:55] op_sel_hi:[0, 1, 1]
	v_pk_fma_f32 v[58:59], s[22:23], v[54:55], v[102:103]
	s_waitcnt lgkmcnt(0)
	s_load_dwordx16 s[56:71], s[54:55], 0x380
	s_load_dwordx8 s[88:95], s[54:55], 0x3c0
	s_load_dwordx4 s[96:99], s[54:55], 0x3e0
	s_load_dwordx4 s[20:23], s[54:55], 0x3f0
	s_nop 0
	v_add_f32_e32 v58, v58, v59
	v_fma_mix_f32 v56, v1, v56, v58 op_sel:[0,1,0] op_sel_hi:[0,1,0]
	v_fma_mixlo_f16 v56, v56, v60, 0 op_sel:[0,1,0] op_sel_hi:[0,1,0]
	ds_write_b16 v68, v56 offset:9296
	v_cvt_f32_f16_e32 v56, v65
	v_pk_mul_f32 v[146:147], v[56:57], v[14:15] op_sel_hi:[0,1]
	v_exp_f32_e32 v146, v146
	v_exp_f32_e32 v147, v147
	v_pk_mul_f32 v[148:149], v[56:57], v[16:17] op_sel_hi:[0,1]
	v_exp_f32_e32 v148, v148
	v_exp_f32_e32 v149, v149
	v_fma_mix_f32 v58, v56, v57, 0 op_sel_hi:[0,1,0]
	v_pk_mul_f32 v[62:63], v[146:147], v[62:63]
	v_pk_fma_f32 v[62:63], v[58:59], s[36:37], v[62:63] op_sel_hi:[0, 1, 1]
	v_pk_fma_f32 v[70:71], s[72:73], v[62:63], 0 op_sel_hi:[1, 1, 0]
	v_pk_mul_f32 v[86:87], v[148:149], v[134:135]
	s_nop 0
	v_pk_fma_f32 v[134:135], v[58:59], s[38:39], v[86:87] op_sel_hi:[0, 1, 1]
	v_pk_mul_f32 v[72:73], v[56:57], v[10:11] op_sel_hi:[0,1]
	v_exp_f32_e32 v72, v72
	v_exp_f32_e32 v73, v73
	v_pk_mul_f32 v[86:87], v[56:57], v[12:13] op_sel_hi:[0,1]
	v_exp_f32_e32 v86, v86
	v_exp_f32_e32 v87, v87
	v_pk_mul_f32 v[72:73], v[72:73], v[136:137]
	v_pk_fma_f32 v[70:71], s[74:75], v[134:135], v[70:71]
	v_pk_fma_f32 v[136:137], v[58:59], s[40:41], v[72:73] op_sel_hi:[0, 1, 1]
	v_pk_mul_f32 v[72:73], v[86:87], v[138:139]
	v_pk_mul_f32 v[74:75], v[56:57], v[8:9] op_sel_hi:[0,1]
	v_pk_fma_f32 v[138:139], v[58:59], s[42:43], v[72:73] op_sel_hi:[0, 1, 1]
	v_pk_mul_f32 v[72:73], v[56:57], v[6:7] op_sel_hi:[0,1]
	v_exp_f32_e32 v72, v72
	v_exp_f32_e32 v73, v73
	v_exp_f32_e32 v74, v74
	v_exp_f32_e32 v75, v75
	v_pk_fma_f32 v[70:71], s[76:77], v[136:137], v[70:71]
	v_pk_mul_f32 v[72:73], v[72:73], v[140:141]
	v_pk_fma_f32 v[70:71], s[78:79], v[138:139], v[70:71]
	v_pk_fma_f32 v[140:141], v[58:59], s[44:45], v[72:73] op_sel_hi:[0, 1, 1]
	v_pk_mul_f32 v[72:73], v[74:75], v[142:143]
	v_pk_mul_f32 v[74:75], v[56:57], v[4:5] op_sel_hi:[0,1]
	v_pk_fma_f32 v[142:143], v[58:59], s[46:47], v[72:73] op_sel_hi:[0, 1, 1]
	v_pk_mul_f32 v[72:73], v[56:57], v[2:3] op_sel_hi:[0,1]
	v_exp_f32_e32 v72, v72
	v_exp_f32_e32 v73, v73
	v_exp_f32_e32 v74, v74
	v_exp_f32_e32 v75, v75
	v_pk_fma_f32 v[70:71], s[80:81], v[140:141], v[70:71]
	v_pk_mul_f32 v[72:73], v[72:73], v[144:145]
	v_pk_fma_f32 v[70:71], s[82:83], v[142:143], v[70:71]
	v_pk_fma_f32 v[144:145], v[58:59], s[48:49], v[72:73] op_sel_hi:[0, 1, 1]
	v_pk_mul_f32 v[54:55], v[74:75], v[54:55]
	v_pk_fma_f32 v[70:71], s[84:85], v[144:145], v[70:71]
	v_pk_fma_f32 v[54:55], v[58:59], s[50:51], v[54:55] op_sel_hi:[0, 1, 1]
	v_pk_fma_f32 v[58:59], s[86:87], v[54:55], v[70:71]
	s_waitcnt lgkmcnt(0)
	s_load_dwordx16 s[36:51], s[54:55], 0x400
	s_load_dwordx16 s[72:87], s[54:55], 0x440
	s_nop 0
	v_add_f32_e32 v56, v58, v59
	v_fma_mix_f32 v56, v1, v57, v56 op_sel_hi:[0,1,0]
	v_fma_mixlo_f16 v56, v56, v61, 0 op_sel_hi:[0,1,0]
	ds_write_b16 v68, v56 offset:10336
	v_cvt_f32_f16_sdwa v56, v65 dst_sel:DWORD dst_unused:UNUSED_PAD src0_sel:WORD_1
	v_pk_mul_f32 v[64:65], v[56:57], v[14:15] op_sel_hi:[0,1]
	v_pk_mul_f32 v[146:147], v[56:57], v[16:17] op_sel_hi:[0,1]
	v_exp_f32_e32 v64, v64
	v_exp_f32_e32 v65, v65
	v_exp_f32_e32 v146, v146
	v_exp_f32_e32 v147, v147
	v_fma_mix_f32 v58, v56, v57, 0 op_sel:[0,1,0] op_sel_hi:[0,1,0]
	v_pk_mul_f32 v[62:63], v[64:65], v[62:63]
	v_pk_mul_f32 v[64:65], v[146:147], v[134:135]
	v_pk_fma_f32 v[134:135], v[58:59], s[58:59], v[64:65] op_sel_hi:[0, 1, 1]
	v_pk_mul_f32 v[64:65], v[56:57], v[10:11] op_sel_hi:[0,1]
	v_pk_fma_f32 v[148:149], v[58:59], s[56:57], v[62:63] op_sel_hi:[0, 1, 1]
	v_exp_f32_e32 v64, v64
	v_exp_f32_e32 v65, v65
	v_pk_mul_f32 v[102:103], v[56:57], v[12:13] op_sel_hi:[0,1]
	v_exp_f32_e32 v102, v102
	v_exp_f32_e32 v103, v103
	v_pk_fma_f32 v[62:63], s[88:89], v[148:149], 0 op_sel_hi:[1, 1, 0]
	v_pk_mul_f32 v[64:65], v[64:65], v[136:137]
	v_pk_fma_f32 v[62:63], s[90:91], v[134:135], v[62:63]
	v_pk_fma_f32 v[136:137], v[58:59], s[60:61], v[64:65] op_sel_hi:[0, 1, 1]
	v_pk_mul_f32 v[64:65], v[102:103], v[138:139]
	v_pk_fma_f32 v[62:63], s[92:93], v[136:137], v[62:63]
	v_pk_fma_f32 v[122:123], v[58:59], s[62:63], v[64:65] op_sel_hi:[0, 1, 1]
	v_pk_mul_f32 v[64:65], v[56:57], v[6:7] op_sel_hi:[0,1]
	v_exp_f32_e32 v64, v64
	v_exp_f32_e32 v65, v65
	v_pk_mul_f32 v[102:103], v[56:57], v[8:9] op_sel_hi:[0,1]
	v_exp_f32_e32 v102, v102
	v_exp_f32_e32 v103, v103
	v_pk_mul_f32 v[64:65], v[64:65], v[140:141]
	v_pk_fma_f32 v[62:63], s[94:95], v[122:123], v[62:63]
	v_pk_fma_f32 v[124:125], v[58:59], s[64:65], v[64:65] op_sel_hi:[0, 1, 1]
	v_pk_mul_f32 v[64:65], v[102:103], v[142:143]
	v_pk_fma_f32 v[62:63], s[96:97], v[124:125], v[62:63]
	v_pk_fma_f32 v[126:127], v[58:59], s[66:67], v[64:65] op_sel_hi:[0, 1, 1]
	v_pk_mul_f32 v[64:65], v[56:57], v[2:3] op_sel_hi:[0,1]
	v_exp_f32_e32 v64, v64
	v_exp_f32_e32 v65, v65
	v_pk_mul_f32 v[102:103], v[56:57], v[4:5] op_sel_hi:[0,1]
	v_exp_f32_e32 v102, v102
	v_exp_f32_e32 v103, v103
	v_pk_mul_f32 v[64:65], v[64:65], v[144:145]
	v_pk_fma_f32 v[62:63], s[98:99], v[126:127], v[62:63]
	v_pk_fma_f32 v[128:129], v[58:59], s[68:69], v[64:65] op_sel_hi:[0, 1, 1]
	v_pk_mul_f32 v[54:55], v[102:103], v[54:55]
	v_pk_fma_f32 v[62:63], s[20:21], v[128:129], v[62:63]
	v_pk_fma_f32 v[130:131], v[58:59], s[70:71], v[54:55] op_sel_hi:[0, 1, 1]
	v_pk_fma_f32 v[54:55], s[22:23], v[130:131], v[62:63]
	s_waitcnt lgkmcnt(0)
	s_load_dwordx16 s[56:71], s[54:55], 0x480
	s_load_dwordx8 s[88:95], s[54:55], 0x4c0
	s_load_dwordx4 s[96:99], s[54:55], 0x4e0
	s_load_dwordx4 s[20:23], s[54:55], 0x4f0
	s_nop 0
	v_add_f32_e32 v54, v54, v55
	v_fma_mix_f32 v54, v1, v57, v54 op_sel:[0,1,0] op_sel_hi:[0,1,0]
	v_fma_mixlo_f16 v54, v54, v61, 0 op_sel:[0,1,0] op_sel_hi:[0,1,0]
	ds_write_b16 v68, v54 offset:11376
	s_waitcnt vmcnt(8)
	v_cvt_f32_f16_e32 v132, v50
	s_waitcnt vmcnt(7)
	v_pk_mul_f32 v[140:141], v[132:133], v[14:15] op_sel_hi:[0,1]
	v_exp_f32_e32 v140, v140
	v_exp_f32_e32 v141, v141
	v_pk_mul_f32 v[142:143], v[132:133], v[16:17] op_sel_hi:[0,1]
	v_exp_f32_e32 v142, v142
	v_exp_f32_e32 v143, v143
	v_fma_mix_f32 v138, v132, v42, 0 op_sel_hi:[0,1,0]
	v_pk_mul_f32 v[140:141], v[140:141], v[148:149]
	v_pk_fma_f32 v[140:141], v[138:139], s[36:37], v[140:141] op_sel_hi:[0, 1, 1]
	v_pk_fma_f32 v[70:71], s[72:73], v[140:141], 0 op_sel_hi:[1, 1, 0]
	v_pk_mul_f32 v[86:87], v[142:143], v[134:135]
	s_nop 0
	v_pk_fma_f32 v[134:135], v[138:139], s[38:39], v[86:87] op_sel_hi:[0, 1, 1]
	v_pk_mul_f32 v[72:73], v[132:133], v[10:11] op_sel_hi:[0,1]
	v_exp_f32_e32 v72, v72
	v_exp_f32_e32 v73, v73
	v_pk_mul_f32 v[86:87], v[132:133], v[12:13] op_sel_hi:[0,1]
	v_exp_f32_e32 v86, v86
	v_exp_f32_e32 v87, v87
	v_pk_mul_f32 v[72:73], v[72:73], v[136:137]
	v_pk_fma_f32 v[70:71], s[74:75], v[134:135], v[70:71]
	v_pk_fma_f32 v[136:137], v[138:139], s[40:41], v[72:73] op_sel_hi:[0, 1, 1]
	v_pk_mul_f32 v[72:73], v[86:87], v[122:123]
	v_pk_mul_f32 v[74:75], v[132:133], v[8:9] op_sel_hi:[0,1]
	v_pk_fma_f32 v[122:123], v[138:139], s[42:43], v[72:73] op_sel_hi:[0, 1, 1]
	v_pk_mul_f32 v[72:73], v[132:133], v[6:7] op_sel_hi:[0,1]
	v_exp_f32_e32 v72, v72
	v_exp_f32_e32 v73, v73
	v_exp_f32_e32 v74, v74
	v_exp_f32_e32 v75, v75
	v_pk_fma_f32 v[70:71], s[76:77], v[136:137], v[70:71]
	v_pk_mul_f32 v[72:73], v[72:73], v[124:125]
	v_pk_fma_f32 v[70:71], s[78:79], v[122:123], v[70:71]
	v_pk_fma_f32 v[124:125], v[138:139], s[44:45], v[72:73] op_sel_hi:[0, 1, 1]
	v_pk_mul_f32 v[72:73], v[74:75], v[126:127]
	v_pk_mul_f32 v[74:75], v[132:133], v[4:5] op_sel_hi:[0,1]
	v_pk_fma_f32 v[126:127], v[138:139], s[46:47], v[72:73] op_sel_hi:[0, 1, 1]
	v_pk_mul_f32 v[72:73], v[132:133], v[2:3] op_sel_hi:[0,1]
	v_exp_f32_e32 v72, v72
	v_exp_f32_e32 v73, v73
	v_exp_f32_e32 v74, v74
	v_exp_f32_e32 v75, v75
	v_pk_fma_f32 v[70:71], s[80:81], v[124:125], v[70:71]
	v_pk_mul_f32 v[72:73], v[72:73], v[128:129]
	v_pk_fma_f32 v[70:71], s[82:83], v[126:127], v[70:71]
	v_pk_fma_f32 v[128:129], v[138:139], s[48:49], v[72:73] op_sel_hi:[0, 1, 1]
	v_pk_mul_f32 v[72:73], v[74:75], v[130:131]
	v_pk_fma_f32 v[70:71], s[84:85], v[128:129], v[70:71]
	v_pk_fma_f32 v[130:131], v[138:139], s[50:51], v[72:73] op_sel_hi:[0, 1, 1]
	v_pk_fma_f32 v[70:71], s[86:87], v[130:131], v[70:71]
	s_waitcnt lgkmcnt(0)
	s_load_dwordx16 s[36:51], s[54:55], 0x500
	s_load_dwordx16 s[72:87], s[54:55], 0x540
	s_nop 0
	v_add_f32_e32 v69, v70, v71
	v_fma_mix_f32 v69, v1, v42, v69 op_sel_hi:[0,1,0]
	s_waitcnt vmcnt(6)
	v_fma_mixlo_f16 v69, v69, v46, 0 op_sel_hi:[0,1,0]
	ds_write_b16 v68, v69 offset:12416
	v_cvt_f32_f16_sdwa v50, v50 dst_sel:DWORD dst_unused:UNUSED_PAD src0_sel:WORD_1
	v_pk_mul_f32 v[138:139], v[50:51], v[14:15] op_sel_hi:[0,1]
	v_exp_f32_e32 v138, v138
	v_exp_f32_e32 v139, v139
	v_pk_mul_f32 v[142:143], v[50:51], v[16:17] op_sel_hi:[0,1]
	v_exp_f32_e32 v142, v142
	v_exp_f32_e32 v143, v143
	v_fma_mix_f32 v132, v50, v42, 0 op_sel:[0,1,0] op_sel_hi:[0,1,0]
	v_pk_mul_f32 v[138:139], v[138:139], v[140:141]
	v_pk_fma_f32 v[138:139], v[132:133], s[56:57], v[138:139] op_sel_hi:[0, 1, 1]
	v_pk_fma_f32 v[54:55], s[88:89], v[138:139], 0 op_sel_hi:[1, 1, 0]
	v_pk_mul_f32 v[106:107], v[142:143], v[134:135]
	s_nop 0
	v_pk_fma_f32 v[134:135], v[132:133], s[58:59], v[106:107] op_sel_hi:[0, 1, 1]
	v_pk_mul_f32 v[56:57], v[50:51], v[10:11] op_sel_hi:[0,1]
	v_exp_f32_e32 v56, v56
	v_exp_f32_e32 v57, v57
	v_pk_mul_f32 v[106:107], v[50:51], v[12:13] op_sel_hi:[0,1]
	v_exp_f32_e32 v106, v106
	v_exp_f32_e32 v107, v107
	v_pk_mul_f32 v[56:57], v[56:57], v[136:137]
	v_pk_fma_f32 v[54:55], s[90:91], v[134:135], v[54:55]
	v_pk_fma_f32 v[136:137], v[132:133], s[60:61], v[56:57] op_sel_hi:[0, 1, 1]
	v_pk_mul_f32 v[56:57], v[106:107], v[122:123]
	v_pk_mul_f32 v[58:59], v[50:51], v[8:9] op_sel_hi:[0,1]
	v_pk_fma_f32 v[122:123], v[132:133], s[62:63], v[56:57] op_sel_hi:[0, 1, 1]
	v_pk_mul_f32 v[56:57], v[50:51], v[6:7] op_sel_hi:[0,1]
	v_exp_f32_e32 v56, v56
	v_exp_f32_e32 v57, v57
	v_exp_f32_e32 v58, v58
	v_exp_f32_e32 v59, v59
	v_pk_fma_f32 v[54:55], s[92:93], v[136:137], v[54:55]
	v_pk_mul_f32 v[56:57], v[56:57], v[124:125]
	v_pk_fma_f32 v[54:55], s[94:95], v[122:123], v[54:55]
	v_pk_fma_f32 v[124:125], v[132:133], s[64:65], v[56:57] op_sel_hi:[0, 1, 1]
	v_pk_mul_f32 v[56:57], v[58:59], v[126:127]
	v_pk_mul_f32 v[58:59], v[50:51], v[4:5] op_sel_hi:[0,1]
	v_pk_fma_f32 v[126:127], v[132:133], s[66:67], v[56:57] op_sel_hi:[0, 1, 1]
	v_pk_mul_f32 v[56:57], v[50:51], v[2:3] op_sel_hi:[0,1]
	v_exp_f32_e32 v56, v56
	v_exp_f32_e32 v57, v57
	v_exp_f32_e32 v58, v58
	v_exp_f32_e32 v59, v59
	v_pk_fma_f32 v[54:55], s[96:97], v[124:125], v[54:55]
	v_pk_mul_f32 v[56:57], v[56:57], v[128:129]
	v_pk_fma_f32 v[54:55], s[98:99], v[126:127], v[54:55]
	v_pk_fma_f32 v[128:129], v[132:133], s[68:69], v[56:57] op_sel_hi:[0, 1, 1]
	v_pk_mul_f32 v[56:57], v[58:59], v[130:131]
	v_pk_fma_f32 v[54:55], s[20:21], v[128:129], v[54:55]
	v_pk_fma_f32 v[130:131], v[132:133], s[70:71], v[56:57] op_sel_hi:[0, 1, 1]
	v_pk_fma_f32 v[54:55], s[22:23], v[130:131], v[54:55]
	s_waitcnt lgkmcnt(0)
	s_load_dwordx16 s[56:71], s[54:55], 0x580
	s_load_dwordx8 s[88:95], s[54:55], 0x5c0
	s_load_dwordx4 s[96:99], s[54:55], 0x5e0
	s_load_dwordx4 s[20:23], s[54:55], 0x5f0
	s_nop 0
	v_add_f32_e32 v50, v54, v55
	v_fma_mix_f32 v42, v1, v42, v50 op_sel:[0,1,0] op_sel_hi:[0,1,0]
	v_fma_mixlo_f16 v42, v42, v46, 0 op_sel:[0,1,0] op_sel_hi:[0,1,0]
	ds_write_b16 v68, v42 offset:13456
	v_cvt_f32_f16_e32 v42, v51
	v_pk_mul_f32 v[132:133], v[42:43], v[14:15] op_sel_hi:[0,1]
	v_exp_f32_e32 v132, v132
	v_exp_f32_e32 v133, v133
	v_pk_mul_f32 v[140:141], v[42:43], v[16:17] op_sel_hi:[0,1]
	v_exp_f32_e32 v140, v140
	v_exp_f32_e32 v141, v141
	v_fma_mix_f32 v46, v42, v43, 0 op_sel_hi:[0,1,0]
	v_pk_mul_f32 v[132:133], v[132:133], v[138:139]
	v_pk_fma_f32 v[132:133], v[46:47], s[36:37], v[132:133] op_sel_hi:[0, 1, 1]
	v_pk_fma_f32 v[70:71], s[72:73], v[132:133], 0 op_sel_hi:[1, 1, 0]
	v_pk_mul_f32 v[86:87], v[140:141], v[134:135]
	s_nop 0
	v_pk_fma_f32 v[134:135], v[46:47], s[38:39], v[86:87] op_sel_hi:[0, 1, 1]
	v_pk_mul_f32 v[72:73], v[42:43], v[10:11] op_sel_hi:[0,1]
	v_exp_f32_e32 v72, v72
	v_exp_f32_e32 v73, v73
	v_pk_mul_f32 v[86:87], v[42:43], v[12:13] op_sel_hi:[0,1]
	v_exp_f32_e32 v86, v86
	v_exp_f32_e32 v87, v87
	v_pk_mul_f32 v[72:73], v[72:73], v[136:137]
	v_pk_fma_f32 v[70:71], s[74:75], v[134:135], v[70:71]
	v_pk_fma_f32 v[136:137], v[46:47], s[40:41], v[72:73] op_sel_hi:[0, 1, 1]
	v_pk_mul_f32 v[72:73], v[86:87], v[122:123]
	v_pk_mul_f32 v[74:75], v[42:43], v[8:9] op_sel_hi:[0,1]
	v_pk_fma_f32 v[122:123], v[46:47], s[42:43], v[72:73] op_sel_hi:[0, 1, 1]
	v_pk_mul_f32 v[72:73], v[42:43], v[6:7] op_sel_hi:[0,1]
	v_exp_f32_e32 v72, v72
	v_exp_f32_e32 v73, v73
	v_exp_f32_e32 v74, v74
	v_exp_f32_e32 v75, v75
	v_pk_fma_f32 v[70:71], s[76:77], v[136:137], v[70:71]
	v_pk_mul_f32 v[72:73], v[72:73], v[124:125]
	v_pk_fma_f32 v[70:71], s[78:79], v[122:123], v[70:71]
	v_pk_fma_f32 v[124:125], v[46:47], s[44:45], v[72:73] op_sel_hi:[0, 1, 1]
	v_pk_mul_f32 v[72:73], v[74:75], v[126:127]
	v_pk_mul_f32 v[74:75], v[42:43], v[4:5] op_sel_hi:[0,1]
	v_pk_fma_f32 v[126:127], v[46:47], s[46:47], v[72:73] op_sel_hi:[0, 1, 1]
	v_pk_mul_f32 v[72:73], v[42:43], v[2:3] op_sel_hi:[0,1]
	v_exp_f32_e32 v72, v72
	v_exp_f32_e32 v73, v73
	v_exp_f32_e32 v74, v74
	v_exp_f32_e32 v75, v75
	v_pk_fma_f32 v[70:71], s[80:81], v[124:125], v[70:71]
	v_pk_mul_f32 v[72:73], v[72:73], v[128:129]
	v_pk_fma_f32 v[70:71], s[82:83], v[126:127], v[70:71]
	v_pk_fma_f32 v[128:129], v[46:47], s[48:49], v[72:73] op_sel_hi:[0, 1, 1]
	v_pk_mul_f32 v[72:73], v[74:75], v[130:131]
	v_pk_fma_f32 v[70:71], s[84:85], v[128:129], v[70:71]
	v_pk_fma_f32 v[130:131], v[46:47], s[50:51], v[72:73] op_sel_hi:[0, 1, 1]
	v_pk_fma_f32 v[70:71], s[86:87], v[130:131], v[70:71]
	s_waitcnt lgkmcnt(0)
	s_load_dwordx16 s[36:51], s[54:55], 0x600
	s_load_dwordx16 s[72:87], s[54:55], 0x640
	s_nop 0
	v_add_f32_e32 v42, v70, v71
	v_fma_mix_f32 v42, v1, v43, v42 op_sel_hi:[0,1,0]
	v_fma_mixlo_f16 v42, v42, v47, 0 op_sel_hi:[0,1,0]
	ds_write_b16 v68, v42 offset:14496
	v_cvt_f32_f16_sdwa v42, v51 dst_sel:DWORD dst_unused:UNUSED_PAD src0_sel:WORD_1
	v_pk_mul_f32 v[50:51], v[42:43], v[14:15] op_sel_hi:[0,1]
	v_exp_f32_e32 v50, v50
	v_exp_f32_e32 v51, v51
	v_pk_mul_f32 v[138:139], v[42:43], v[16:17] op_sel_hi:[0,1]
	v_exp_f32_e32 v138, v138
	v_exp_f32_e32 v139, v139
	v_fma_mix_f32 v46, v42, v43, 0 op_sel:[0,1,0] op_sel_hi:[0,1,0]
	v_pk_mul_f32 v[50:51], v[50:51], v[132:133]
	v_pk_fma_f32 v[50:51], v[46:47], s[56:57], v[50:51] op_sel_hi:[0, 1, 1]
	v_pk_fma_f32 v[54:55], s[88:89], v[50:51], 0 op_sel_hi:[1, 1, 0]
	v_pk_mul_f32 v[106:107], v[138:139], v[134:135]
	s_nop 0
	v_pk_fma_f32 v[132:133], v[46:47], s[58:59], v[106:107] op_sel_hi:[0, 1, 1]
	v_pk_mul_f32 v[56:57], v[42:43], v[10:11] op_sel_hi:[0,1]
	v_exp_f32_e32 v56, v56
	v_exp_f32_e32 v57, v57
	v_pk_mul_f32 v[106:107], v[42:43], v[12:13] op_sel_hi:[0,1]
	v_exp_f32_e32 v106, v106
	v_exp_f32_e32 v107, v107
	v_pk_mul_f32 v[56:57], v[56:57], v[136:137]
	v_pk_fma_f32 v[54:55], s[90:91], v[132:133], v[54:55]
	v_pk_fma_f32 v[134:135], v[46:47], s[60:61], v[56:57] op_sel_hi:[0, 1, 1]
	v_pk_mul_f32 v[56:57], v[106:107], v[122:123]
	v_pk_mul_f32 v[58:59], v[42:43], v[8:9] op_sel_hi:[0,1]
	v_pk_fma_f32 v[122:123], v[46:47], s[62:63], v[56:57] op_sel_hi:[0, 1, 1]
	v_pk_mul_f32 v[56:57], v[42:43], v[6:7] op_sel_hi:[0,1]
	v_exp_f32_e32 v56, v56
	v_exp_f32_e32 v57, v57
	v_exp_f32_e32 v58, v58
	v_exp_f32_e32 v59, v59
	v_pk_fma_f32 v[54:55], s[92:93], v[134:135], v[54:55]
	v_pk_mul_f32 v[56:57], v[56:57], v[124:125]
	v_pk_fma_f32 v[54:55], s[94:95], v[122:123], v[54:55]
	v_pk_fma_f32 v[124:125], v[46:47], s[64:65], v[56:57] op_sel_hi:[0, 1, 1]
	v_pk_mul_f32 v[56:57], v[58:59], v[126:127]
	v_pk_mul_f32 v[58:59], v[42:43], v[4:5] op_sel_hi:[0,1]
	v_pk_fma_f32 v[126:127], v[46:47], s[66:67], v[56:57] op_sel_hi:[0, 1, 1]
	v_pk_mul_f32 v[56:57], v[42:43], v[2:3] op_sel_hi:[0,1]
	v_exp_f32_e32 v56, v56
	v_exp_f32_e32 v57, v57
	v_exp_f32_e32 v58, v58
	v_exp_f32_e32 v59, v59
	v_pk_fma_f32 v[54:55], s[96:97], v[124:125], v[54:55]
	v_pk_mul_f32 v[56:57], v[56:57], v[128:129]
	v_pk_fma_f32 v[54:55], s[98:99], v[126:127], v[54:55]
	v_pk_fma_f32 v[128:129], v[46:47], s[68:69], v[56:57] op_sel_hi:[0, 1, 1]
	v_pk_mul_f32 v[56:57], v[58:59], v[130:131]
	v_pk_fma_f32 v[54:55], s[20:21], v[128:129], v[54:55]
	v_pk_fma_f32 v[130:131], v[46:47], s[70:71], v[56:57] op_sel_hi:[0, 1, 1]
	v_pk_fma_f32 v[54:55], s[22:23], v[130:131], v[54:55]
	s_waitcnt lgkmcnt(0)
	s_load_dwordx16 s[56:71], s[54:55], 0x680
	s_load_dwordx8 s[88:95], s[54:55], 0x6c0
	s_load_dwordx4 s[96:99], s[54:55], 0x6e0
	s_load_dwordx4 s[20:23], s[54:55], 0x6f0
	s_nop 0
	v_add_f32_e32 v42, v54, v55
	v_fma_mix_f32 v42, v1, v43, v42 op_sel:[0,1,0] op_sel_hi:[0,1,0]
	v_fma_mixlo_f16 v42, v42, v47, 0 op_sel:[0,1,0] op_sel_hi:[0,1,0]
	ds_write_b16 v68, v42 offset:15536
	v_cvt_f32_f16_e32 v42, v52
	v_pk_mul_f32 v[136:137], v[42:43], v[14:15] op_sel_hi:[0,1]
	v_exp_f32_e32 v136, v136
	v_exp_f32_e32 v137, v137
	v_pk_mul_f32 v[138:139], v[42:43], v[16:17] op_sel_hi:[0,1]
	v_exp_f32_e32 v138, v138
	v_exp_f32_e32 v139, v139
	v_fma_mix_f32 v46, v42, v44, 0 op_sel_hi:[0,1,0]
	v_pk_mul_f32 v[50:51], v[136:137], v[50:51]
	v_pk_fma_f32 v[50:51], v[46:47], s[36:37], v[50:51] op_sel_hi:[0, 1, 1]
	v_pk_fma_f32 v[70:71], s[72:73], v[50:51], 0 op_sel_hi:[1, 1, 0]
	v_pk_mul_f32 v[86:87], v[138:139], v[132:133]
	s_nop 0
	v_pk_fma_f32 v[132:133], v[46:47], s[38:39], v[86:87] op_sel_hi:[0, 1, 1]
	v_pk_mul_f32 v[72:73], v[42:43], v[10:11] op_sel_hi:[0,1]
	v_exp_f32_e32 v72, v72
	v_exp_f32_e32 v73, v73
	v_pk_mul_f32 v[86:87], v[42:43], v[12:13] op_sel_hi:[0,1]
	v_exp_f32_e32 v86, v86
	v_exp_f32_e32 v87, v87
	v_pk_mul_f32 v[72:73], v[72:73], v[134:135]
	v_pk_fma_f32 v[70:71], s[74:75], v[132:133], v[70:71]
	v_pk_fma_f32 v[134:135], v[46:47], s[40:41], v[72:73] op_sel_hi:[0, 1, 1]
	v_pk_mul_f32 v[72:73], v[86:87], v[122:123]
	v_pk_mul_f32 v[74:75], v[42:43], v[8:9] op_sel_hi:[0,1]
	v_pk_fma_f32 v[122:123], v[46:47], s[42:43], v[72:73] op_sel_hi:[0, 1, 1]
	v_pk_mul_f32 v[72:73], v[42:43], v[6:7] op_sel_hi:[0,1]
	v_exp_f32_e32 v72, v72
	v_exp_f32_e32 v73, v73
	v_exp_f32_e32 v74, v74
	v_exp_f32_e32 v75, v75
	v_pk_fma_f32 v[70:71], s[76:77], v[134:135], v[70:71]
	v_pk_mul_f32 v[72:73], v[72:73], v[124:125]
	v_pk_fma_f32 v[70:71], s[78:79], v[122:123], v[70:71]
	v_pk_fma_f32 v[124:125], v[46:47], s[44:45], v[72:73] op_sel_hi:[0, 1, 1]
	v_pk_mul_f32 v[72:73], v[74:75], v[126:127]
	v_pk_fma_f32 v[70:71], s[80:81], v[124:125], v[70:71]
	v_pk_fma_f32 v[126:127], v[46:47], s[46:47], v[72:73] op_sel_hi:[0, 1, 1]
	v_pk_mul_f32 v[72:73], v[42:43], v[2:3] op_sel_hi:[0,1]
	v_exp_f32_e32 v72, v72
	v_exp_f32_e32 v73, v73
	v_pk_mul_f32 v[42:43], v[42:43], v[4:5] op_sel_hi:[0,1]
	v_exp_f32_e32 v42, v42
	v_exp_f32_e32 v43, v43
	v_pk_mul_f32 v[72:73], v[72:73], v[128:129]
	v_pk_fma_f32 v[70:71], s[82:83], v[126:127], v[70:71]
	v_pk_fma_f32 v[128:129], v[46:47], s[48:49], v[72:73] op_sel_hi:[0, 1, 1]
	v_pk_mul_f32 v[42:43], v[42:43], v[130:131]
	v_pk_fma_f32 v[70:71], s[84:85], v[128:129], v[70:71]
	v_pk_fma_f32 v[42:43], v[46:47], s[50:51], v[42:43] op_sel_hi:[0, 1, 1]
	v_pk_fma_f32 v[46:47], s[86:87], v[42:43], v[70:71]
	s_waitcnt lgkmcnt(0)
	s_load_dwordx16 s[36:51], s[54:55], 0x700
	s_load_dwordx16 s[72:87], s[54:55], 0x740
	s_nop 0
	v_add_f32_e32 v46, v46, v47
	v_fma_mix_f32 v46, v1, v44, v46 op_sel_hi:[0,1,0]
	v_fma_mixlo_f16 v46, v46, v48, 0 op_sel_hi:[0,1,0]
	ds_write_b16 v68, v46 offset:16576
	v_cvt_f32_f16_sdwa v46, v52 dst_sel:DWORD dst_unused:UNUSED_PAD src0_sel:WORD_1
	v_pk_mul_f32 v[130:131], v[46:47], v[14:15] op_sel_hi:[0,1]
	v_exp_f32_e32 v130, v130
	v_exp_f32_e32 v131, v131
	v_pk_mul_f32 v[136:137], v[46:47], v[16:17] op_sel_hi:[0,1]
	v_exp_f32_e32 v136, v136
	v_exp_f32_e32 v137, v137
	v_fma_mix_f32 v52, v46, v44, 0 op_sel:[0,1,0] op_sel_hi:[0,1,0]
	v_pk_mul_f32 v[50:51], v[130:131], v[50:51]
	v_pk_fma_f32 v[50:51], v[52:53], s[56:57], v[50:51] op_sel_hi:[0, 1, 1]
	v_pk_fma_f32 v[54:55], s[88:89], v[50:51], 0 op_sel_hi:[1, 1, 0]
	v_pk_mul_f32 v[106:107], v[136:137], v[132:133]
	s_nop 0
	v_pk_fma_f32 v[130:131], v[52:53], s[58:59], v[106:107] op_sel_hi:[0, 1, 1]
	v_pk_mul_f32 v[56:57], v[46:47], v[10:11] op_sel_hi:[0,1]
	v_exp_f32_e32 v56, v56
	v_exp_f32_e32 v57, v57
	v_pk_mul_f32 v[106:107], v[46:47], v[12:13] op_sel_hi:[0,1]
	v_exp_f32_e32 v106, v106
	v_exp_f32_e32 v107, v107
	v_pk_mul_f32 v[56:57], v[56:57], v[134:135]
	v_pk_fma_f32 v[54:55], s[90:91], v[130:131], v[54:55]
	v_pk_fma_f32 v[132:133], v[52:53], s[60:61], v[56:57] op_sel_hi:[0, 1, 1]
	v_pk_mul_f32 v[56:57], v[106:107], v[122:123]
	v_pk_mul_f32 v[58:59], v[46:47], v[8:9] op_sel_hi:[0,1]
	v_pk_fma_f32 v[122:123], v[52:53], s[62:63], v[56:57] op_sel_hi:[0, 1, 1]
	v_pk_mul_f32 v[56:57], v[46:47], v[6:7] op_sel_hi:[0,1]
	v_exp_f32_e32 v56, v56
	v_exp_f32_e32 v57, v57
	v_exp_f32_e32 v58, v58
	v_exp_f32_e32 v59, v59
	v_pk_fma_f32 v[54:55], s[92:93], v[132:133], v[54:55]
	v_pk_mul_f32 v[56:57], v[56:57], v[124:125]
	v_pk_fma_f32 v[54:55], s[94:95], v[122:123], v[54:55]
	v_pk_fma_f32 v[124:125], v[52:53], s[64:65], v[56:57] op_sel_hi:[0, 1, 1]
	v_pk_mul_f32 v[56:57], v[58:59], v[126:127]
	v_pk_fma_f32 v[54:55], s[96:97], v[124:125], v[54:55]
	v_pk_fma_f32 v[126:127], v[52:53], s[66:67], v[56:57] op_sel_hi:[0, 1, 1]
	v_pk_mul_f32 v[56:57], v[46:47], v[2:3] op_sel_hi:[0,1]
	v_exp_f32_e32 v56, v56
	v_exp_f32_e32 v57, v57
	v_pk_mul_f32 v[46:47], v[46:47], v[4:5] op_sel_hi:[0,1]
	v_exp_f32_e32 v46, v46
	v_exp_f32_e32 v47, v47
	v_pk_mul_f32 v[56:57], v[56:57], v[128:129]
	v_pk_fma_f32 v[54:55], s[98:99], v[126:127], v[54:55]
	v_pk_fma_f32 v[128:129], v[52:53], s[68:69], v[56:57] op_sel_hi:[0, 1, 1]
	v_pk_mul_f32 v[42:43], v[46:47], v[42:43]
	v_pk_fma_f32 v[54:55], s[20:21], v[128:129], v[54:55]
	v_pk_fma_f32 v[42:43], v[52:53], s[70:71], v[42:43] op_sel_hi:[0, 1, 1]
	v_pk_fma_f32 v[46:47], s[22:23], v[42:43], v[54:55]
	s_waitcnt lgkmcnt(0)
	s_load_dwordx16 s[56:71], s[54:55], 0x780
	s_load_dwordx8 s[88:95], s[54:55], 0x7c0
	s_load_dwordx4 s[96:99], s[54:55], 0x7e0
	s_load_dwordx4 s[20:23], s[54:55], 0x7f0
	s_nop 0
	v_add_f32_e32 v46, v46, v47
	v_fma_mix_f32 v44, v1, v44, v46 op_sel:[0,1,0] op_sel_hi:[0,1,0]
	v_fma_mixlo_f16 v44, v44, v48, 0 op_sel:[0,1,0] op_sel_hi:[0,1,0]
	ds_write_b16 v68, v44 offset:17616
	v_cvt_f32_f16_e32 v44, v53
	v_pk_mul_f32 v[134:135], v[44:45], v[14:15] op_sel_hi:[0,1]
	v_exp_f32_e32 v134, v134
	v_exp_f32_e32 v135, v135
	v_pk_mul_f32 v[136:137], v[44:45], v[16:17] op_sel_hi:[0,1]
	v_exp_f32_e32 v136, v136
	v_exp_f32_e32 v137, v137
	v_fma_mix_f32 v46, v44, v45, 0 op_sel_hi:[0,1,0]
	v_pk_mul_f32 v[50:51], v[134:135], v[50:51]
	v_pk_fma_f32 v[50:51], v[46:47], s[36:37], v[50:51] op_sel_hi:[0, 1, 1]
	v_pk_fma_f32 v[70:71], s[72:73], v[50:51], 0 op_sel_hi:[1, 1, 0]
	v_pk_mul_f32 v[86:87], v[136:137], v[130:131]
	s_nop 0
	v_pk_fma_f32 v[130:131], v[46:47], s[38:39], v[86:87] op_sel_hi:[0, 1, 1]
	v_pk_mul_f32 v[72:73], v[44:45], v[10:11] op_sel_hi:[0,1]
	v_exp_f32_e32 v72, v72
	v_exp_f32_e32 v73, v73
	v_pk_mul_f32 v[86:87], v[44:45], v[12:13] op_sel_hi:[0,1]
	v_exp_f32_e32 v86, v86
	v_exp_f32_e32 v87, v87
	v_pk_mul_f32 v[72:73], v[72:73], v[132:133]
	v_pk_fma_f32 v[70:71], s[74:75], v[130:131], v[70:71]
	v_pk_fma_f32 v[132:133], v[46:47], s[40:41], v[72:73] op_sel_hi:[0, 1, 1]
	v_pk_mul_f32 v[72:73], v[86:87], v[122:123]
	v_pk_mul_f32 v[74:75], v[44:45], v[8:9] op_sel_hi:[0,1]
	v_pk_fma_f32 v[122:123], v[46:47], s[42:43], v[72:73] op_sel_hi:[0, 1, 1]
	v_pk_mul_f32 v[72:73], v[44:45], v[6:7] op_sel_hi:[0,1]
	v_exp_f32_e32 v72, v72
	v_exp_f32_e32 v73, v73
	v_exp_f32_e32 v74, v74
	v_exp_f32_e32 v75, v75
	v_pk_fma_f32 v[70:71], s[76:77], v[132:133], v[70:71]
	v_pk_mul_f32 v[72:73], v[72:73], v[124:125]
	v_pk_fma_f32 v[70:71], s[78:79], v[122:123], v[70:71]
	v_pk_fma_f32 v[124:125], v[46:47], s[44:45], v[72:73] op_sel_hi:[0, 1, 1]
	v_pk_mul_f32 v[72:73], v[74:75], v[126:127]
	v_pk_mul_f32 v[74:75], v[44:45], v[4:5] op_sel_hi:[0,1]
	v_pk_fma_f32 v[126:127], v[46:47], s[46:47], v[72:73] op_sel_hi:[0, 1, 1]
	v_pk_mul_f32 v[72:73], v[44:45], v[2:3] op_sel_hi:[0,1]
	v_exp_f32_e32 v72, v72
	v_exp_f32_e32 v73, v73
	v_exp_f32_e32 v74, v74
	v_exp_f32_e32 v75, v75
	v_pk_fma_f32 v[70:71], s[80:81], v[124:125], v[70:71]
	v_pk_mul_f32 v[72:73], v[72:73], v[128:129]
	v_pk_fma_f32 v[70:71], s[82:83], v[126:127], v[70:71]
	v_pk_fma_f32 v[128:129], v[46:47], s[48:49], v[72:73] op_sel_hi:[0, 1, 1]
	v_pk_mul_f32 v[42:43], v[74:75], v[42:43]
	v_pk_fma_f32 v[70:71], s[84:85], v[128:129], v[70:71]
	v_pk_fma_f32 v[42:43], v[46:47], s[50:51], v[42:43] op_sel_hi:[0, 1, 1]
	v_pk_fma_f32 v[46:47], s[86:87], v[42:43], v[70:71]
	s_waitcnt lgkmcnt(0)
	s_load_dwordx16 s[36:51], s[54:55], 0x800
	s_load_dwordx16 s[72:87], s[54:55], 0x840
	s_nop 0
	v_add_f32_e32 v44, v46, v47
	v_fma_mix_f32 v44, v1, v45, v44 op_sel_hi:[0,1,0]
	v_fma_mixlo_f16 v44, v44, v49, 0 op_sel_hi:[0,1,0]
	ds_write_b16 v68, v44 offset:18656
	v_cvt_f32_f16_sdwa v44, v53 dst_sel:DWORD dst_unused:UNUSED_PAD src0_sel:WORD_1
	v_pk_mul_f32 v[52:53], v[44:45], v[14:15] op_sel_hi:[0,1]
	v_pk_mul_f32 v[134:135], v[44:45], v[16:17] op_sel_hi:[0,1]
	v_exp_f32_e32 v52, v52
	v_exp_f32_e32 v53, v53
	v_exp_f32_e32 v134, v134
	v_exp_f32_e32 v135, v135
	v_fma_mix_f32 v46, v44, v45, 0 op_sel:[0,1,0] op_sel_hi:[0,1,0]
	v_pk_mul_f32 v[50:51], v[52:53], v[50:51]
	v_pk_mul_f32 v[52:53], v[134:135], v[130:131]
	v_pk_fma_f32 v[130:131], v[46:47], s[58:59], v[52:53] op_sel_hi:[0, 1, 1]
	v_pk_mul_f32 v[52:53], v[44:45], v[10:11] op_sel_hi:[0,1]
	v_pk_fma_f32 v[136:137], v[46:47], s[56:57], v[50:51] op_sel_hi:[0, 1, 1]
	v_exp_f32_e32 v52, v52
	v_exp_f32_e32 v53, v53
	v_pk_mul_f32 v[54:55], v[44:45], v[12:13] op_sel_hi:[0,1]
	v_exp_f32_e32 v54, v54
	v_exp_f32_e32 v55, v55
	v_pk_fma_f32 v[50:51], s[88:89], v[136:137], 0 op_sel_hi:[1, 1, 0]
	v_pk_mul_f32 v[52:53], v[52:53], v[132:133]
	v_pk_fma_f32 v[50:51], s[90:91], v[130:131], v[50:51]
	v_pk_fma_f32 v[132:133], v[46:47], s[60:61], v[52:53] op_sel_hi:[0, 1, 1]
	v_pk_mul_f32 v[52:53], v[54:55], v[122:123]
	v_pk_fma_f32 v[50:51], s[92:93], v[132:133], v[50:51]
	v_pk_fma_f32 v[110:111], v[46:47], s[62:63], v[52:53] op_sel_hi:[0, 1, 1]
	v_pk_mul_f32 v[52:53], v[44:45], v[6:7] op_sel_hi:[0,1]
	v_exp_f32_e32 v52, v52
	v_exp_f32_e32 v53, v53
	v_pk_mul_f32 v[54:55], v[44:45], v[8:9] op_sel_hi:[0,1]
	v_exp_f32_e32 v54, v54
	v_exp_f32_e32 v55, v55
	v_pk_mul_f32 v[52:53], v[52:53], v[124:125]
	v_pk_fma_f32 v[50:51], s[94:95], v[110:111], v[50:51]
	v_pk_fma_f32 v[112:113], v[46:47], s[64:65], v[52:53] op_sel_hi:[0, 1, 1]
	v_pk_mul_f32 v[52:53], v[54:55], v[126:127]
	v_pk_fma_f32 v[50:51], s[96:97], v[112:113], v[50:51]
	v_pk_fma_f32 v[114:115], v[46:47], s[66:67], v[52:53] op_sel_hi:[0, 1, 1]
	v_pk_mul_f32 v[52:53], v[44:45], v[2:3] op_sel_hi:[0,1]
	v_exp_f32_e32 v52, v52
	v_exp_f32_e32 v53, v53
	v_pk_mul_f32 v[54:55], v[44:45], v[4:5] op_sel_hi:[0,1]
	v_exp_f32_e32 v54, v54
	v_exp_f32_e32 v55, v55
	v_pk_mul_f32 v[52:53], v[52:53], v[128:129]
	v_pk_fma_f32 v[50:51], s[98:99], v[114:115], v[50:51]
	v_pk_fma_f32 v[116:117], v[46:47], s[68:69], v[52:53] op_sel_hi:[0, 1, 1]
	v_pk_mul_f32 v[42:43], v[54:55], v[42:43]
	v_pk_fma_f32 v[50:51], s[20:21], v[116:117], v[50:51]
	v_pk_fma_f32 v[118:119], v[46:47], s[70:71], v[42:43] op_sel_hi:[0, 1, 1]
	v_pk_fma_f32 v[42:43], s[22:23], v[118:119], v[50:51]
	s_waitcnt lgkmcnt(0)
	s_load_dwordx16 s[56:71], s[54:55], 0x880
	s_load_dwordx8 s[88:95], s[54:55], 0x8c0
	s_load_dwordx4 s[96:99], s[54:55], 0x8e0
	s_load_dwordx4 s[20:23], s[54:55], 0x8f0
	s_nop 0
	v_add_f32_e32 v42, v42, v43
	v_fma_mix_f32 v42, v1, v45, v42 op_sel:[0,1,0] op_sel_hi:[0,1,0]
	v_fma_mixlo_f16 v42, v42, v49, 0 op_sel:[0,1,0] op_sel_hi:[0,1,0]
	ds_write_b16 v68, v42 offset:19696
	s_waitcnt vmcnt(5)
	v_cvt_f32_f16_e32 v120, v38
	s_waitcnt vmcnt(4)
	v_pk_mul_f32 v[124:125], v[120:121], v[14:15] op_sel_hi:[0,1]
	v_exp_f32_e32 v124, v124
	v_exp_f32_e32 v125, v125
	v_pk_mul_f32 v[126:127], v[120:121], v[16:17] op_sel_hi:[0,1]
	v_exp_f32_e32 v126, v126
	v_exp_f32_e32 v127, v127
	v_fma_mix_f32 v122, v120, v30, 0 op_sel_hi:[0,1,0]
	v_pk_mul_f32 v[124:125], v[124:125], v[136:137]
	v_pk_fma_f32 v[124:125], v[122:123], s[36:37], v[124:125] op_sel_hi:[0, 1, 1]
	v_pk_fma_f32 v[70:71], s[72:73], v[124:125], 0 op_sel_hi:[1, 1, 0]
	v_pk_mul_f32 v[86:87], v[126:127], v[130:131]
	s_nop 0
	v_pk_fma_f32 v[126:127], v[122:123], s[38:39], v[86:87] op_sel_hi:[0, 1, 1]
	v_pk_mul_f32 v[72:73], v[120:121], v[10:11] op_sel_hi:[0,1]
	v_exp_f32_e32 v72, v72
	v_exp_f32_e32 v73, v73
	v_pk_mul_f32 v[86:87], v[120:121], v[12:13] op_sel_hi:[0,1]
	v_exp_f32_e32 v86, v86
	v_exp_f32_e32 v87, v87
	v_pk_mul_f32 v[72:73], v[72:73], v[132:133]
	v_pk_fma_f32 v[70:71], s[74:75], v[126:127], v[70:71]
	v_pk_fma_f32 v[128:129], v[122:123], s[40:41], v[72:73] op_sel_hi:[0, 1, 1]
	v_pk_mul_f32 v[72:73], v[86:87], v[110:111]
	v_pk_mul_f32 v[74:75], v[120:121], v[8:9] op_sel_hi:[0,1]
	v_pk_fma_f32 v[110:111], v[122:123], s[42:43], v[72:73] op_sel_hi:[0, 1, 1]
	v_pk_mul_f32 v[72:73], v[120:121], v[6:7] op_sel_hi:[0,1]
	v_exp_f32_e32 v72, v72
	v_exp_f32_e32 v73, v73
	v_exp_f32_e32 v74, v74
	v_exp_f32_e32 v75, v75
	v_pk_fma_f32 v[70:71], s[76:77], v[128:129], v[70:71]
	v_pk_mul_f32 v[72:73], v[72:73], v[112:113]
	v_pk_fma_f32 v[70:71], s[78:79], v[110:111], v[70:71]
	v_pk_fma_f32 v[112:113], v[122:123], s[44:45], v[72:73] op_sel_hi:[0, 1, 1]
	v_pk_mul_f32 v[72:73], v[74:75], v[114:115]
	v_pk_mul_f32 v[74:75], v[120:121], v[4:5] op_sel_hi:[0,1]
	v_pk_fma_f32 v[114:115], v[122:123], s[46:47], v[72:73] op_sel_hi:[0, 1, 1]
	v_pk_mul_f32 v[72:73], v[120:121], v[2:3] op_sel_hi:[0,1]
	v_exp_f32_e32 v72, v72
	v_exp_f32_e32 v73, v73
	v_exp_f32_e32 v74, v74
	v_exp_f32_e32 v75, v75
	v_pk_fma_f32 v[70:71], s[80:81], v[112:113], v[70:71]
	v_pk_mul_f32 v[72:73], v[72:73], v[116:117]
	v_pk_fma_f32 v[70:71], s[82:83], v[114:115], v[70:71]
	v_pk_fma_f32 v[116:117], v[122:123], s[48:49], v[72:73] op_sel_hi:[0, 1, 1]
	v_pk_mul_f32 v[72:73], v[74:75], v[118:119]
	v_pk_fma_f32 v[70:71], s[84:85], v[116:117], v[70:71]
	v_pk_fma_f32 v[118:119], v[122:123], s[50:51], v[72:73] op_sel_hi:[0, 1, 1]
	v_pk_fma_f32 v[70:71], s[86:87], v[118:119], v[70:71]
	s_waitcnt lgkmcnt(0)
	s_load_dwordx16 s[36:51], s[54:55], 0x900
	s_load_dwordx16 s[72:87], s[54:55], 0x940
	s_nop 0
	v_add_f32_e32 v69, v70, v71
	v_fma_mix_f32 v69, v1, v30, v69 op_sel_hi:[0,1,0]
	s_waitcnt vmcnt(3)
	v_fma_mixlo_f16 v69, v69, v34, 0 op_sel_hi:[0,1,0]
	ds_write_b16 v68, v69 offset:20736
	v_cvt_f32_f16_sdwa v38, v38 dst_sel:DWORD dst_unused:UNUSED_PAD src0_sel:WORD_1
	v_pk_mul_f32 v[122:123], v[38:39], v[14:15] op_sel_hi:[0,1]
	v_exp_f32_e32 v122, v122
	v_exp_f32_e32 v123, v123
	v_pk_mul_f32 v[130:131], v[38:39], v[16:17] op_sel_hi:[0,1]
	v_exp_f32_e32 v130, v130
	v_exp_f32_e32 v131, v131
	v_fma_mix_f32 v120, v38, v30, 0 op_sel:[0,1,0] op_sel_hi:[0,1,0]
	v_pk_mul_f32 v[122:123], v[122:123], v[124:125]
	v_pk_fma_f32 v[122:123], v[120:121], s[56:57], v[122:123] op_sel_hi:[0, 1, 1]
	v_pk_fma_f32 v[42:43], s[88:89], v[122:123], 0 op_sel_hi:[1, 1, 0]
	v_pk_mul_f32 v[58:59], v[130:131], v[126:127]
	s_nop 0
	v_pk_fma_f32 v[124:125], v[120:121], s[58:59], v[58:59] op_sel_hi:[0, 1, 1]
	v_pk_mul_f32 v[44:45], v[38:39], v[10:11] op_sel_hi:[0,1]
	v_exp_f32_e32 v44, v44
	v_exp_f32_e32 v45, v45
	v_pk_mul_f32 v[58:59], v[38:39], v[12:13] op_sel_hi:[0,1]
	v_exp_f32_e32 v58, v58
	v_exp_f32_e32 v59, v59
	v_pk_mul_f32 v[44:45], v[44:45], v[128:129]
	v_pk_fma_f32 v[42:43], s[90:91], v[124:125], v[42:43]
	v_pk_fma_f32 v[126:127], v[120:121], s[60:61], v[44:45] op_sel_hi:[0, 1, 1]
	v_pk_mul_f32 v[44:45], v[58:59], v[110:111]
	v_pk_mul_f32 v[46:47], v[38:39], v[8:9] op_sel_hi:[0,1]
	v_pk_fma_f32 v[110:111], v[120:121], s[62:63], v[44:45] op_sel_hi:[0, 1, 1]
	v_pk_mul_f32 v[44:45], v[38:39], v[6:7] op_sel_hi:[0,1]
	v_exp_f32_e32 v44, v44
	v_exp_f32_e32 v45, v45
	v_exp_f32_e32 v46, v46
	v_exp_f32_e32 v47, v47
	v_pk_fma_f32 v[42:43], s[92:93], v[126:127], v[42:43]
	v_pk_mul_f32 v[44:45], v[44:45], v[112:113]
	v_pk_fma_f32 v[42:43], s[94:95], v[110:111], v[42:43]
	v_pk_fma_f32 v[112:113], v[120:121], s[64:65], v[44:45] op_sel_hi:[0, 1, 1]
	v_pk_mul_f32 v[44:45], v[46:47], v[114:115]
	v_pk_mul_f32 v[46:47], v[38:39], v[4:5] op_sel_hi:[0,1]
	v_pk_fma_f32 v[114:115], v[120:121], s[66:67], v[44:45] op_sel_hi:[0, 1, 1]
	v_pk_mul_f32 v[44:45], v[38:39], v[2:3] op_sel_hi:[0,1]
	v_exp_f32_e32 v44, v44
	v_exp_f32_e32 v45, v45
	v_exp_f32_e32 v46, v46
	v_exp_f32_e32 v47, v47
	v_pk_fma_f32 v[42:43], s[96:97], v[112:113], v[42:43]
	v_pk_mul_f32 v[44:45], v[44:45], v[116:117]
	v_pk_fma_f32 v[42:43], s[98:99], v[114:115], v[42:43]
	v_pk_fma_f32 v[116:117], v[120:121], s[68:69], v[44:45] op_sel_hi:[0, 1, 1]
	v_pk_mul_f32 v[44:45], v[46:47], v[118:119]
	v_pk_fma_f32 v[42:43], s[20:21], v[116:117], v[42:43]
	v_pk_fma_f32 v[118:119], v[120:121], s[70:71], v[44:45] op_sel_hi:[0, 1, 1]
	v_pk_fma_f32 v[42:43], s[22:23], v[118:119], v[42:43]
	s_waitcnt lgkmcnt(0)
	s_load_dwordx16 s[56:71], s[54:55], 0x980
	s_load_dwordx8 s[88:95], s[54:55], 0x9c0
	s_load_dwordx4 s[96:99], s[54:55], 0x9e0
	s_load_dwordx4 s[20:23], s[54:55], 0x9f0
	s_nop 0
	v_add_f32_e32 v38, v42, v43
	v_fma_mix_f32 v30, v1, v30, v38 op_sel:[0,1,0] op_sel_hi:[0,1,0]
	v_fma_mixlo_f16 v30, v30, v34, 0 op_sel:[0,1,0] op_sel_hi:[0,1,0]
	ds_write_b16 v68, v30 offset:21776
	v_cvt_f32_f16_e32 v30, v39
	v_pk_mul_f32 v[120:121], v[30:31], v[14:15] op_sel_hi:[0,1]
	v_exp_f32_e32 v120, v120
	v_exp_f32_e32 v121, v121
	v_pk_mul_f32 v[128:129], v[30:31], v[16:17] op_sel_hi:[0,1]
	v_exp_f32_e32 v128, v128
	v_exp_f32_e32 v129, v129
	v_fma_mix_f32 v34, v30, v31, 0 op_sel_hi:[0,1,0]
	v_pk_mul_f32 v[120:121], v[120:121], v[122:123]
	v_pk_fma_f32 v[120:121], v[34:35], s[36:37], v[120:121] op_sel_hi:[0, 1, 1]
	v_pk_fma_f32 v[70:71], s[72:73], v[120:121], 0 op_sel_hi:[1, 1, 0]
	v_pk_mul_f32 v[86:87], v[128:129], v[124:125]
	s_nop 0
	v_pk_fma_f32 v[122:123], v[34:35], s[38:39], v[86:87] op_sel_hi:[0, 1, 1]
	v_pk_mul_f32 v[72:73], v[30:31], v[10:11] op_sel_hi:[0,1]
	v_exp_f32_e32 v72, v72
	v_exp_f32_e32 v73, v73
	v_pk_mul_f32 v[86:87], v[30:31], v[12:13] op_sel_hi:[0,1]
	v_exp_f32_e32 v86, v86
	v_exp_f32_e32 v87, v87
	v_pk_mul_f32 v[72:73], v[72:73], v[126:127]
	v_pk_fma_f32 v[70:71], s[74:75], v[122:123], v[70:71]
	v_pk_fma_f32 v[124:125], v[34:35], s[40:41], v[72:73] op_sel_hi:[0, 1, 1]
	v_pk_mul_f32 v[72:73], v[86:87], v[110:111]
	v_pk_mul_f32 v[74:75], v[30:31], v[8:9] op_sel_hi:[0,1]
	v_pk_fma_f32 v[110:111], v[34:35], s[42:43], v[72:73] op_sel_hi:[0, 1, 1]
	v_pk_mul_f32 v[72:73], v[30:31], v[6:7] op_sel_hi:[0,1]
	v_exp_f32_e32 v72, v72
	v_exp_f32_e32 v73, v73
	v_exp_f32_e32 v74, v74
	v_exp_f32_e32 v75, v75
	v_pk_fma_f32 v[70:71], s[76:77], v[124:125], v[70:71]
	v_pk_mul_f32 v[72:73], v[72:73], v[112:113]
	v_pk_fma_f32 v[70:71], s[78:79], v[110:111], v[70:71]
	v_pk_fma_f32 v[112:113], v[34:35], s[44:45], v[72:73] op_sel_hi:[0, 1, 1]
	v_pk_mul_f32 v[72:73], v[74:75], v[114:115]
	v_pk_mul_f32 v[74:75], v[30:31], v[4:5] op_sel_hi:[0,1]
	v_pk_fma_f32 v[114:115], v[34:35], s[46:47], v[72:73] op_sel_hi:[0, 1, 1]
	v_pk_mul_f32 v[72:73], v[30:31], v[2:3] op_sel_hi:[0,1]
	v_exp_f32_e32 v72, v72
	v_exp_f32_e32 v73, v73
	v_exp_f32_e32 v74, v74
	v_exp_f32_e32 v75, v75
	v_pk_fma_f32 v[70:71], s[80:81], v[112:113], v[70:71]
	v_pk_mul_f32 v[72:73], v[72:73], v[116:117]
	v_pk_fma_f32 v[70:71], s[82:83], v[114:115], v[70:71]
	v_pk_fma_f32 v[116:117], v[34:35], s[48:49], v[72:73] op_sel_hi:[0, 1, 1]
	v_pk_mul_f32 v[72:73], v[74:75], v[118:119]
	v_pk_fma_f32 v[70:71], s[84:85], v[116:117], v[70:71]
	v_pk_fma_f32 v[118:119], v[34:35], s[50:51], v[72:73] op_sel_hi:[0, 1, 1]
	v_pk_fma_f32 v[70:71], s[86:87], v[118:119], v[70:71]
	s_waitcnt lgkmcnt(0)
	s_load_dwordx16 s[36:51], s[54:55], 0xa00
	s_load_dwordx16 s[72:87], s[54:55], 0xa40
	s_nop 0
	v_add_f32_e32 v30, v70, v71
	v_fma_mix_f32 v30, v1, v31, v30 op_sel_hi:[0,1,0]
	v_fma_mixlo_f16 v30, v30, v35, 0 op_sel_hi:[0,1,0]
	ds_write_b16 v68, v30 offset:22816
	v_cvt_f32_f16_sdwa v30, v39 dst_sel:DWORD dst_unused:UNUSED_PAD src0_sel:WORD_1
	v_pk_mul_f32 v[38:39], v[30:31], v[14:15] op_sel_hi:[0,1]
	v_exp_f32_e32 v38, v38
	v_exp_f32_e32 v39, v39
	v_pk_mul_f32 v[126:127], v[30:31], v[16:17] op_sel_hi:[0,1]
	v_exp_f32_e32 v126, v126
	v_exp_f32_e32 v127, v127
	v_fma_mix_f32 v34, v30, v31, 0 op_sel:[0,1,0] op_sel_hi:[0,1,0]
	v_pk_mul_f32 v[38:39], v[38:39], v[120:121]
	v_pk_fma_f32 v[38:39], v[34:35], s[56:57], v[38:39] op_sel_hi:[0, 1, 1]
	v_pk_fma_f32 v[42:43], s[88:89], v[38:39], 0 op_sel_hi:[1, 1, 0]
	v_pk_mul_f32 v[58:59], v[126:127], v[122:123]
	s_nop 0
	v_pk_fma_f32 v[120:121], v[34:35], s[58:59], v[58:59] op_sel_hi:[0, 1, 1]
	v_pk_mul_f32 v[44:45], v[30:31], v[10:11] op_sel_hi:[0,1]
	v_exp_f32_e32 v44, v44
	v_exp_f32_e32 v45, v45
	v_pk_mul_f32 v[58:59], v[30:31], v[12:13] op_sel_hi:[0,1]
	v_exp_f32_e32 v58, v58
	v_exp_f32_e32 v59, v59
	v_pk_mul_f32 v[44:45], v[44:45], v[124:125]
	v_pk_fma_f32 v[42:43], s[90:91], v[120:121], v[42:43]
	v_pk_fma_f32 v[122:123], v[34:35], s[60:61], v[44:45] op_sel_hi:[0, 1, 1]
	v_pk_mul_f32 v[44:45], v[58:59], v[110:111]
	v_pk_mul_f32 v[46:47], v[30:31], v[8:9] op_sel_hi:[0,1]
	v_pk_fma_f32 v[110:111], v[34:35], s[62:63], v[44:45] op_sel_hi:[0, 1, 1]
	v_pk_mul_f32 v[44:45], v[30:31], v[6:7] op_sel_hi:[0,1]
	v_exp_f32_e32 v44, v44
	v_exp_f32_e32 v45, v45
	v_exp_f32_e32 v46, v46
	v_exp_f32_e32 v47, v47
	v_pk_fma_f32 v[42:43], s[92:93], v[122:123], v[42:43]
	v_pk_mul_f32 v[44:45], v[44:45], v[112:113]
	v_pk_fma_f32 v[42:43], s[94:95], v[110:111], v[42:43]
	v_pk_fma_f32 v[112:113], v[34:35], s[64:65], v[44:45] op_sel_hi:[0, 1, 1]
	v_pk_mul_f32 v[44:45], v[46:47], v[114:115]
	v_pk_mul_f32 v[46:47], v[30:31], v[4:5] op_sel_hi:[0,1]
	v_pk_fma_f32 v[114:115], v[34:35], s[66:67], v[44:45] op_sel_hi:[0, 1, 1]
	v_pk_mul_f32 v[44:45], v[30:31], v[2:3] op_sel_hi:[0,1]
	v_exp_f32_e32 v44, v44
	v_exp_f32_e32 v45, v45
	v_exp_f32_e32 v46, v46
	v_exp_f32_e32 v47, v47
	v_pk_fma_f32 v[42:43], s[96:97], v[112:113], v[42:43]
	v_pk_mul_f32 v[44:45], v[44:45], v[116:117]
	v_pk_fma_f32 v[42:43], s[98:99], v[114:115], v[42:43]
	v_pk_fma_f32 v[116:117], v[34:35], s[68:69], v[44:45] op_sel_hi:[0, 1, 1]
	v_pk_mul_f32 v[44:45], v[46:47], v[118:119]
	v_pk_fma_f32 v[42:43], s[20:21], v[116:117], v[42:43]
	v_pk_fma_f32 v[118:119], v[34:35], s[70:71], v[44:45] op_sel_hi:[0, 1, 1]
	v_pk_fma_f32 v[42:43], s[22:23], v[118:119], v[42:43]
	s_waitcnt lgkmcnt(0)
	s_load_dwordx16 s[56:71], s[54:55], 0xa80
	s_load_dwordx8 s[88:95], s[54:55], 0xac0
	s_load_dwordx4 s[96:99], s[54:55], 0xae0
	s_load_dwordx4 s[20:23], s[54:55], 0xaf0
	s_nop 0
	v_add_f32_e32 v30, v42, v43
	v_fma_mix_f32 v30, v1, v31, v30 op_sel:[0,1,0] op_sel_hi:[0,1,0]
	v_fma_mixlo_f16 v30, v30, v35, 0 op_sel:[0,1,0] op_sel_hi:[0,1,0]
	ds_write_b16 v68, v30 offset:23856
	v_cvt_f32_f16_e32 v30, v40
	v_pk_mul_f32 v[124:125], v[30:31], v[14:15] op_sel_hi:[0,1]
	v_exp_f32_e32 v124, v124
	v_exp_f32_e32 v125, v125
	v_pk_mul_f32 v[126:127], v[30:31], v[16:17] op_sel_hi:[0,1]
	v_exp_f32_e32 v126, v126
	v_exp_f32_e32 v127, v127
	v_fma_mix_f32 v34, v30, v32, 0 op_sel_hi:[0,1,0]
	v_pk_mul_f32 v[38:39], v[124:125], v[38:39]
	v_pk_fma_f32 v[38:39], v[34:35], s[36:37], v[38:39] op_sel_hi:[0, 1, 1]
	v_pk_fma_f32 v[70:71], s[72:73], v[38:39], 0 op_sel_hi:[1, 1, 0]
	v_pk_mul_f32 v[86:87], v[126:127], v[120:121]
	s_nop 0
	v_pk_fma_f32 v[120:121], v[34:35], s[38:39], v[86:87] op_sel_hi:[0, 1, 1]
	v_pk_mul_f32 v[72:73], v[30:31], v[10:11] op_sel_hi:[0,1]
	v_exp_f32_e32 v72, v72
	v_exp_f32_e32 v73, v73
	v_pk_mul_f32 v[86:87], v[30:31], v[12:13] op_sel_hi:[0,1]
	v_exp_f32_e32 v86, v86
	v_exp_f32_e32 v87, v87
	v_pk_mul_f32 v[72:73], v[72:73], v[122:123]
	v_pk_fma_f32 v[70:71], s[74:75], v[120:121], v[70:71]
	v_pk_fma_f32 v[122:123], v[34:35], s[40:41], v[72:73] op_sel_hi:[0, 1, 1]
	v_pk_mul_f32 v[72:73], v[86:87], v[110:111]
	v_pk_mul_f32 v[74:75], v[30:31], v[8:9] op_sel_hi:[0,1]
	v_pk_fma_f32 v[110:111], v[34:35], s[42:43], v[72:73] op_sel_hi:[0, 1, 1]
	v_pk_mul_f32 v[72:73], v[30:31], v[6:7] op_sel_hi:[0,1]
	v_exp_f32_e32 v72, v72
	v_exp_f32_e32 v73, v73
	v_exp_f32_e32 v74, v74
	v_exp_f32_e32 v75, v75
	v_pk_fma_f32 v[70:71], s[76:77], v[122:123], v[70:71]
	v_pk_mul_f32 v[72:73], v[72:73], v[112:113]
	v_pk_fma_f32 v[70:71], s[78:79], v[110:111], v[70:71]
	v_pk_fma_f32 v[112:113], v[34:35], s[44:45], v[72:73] op_sel_hi:[0, 1, 1]
	v_pk_mul_f32 v[72:73], v[74:75], v[114:115]
	v_pk_fma_f32 v[70:71], s[80:81], v[112:113], v[70:71]
	v_pk_fma_f32 v[114:115], v[34:35], s[46:47], v[72:73] op_sel_hi:[0, 1, 1]
	v_pk_mul_f32 v[72:73], v[30:31], v[2:3] op_sel_hi:[0,1]
	v_exp_f32_e32 v72, v72
	v_exp_f32_e32 v73, v73
	v_pk_mul_f32 v[30:31], v[30:31], v[4:5] op_sel_hi:[0,1]
	v_exp_f32_e32 v30, v30
	v_exp_f32_e32 v31, v31
	v_pk_mul_f32 v[72:73], v[72:73], v[116:117]
	v_pk_fma_f32 v[70:71], s[82:83], v[114:115], v[70:71]
	v_pk_fma_f32 v[116:117], v[34:35], s[48:49], v[72:73] op_sel_hi:[0, 1, 1]
	v_pk_mul_f32 v[30:31], v[30:31], v[118:119]
	v_pk_fma_f32 v[70:71], s[84:85], v[116:117], v[70:71]
	v_pk_fma_f32 v[30:31], v[34:35], s[50:51], v[30:31] op_sel_hi:[0, 1, 1]
	v_pk_fma_f32 v[34:35], s[86:87], v[30:31], v[70:71]
	s_waitcnt lgkmcnt(0)
	s_load_dwordx16 s[36:51], s[54:55], 0xb00
	s_load_dwordx16 s[72:87], s[54:55], 0xb40
	s_nop 0
	v_add_f32_e32 v34, v34, v35
	v_fma_mix_f32 v34, v1, v32, v34 op_sel_hi:[0,1,0]
	v_fma_mixlo_f16 v34, v34, v36, 0 op_sel_hi:[0,1,0]
	ds_write_b16 v68, v34 offset:24896
	v_cvt_f32_f16_sdwa v34, v40 dst_sel:DWORD dst_unused:UNUSED_PAD src0_sel:WORD_1
	v_pk_mul_f32 v[118:119], v[34:35], v[14:15] op_sel_hi:[0,1]
	v_exp_f32_e32 v118, v118
	v_exp_f32_e32 v119, v119
	v_pk_mul_f32 v[124:125], v[34:35], v[16:17] op_sel_hi:[0,1]
	v_exp_f32_e32 v124, v124
	v_exp_f32_e32 v125, v125
	v_fma_mix_f32 v40, v34, v32, 0 op_sel:[0,1,0] op_sel_hi:[0,1,0]
	v_pk_mul_f32 v[38:39], v[118:119], v[38:39]
	v_pk_fma_f32 v[38:39], v[40:41], s[56:57], v[38:39] op_sel_hi:[0, 1, 1]
	v_pk_fma_f32 v[42:43], s[88:89], v[38:39], 0 op_sel_hi:[1, 1, 0]
	v_pk_mul_f32 v[58:59], v[124:125], v[120:121]
	s_nop 0
	v_pk_fma_f32 v[118:119], v[40:41], s[58:59], v[58:59] op_sel_hi:[0, 1, 1]
	v_pk_mul_f32 v[44:45], v[34:35], v[10:11] op_sel_hi:[0,1]
	v_exp_f32_e32 v44, v44
	v_exp_f32_e32 v45, v45
	v_pk_mul_f32 v[58:59], v[34:35], v[12:13] op_sel_hi:[0,1]
	v_exp_f32_e32 v58, v58
	v_exp_f32_e32 v59, v59
	v_pk_mul_f32 v[44:45], v[44:45], v[122:123]
	v_pk_fma_f32 v[42:43], s[90:91], v[118:119], v[42:43]
	v_pk_fma_f32 v[120:121], v[40:41], s[60:61], v[44:45] op_sel_hi:[0, 1, 1]
	v_pk_mul_f32 v[44:45], v[58:59], v[110:111]
	v_pk_mul_f32 v[46:47], v[34:35], v[8:9] op_sel_hi:[0,1]
	v_pk_fma_f32 v[110:111], v[40:41], s[62:63], v[44:45] op_sel_hi:[0, 1, 1]
	v_pk_mul_f32 v[44:45], v[34:35], v[6:7] op_sel_hi:[0,1]
	v_exp_f32_e32 v44, v44
	v_exp_f32_e32 v45, v45
	v_exp_f32_e32 v46, v46
	v_exp_f32_e32 v47, v47
	v_pk_fma_f32 v[42:43], s[92:93], v[120:121], v[42:43]
	v_pk_mul_f32 v[44:45], v[44:45], v[112:113]
	v_pk_fma_f32 v[42:43], s[94:95], v[110:111], v[42:43]
	v_pk_fma_f32 v[112:113], v[40:41], s[64:65], v[44:45] op_sel_hi:[0, 1, 1]
	v_pk_mul_f32 v[44:45], v[46:47], v[114:115]
	v_pk_fma_f32 v[42:43], s[96:97], v[112:113], v[42:43]
	v_pk_fma_f32 v[114:115], v[40:41], s[66:67], v[44:45] op_sel_hi:[0, 1, 1]
	v_pk_mul_f32 v[44:45], v[34:35], v[2:3] op_sel_hi:[0,1]
	v_exp_f32_e32 v44, v44
	v_exp_f32_e32 v45, v45
	v_pk_mul_f32 v[34:35], v[34:35], v[4:5] op_sel_hi:[0,1]
	v_exp_f32_e32 v34, v34
	v_exp_f32_e32 v35, v35
	v_pk_mul_f32 v[44:45], v[44:45], v[116:117]
	v_pk_fma_f32 v[42:43], s[98:99], v[114:115], v[42:43]
	v_pk_fma_f32 v[116:117], v[40:41], s[68:69], v[44:45] op_sel_hi:[0, 1, 1]
	v_pk_mul_f32 v[30:31], v[34:35], v[30:31]
	v_pk_fma_f32 v[42:43], s[20:21], v[116:117], v[42:43]
	v_pk_fma_f32 v[30:31], v[40:41], s[70:71], v[30:31] op_sel_hi:[0, 1, 1]
	v_pk_fma_f32 v[34:35], s[22:23], v[30:31], v[42:43]
	s_waitcnt lgkmcnt(0)
	s_load_dwordx16 s[56:71], s[54:55], 0xb80
	s_load_dwordx8 s[88:95], s[54:55], 0xbc0
	s_load_dwordx4 s[96:99], s[54:55], 0xbe0
	s_load_dwordx4 s[20:23], s[54:55], 0xbf0
	s_nop 0
	v_add_f32_e32 v34, v34, v35
	v_fma_mix_f32 v32, v1, v32, v34 op_sel:[0,1,0] op_sel_hi:[0,1,0]
	v_fma_mixlo_f16 v32, v32, v36, 0 op_sel:[0,1,0] op_sel_hi:[0,1,0]
	ds_write_b16 v68, v32 offset:25936
	v_cvt_f32_f16_e32 v32, v41
	v_pk_mul_f32 v[122:123], v[32:33], v[14:15] op_sel_hi:[0,1]
	v_exp_f32_e32 v122, v122
	v_exp_f32_e32 v123, v123
	v_pk_mul_f32 v[124:125], v[32:33], v[16:17] op_sel_hi:[0,1]
	v_exp_f32_e32 v124, v124
	v_exp_f32_e32 v125, v125
	v_fma_mix_f32 v34, v32, v33, 0 op_sel_hi:[0,1,0]
	v_pk_mul_f32 v[38:39], v[122:123], v[38:39]
	v_pk_fma_f32 v[38:39], v[34:35], s[36:37], v[38:39] op_sel_hi:[0, 1, 1]
	v_pk_fma_f32 v[70:71], s[72:73], v[38:39], 0 op_sel_hi:[1, 1, 0]
	v_pk_mul_f32 v[86:87], v[124:125], v[118:119]
	s_nop 0
	v_pk_fma_f32 v[118:119], v[34:35], s[38:39], v[86:87] op_sel_hi:[0, 1, 1]
	v_pk_mul_f32 v[72:73], v[32:33], v[10:11] op_sel_hi:[0,1]
	v_exp_f32_e32 v72, v72
	v_exp_f32_e32 v73, v73
	v_pk_mul_f32 v[86:87], v[32:33], v[12:13] op_sel_hi:[0,1]
	v_exp_f32_e32 v86, v86
	v_exp_f32_e32 v87, v87
	v_pk_mul_f32 v[72:73], v[72:73], v[120:121]
	v_pk_fma_f32 v[70:71], s[74:75], v[118:119], v[70:71]
	v_pk_fma_f32 v[120:121], v[34:35], s[40:41], v[72:73] op_sel_hi:[0, 1, 1]
	v_pk_mul_f32 v[72:73], v[86:87], v[110:111]
	v_pk_mul_f32 v[74:75], v[32:33], v[8:9] op_sel_hi:[0,1]
	v_pk_fma_f32 v[110:111], v[34:35], s[42:43], v[72:73] op_sel_hi:[0, 1, 1]
	v_pk_mul_f32 v[72:73], v[32:33], v[6:7] op_sel_hi:[0,1]
	v_exp_f32_e32 v72, v72
	v_exp_f32_e32 v73, v73
	v_exp_f32_e32 v74, v74
	v_exp_f32_e32 v75, v75
	v_pk_fma_f32 v[70:71], s[76:77], v[120:121], v[70:71]
	v_pk_mul_f32 v[72:73], v[72:73], v[112:113]
	v_pk_fma_f32 v[70:71], s[78:79], v[110:111], v[70:71]
	v_pk_fma_f32 v[112:113], v[34:35], s[44:45], v[72:73] op_sel_hi:[0, 1, 1]
	v_pk_mul_f32 v[72:73], v[74:75], v[114:115]
	v_pk_mul_f32 v[74:75], v[32:33], v[4:5] op_sel_hi:[0,1]
	v_pk_fma_f32 v[114:115], v[34:35], s[46:47], v[72:73] op_sel_hi:[0, 1, 1]
	v_pk_mul_f32 v[72:73], v[32:33], v[2:3] op_sel_hi:[0,1]
	v_exp_f32_e32 v72, v72
	v_exp_f32_e32 v73, v73
	v_exp_f32_e32 v74, v74
	v_exp_f32_e32 v75, v75
	v_pk_fma_f32 v[70:71], s[80:81], v[112:113], v[70:71]
	v_pk_mul_f32 v[72:73], v[72:73], v[116:117]
	v_pk_fma_f32 v[70:71], s[82:83], v[114:115], v[70:71]
	v_pk_fma_f32 v[116:117], v[34:35], s[48:49], v[72:73] op_sel_hi:[0, 1, 1]
	v_pk_mul_f32 v[30:31], v[74:75], v[30:31]
	v_pk_fma_f32 v[70:71], s[84:85], v[116:117], v[70:71]
	v_pk_fma_f32 v[30:31], v[34:35], s[50:51], v[30:31] op_sel_hi:[0, 1, 1]
	v_pk_fma_f32 v[34:35], s[86:87], v[30:31], v[70:71]
	s_waitcnt lgkmcnt(0)
	s_load_dwordx16 s[36:51], s[54:55], 0xc00
	s_load_dwordx16 s[72:87], s[54:55], 0xc40
	s_nop 0
	v_add_f32_e32 v32, v34, v35
	v_fma_mix_f32 v32, v1, v33, v32 op_sel_hi:[0,1,0]
	v_fma_mixlo_f16 v32, v32, v37, 0 op_sel_hi:[0,1,0]
	ds_write_b16 v68, v32 offset:26976
	v_cvt_f32_f16_sdwa v32, v41 dst_sel:DWORD dst_unused:UNUSED_PAD src0_sel:WORD_1
	v_pk_mul_f32 v[40:41], v[32:33], v[14:15] op_sel_hi:[0,1]
	v_pk_mul_f32 v[122:123], v[32:33], v[16:17] op_sel_hi:[0,1]
	v_exp_f32_e32 v40, v40
	v_exp_f32_e32 v41, v41
	v_exp_f32_e32 v122, v122
	v_exp_f32_e32 v123, v123
	v_fma_mix_f32 v34, v32, v33, 0 op_sel:[0,1,0] op_sel_hi:[0,1,0]
	v_pk_mul_f32 v[38:39], v[40:41], v[38:39]
	v_pk_mul_f32 v[40:41], v[122:123], v[118:119]
	v_pk_fma_f32 v[118:119], v[34:35], s[58:59], v[40:41] op_sel_hi:[0, 1, 1]
	v_pk_mul_f32 v[40:41], v[32:33], v[10:11] op_sel_hi:[0,1]
	v_pk_fma_f32 v[124:125], v[34:35], s[56:57], v[38:39] op_sel_hi:[0, 1, 1]
	v_exp_f32_e32 v40, v40
	v_exp_f32_e32 v41, v41
	v_pk_mul_f32 v[42:43], v[32:33], v[12:13] op_sel_hi:[0,1]
	v_exp_f32_e32 v42, v42
	v_exp_f32_e32 v43, v43
	v_pk_fma_f32 v[38:39], s[88:89], v[124:125], 0 op_sel_hi:[1, 1, 0]
	v_pk_mul_f32 v[40:41], v[40:41], v[120:121]
	v_pk_fma_f32 v[38:39], s[90:91], v[118:119], v[38:39]
	v_pk_fma_f32 v[120:121], v[34:35], s[60:61], v[40:41] op_sel_hi:[0, 1, 1]
	v_pk_mul_f32 v[40:41], v[42:43], v[110:111]
	v_pk_fma_f32 v[38:39], s[92:93], v[120:121], v[38:39]
	v_pk_fma_f32 v[62:63], v[34:35], s[62:63], v[40:41] op_sel_hi:[0, 1, 1]
	v_pk_mul_f32 v[40:41], v[32:33], v[6:7] op_sel_hi:[0,1]
	v_exp_f32_e32 v40, v40
	v_exp_f32_e32 v41, v41
	v_pk_mul_f32 v[42:43], v[32:33], v[8:9] op_sel_hi:[0,1]
	v_exp_f32_e32 v42, v42
	v_exp_f32_e32 v43, v43
	v_pk_mul_f32 v[40:41], v[40:41], v[112:113]
	v_pk_fma_f32 v[38:39], s[94:95], v[62:63], v[38:39]
	v_pk_fma_f32 v[64:65], v[34:35], s[64:65], v[40:41] op_sel_hi:[0, 1, 1]
	v_pk_mul_f32 v[40:41], v[42:43], v[114:115]
	v_pk_fma_f32 v[38:39], s[96:97], v[64:65], v[38:39]
	v_pk_fma_f32 v[102:103], v[34:35], s[66:67], v[40:41] op_sel_hi:[0, 1, 1]
	v_pk_mul_f32 v[40:41], v[32:33], v[2:3] op_sel_hi:[0,1]
	v_exp_f32_e32 v40, v40
	v_exp_f32_e32 v41, v41
	v_pk_mul_f32 v[42:43], v[32:33], v[4:5] op_sel_hi:[0,1]
	v_exp_f32_e32 v42, v42
	v_exp_f32_e32 v43, v43
	v_pk_mul_f32 v[40:41], v[40:41], v[116:117]
	v_pk_fma_f32 v[38:39], s[98:99], v[102:103], v[38:39]
	v_pk_fma_f32 v[104:105], v[34:35], s[68:69], v[40:41] op_sel_hi:[0, 1, 1]
	v_pk_mul_f32 v[30:31], v[42:43], v[30:31]
	v_pk_fma_f32 v[38:39], s[20:21], v[104:105], v[38:39]
	v_pk_fma_f32 v[106:107], v[34:35], s[70:71], v[30:31] op_sel_hi:[0, 1, 1]
	v_pk_fma_f32 v[30:31], s[22:23], v[106:107], v[38:39]
	s_waitcnt lgkmcnt(0)
	s_load_dwordx16 s[56:71], s[54:55], 0xc80
	s_load_dwordx8 s[88:95], s[54:55], 0xcc0
	s_load_dwordx4 s[96:99], s[54:55], 0xce0
	s_load_dwordx4 s[20:23], s[54:55], 0xcf0
	s_nop 0
	v_add_f32_e32 v30, v30, v31
	v_fma_mix_f32 v30, v1, v33, v30 op_sel:[0,1,0] op_sel_hi:[0,1,0]
	v_fma_mixlo_f16 v30, v30, v37, 0 op_sel:[0,1,0] op_sel_hi:[0,1,0]
	ds_write_b16 v68, v30 offset:28016
	s_waitcnt vmcnt(2)
	v_cvt_f32_f16_e32 v108, v26
	s_waitcnt vmcnt(1)
	v_pk_mul_f32 v[112:113], v[108:109], v[14:15] op_sel_hi:[0,1]
	v_exp_f32_e32 v112, v112
	v_exp_f32_e32 v113, v113
	v_pk_mul_f32 v[114:115], v[108:109], v[16:17] op_sel_hi:[0,1]
	v_exp_f32_e32 v114, v114
	v_exp_f32_e32 v115, v115
	v_fma_mix_f32 v110, v108, v18, 0 op_sel_hi:[0,1,0]
	v_pk_mul_f32 v[112:113], v[112:113], v[124:125]
	v_pk_fma_f32 v[112:113], v[110:111], s[36:37], v[112:113] op_sel_hi:[0, 1, 1]
	v_pk_fma_f32 v[70:71], s[72:73], v[112:113], 0 op_sel_hi:[1, 1, 0]
	v_pk_mul_f32 v[86:87], v[114:115], v[118:119]
	s_nop 0
	v_pk_fma_f32 v[114:115], v[110:111], s[38:39], v[86:87] op_sel_hi:[0, 1, 1]
	v_pk_mul_f32 v[72:73], v[108:109], v[10:11] op_sel_hi:[0,1]
	v_exp_f32_e32 v72, v72
	v_exp_f32_e32 v73, v73
	v_pk_mul_f32 v[86:87], v[108:109], v[12:13] op_sel_hi:[0,1]
	v_exp_f32_e32 v86, v86
	v_exp_f32_e32 v87, v87
	v_pk_mul_f32 v[72:73], v[72:73], v[120:121]
	v_pk_fma_f32 v[70:71], s[74:75], v[114:115], v[70:71]
	v_pk_fma_f32 v[116:117], v[110:111], s[40:41], v[72:73] op_sel_hi:[0, 1, 1]
	v_pk_mul_f32 v[62:63], v[86:87], v[62:63]
	v_pk_fma_f32 v[70:71], s[76:77], v[116:117], v[70:71]
	v_pk_fma_f32 v[118:119], v[110:111], s[42:43], v[62:63] op_sel_hi:[0, 1, 1]
	v_pk_fma_f32 v[62:63], s[78:79], v[118:119], v[70:71]
	v_pk_mul_f32 v[70:71], v[108:109], v[6:7] op_sel_hi:[0,1]
	v_exp_f32_e32 v70, v70
	v_exp_f32_e32 v71, v71
	v_pk_mul_f32 v[72:73], v[108:109], v[8:9] op_sel_hi:[0,1]
	v_exp_f32_e32 v72, v72
	v_exp_f32_e32 v73, v73
	v_pk_mul_f32 v[64:65], v[70:71], v[64:65]
	v_pk_mul_f32 v[70:71], v[108:109], v[4:5] op_sel_hi:[0,1]
	v_pk_fma_f32 v[120:121], v[110:111], s[44:45], v[64:65] op_sel_hi:[0, 1, 1]
	v_pk_mul_f32 v[64:65], v[72:73], v[102:103]
	v_exp_f32_e32 v70, v70
	v_pk_fma_f32 v[102:103], v[110:111], s[46:47], v[64:65] op_sel_hi:[0, 1, 1]
	v_pk_mul_f32 v[64:65], v[108:109], v[2:3] op_sel_hi:[0,1]
	v_exp_f32_e32 v64, v64
	v_exp_f32_e32 v65, v65
	v_exp_f32_e32 v71, v71
	v_pk_fma_f32 v[62:63], s[80:81], v[120:121], v[62:63]
	v_pk_mul_f32 v[64:65], v[64:65], v[104:105]
	v_pk_fma_f32 v[62:63], s[82:83], v[102:103], v[62:63]
	v_pk_fma_f32 v[104:105], v[110:111], s[48:49], v[64:65] op_sel_hi:[0, 1, 1]
	v_pk_mul_f32 v[64:65], v[70:71], v[106:107]
	v_pk_fma_f32 v[62:63], s[84:85], v[104:105], v[62:63]
	v_pk_fma_f32 v[98:99], v[110:111], s[50:51], v[64:65] op_sel_hi:[0, 1, 1]
	v_pk_fma_f32 v[62:63], s[86:87], v[98:99], v[62:63]
	s_nop 0
	v_add_f32_e32 v62, v62, v63
	v_fma_mix_f32 v62, v1, v18, v62 op_sel_hi:[0,1,0]
	s_waitcnt vmcnt(0)
	v_fma_mixlo_f16 v62, v62, v22, 0 op_sel_hi:[0,1,0]
	ds_write_b16 v68, v62 offset:29056
	v_lshrrev_b32_e32 v196, 6, v0
	v_and_b32_e32 v197, 48, v0
	v_lshl_or_b32 v196, v196, 7, v197
	v_and_b32_e32 v197, 15, v0
	v_or_b32_e32 v197, s28, v197
	v_lshl_or_b32 v196, v197, 10, v196
	v_add_u32_e32 v197, 0x4000, v196
	global_load_dwordx4 v[180:183], v196, s[4:5]
	global_load_dwordx4 v[184:187], v196, s[4:5] offset:64
	global_load_dwordx4 v[188:191], v197, s[4:5]
	global_load_dwordx4 v[192:195], v197, s[4:5] offset:64
	v_and_b32_e32 v196, 63, v0
	v_lshlrev_b32_e32 v196, 4, v196
	global_load_dwordx4 v[204:207], v196, s[6:7]
	global_load_dwordx4 v[208:211], v196, s[8:9]
	s_waitcnt lgkmcnt(0)
	s_load_dwordx16 s[36:51], s[54:55], 0xd00
	s_load_dwordx16 s[72:87], s[54:55], 0xd40
	v_cvt_f32_f16_sdwa v26, v26 dst_sel:DWORD dst_unused:UNUSED_PAD src0_sel:WORD_1
	v_pk_mul_f32 v[106:107], v[26:27], v[14:15] op_sel_hi:[0,1]
	v_exp_f32_e32 v106, v106
	v_exp_f32_e32 v107, v107
	v_pk_mul_f32 v[108:109], v[26:27], v[16:17] op_sel_hi:[0,1]
	v_exp_f32_e32 v108, v108
	v_exp_f32_e32 v109, v109
	v_fma_mix_f32 v100, v26, v18, 0 op_sel:[0,1,0] op_sel_hi:[0,1,0]
	v_pk_mul_f32 v[106:107], v[106:107], v[112:113]
	v_pk_fma_f32 v[106:107], v[100:101], s[56:57], v[106:107] op_sel_hi:[0, 1, 1]
	v_pk_fma_f32 v[30:31], s[88:89], v[106:107], 0 op_sel_hi:[1, 1, 0]
	v_pk_mul_f32 v[46:47], v[108:109], v[114:115]
	s_nop 0
	v_pk_fma_f32 v[108:109], v[100:101], s[58:59], v[46:47] op_sel_hi:[0, 1, 1]
	v_pk_mul_f32 v[32:33], v[26:27], v[10:11] op_sel_hi:[0,1]
	v_exp_f32_e32 v32, v32
	v_exp_f32_e32 v33, v33
	v_pk_mul_f32 v[46:47], v[26:27], v[12:13] op_sel_hi:[0,1]
	v_exp_f32_e32 v46, v46
	v_exp_f32_e32 v47, v47
	v_pk_mul_f32 v[32:33], v[32:33], v[116:117]
	v_pk_fma_f32 v[30:31], s[90:91], v[108:109], v[30:31]
	v_pk_fma_f32 v[110:111], v[100:101], s[60:61], v[32:33] op_sel_hi:[0, 1, 1]
	v_pk_mul_f32 v[32:33], v[46:47], v[118:119]
	v_pk_mul_f32 v[34:35], v[26:27], v[8:9] op_sel_hi:[0,1]
	v_pk_fma_f32 v[112:113], v[100:101], s[62:63], v[32:33] op_sel_hi:[0, 1, 1]
	v_pk_mul_f32 v[32:33], v[26:27], v[6:7] op_sel_hi:[0,1]
	v_exp_f32_e32 v32, v32
	v_exp_f32_e32 v33, v33
	v_exp_f32_e32 v34, v34
	v_exp_f32_e32 v35, v35
	v_pk_fma_f32 v[30:31], s[92:93], v[110:111], v[30:31]
	v_pk_mul_f32 v[32:33], v[32:33], v[120:121]
	v_pk_fma_f32 v[30:31], s[94:95], v[112:113], v[30:31]
	v_pk_fma_f32 v[114:115], v[100:101], s[64:65], v[32:33] op_sel_hi:[0, 1, 1]
	v_pk_mul_f32 v[32:33], v[34:35], v[102:103]
	v_pk_mul_f32 v[34:35], v[26:27], v[4:5] op_sel_hi:[0,1]
	v_pk_fma_f32 v[102:103], v[100:101], s[66:67], v[32:33] op_sel_hi:[0, 1, 1]
	v_pk_mul_f32 v[32:33], v[26:27], v[2:3] op_sel_hi:[0,1]
	v_exp_f32_e32 v32, v32
	v_exp_f32_e32 v33, v33
	v_exp_f32_e32 v34, v34
	v_exp_f32_e32 v35, v35
	v_pk_fma_f32 v[30:31], s[96:97], v[114:115], v[30:31]
	v_pk_mul_f32 v[32:33], v[32:33], v[104:105]
	v_pk_fma_f32 v[30:31], s[98:99], v[102:103], v[30:31]
	v_pk_fma_f32 v[104:105], v[100:101], s[68:69], v[32:33] op_sel_hi:[0, 1, 1]
	v_pk_mul_f32 v[32:33], v[34:35], v[98:99]
	v_pk_fma_f32 v[30:31], s[20:21], v[104:105], v[30:31]
	v_pk_fma_f32 v[98:99], v[100:101], s[70:71], v[32:33] op_sel_hi:[0, 1, 1]
	v_pk_fma_f32 v[30:31], s[22:23], v[98:99], v[30:31]
	s_waitcnt lgkmcnt(0)
	s_load_dwordx16 s[56:71], s[54:55], 0xd80
	s_load_dwordx8 s[88:95], s[54:55], 0xdc0
	s_load_dwordx4 s[96:99], s[54:55], 0xde0
	s_load_dwordx4 s[20:23], s[54:55], 0xdf0
	s_nop 0
	v_add_f32_e32 v26, v30, v31
	v_fma_mix_f32 v18, v1, v18, v26 op_sel:[0,1,0] op_sel_hi:[0,1,0]
	v_fma_mixlo_f16 v18, v18, v22, 0 op_sel:[0,1,0] op_sel_hi:[0,1,0]
	ds_write_b16 v68, v18 offset:30096
	v_cvt_f32_f16_e32 v18, v27
	v_pk_mul_f32 v[100:101], v[18:19], v[14:15] op_sel_hi:[0,1]
	v_exp_f32_e32 v100, v100
	v_exp_f32_e32 v101, v101
	v_pk_mul_f32 v[116:117], v[18:19], v[16:17] op_sel_hi:[0,1]
	v_exp_f32_e32 v116, v116
	v_exp_f32_e32 v117, v117
	v_fma_mix_f32 v22, v18, v19, 0 op_sel_hi:[0,1,0]
	v_pk_mul_f32 v[100:101], v[100:101], v[106:107]
	v_pk_fma_f32 v[100:101], v[22:23], s[36:37], v[100:101] op_sel_hi:[0, 1, 1]
	v_pk_fma_f32 v[62:63], s[72:73], v[100:101], 0 op_sel_hi:[1, 1, 0]
	v_pk_mul_f32 v[82:83], v[116:117], v[108:109]
	s_nop 0
	v_pk_fma_f32 v[106:107], v[22:23], s[38:39], v[82:83] op_sel_hi:[0, 1, 1]
	v_pk_mul_f32 v[64:65], v[18:19], v[10:11] op_sel_hi:[0,1]
	v_exp_f32_e32 v64, v64
	v_exp_f32_e32 v65, v65
	v_pk_mul_f32 v[82:83], v[18:19], v[12:13] op_sel_hi:[0,1]
	v_exp_f32_e32 v82, v82
	v_exp_f32_e32 v83, v83
	v_pk_mul_f32 v[64:65], v[64:65], v[110:111]
	v_pk_fma_f32 v[62:63], s[74:75], v[106:107], v[62:63]
	v_pk_fma_f32 v[108:109], v[22:23], s[40:41], v[64:65] op_sel_hi:[0, 1, 1]
	v_pk_mul_f32 v[64:65], v[82:83], v[112:113]
	v_pk_mul_f32 v[70:71], v[18:19], v[8:9] op_sel_hi:[0,1]
	v_pk_fma_f32 v[110:111], v[22:23], s[42:43], v[64:65] op_sel_hi:[0, 1, 1]
	v_pk_mul_f32 v[64:65], v[18:19], v[6:7] op_sel_hi:[0,1]
	v_exp_f32_e32 v64, v64
	v_exp_f32_e32 v65, v65
	v_exp_f32_e32 v70, v70
	v_exp_f32_e32 v71, v71
	v_pk_fma_f32 v[62:63], s[76:77], v[108:109], v[62:63]
	v_pk_mul_f32 v[64:65], v[64:65], v[114:115]
	v_pk_fma_f32 v[62:63], s[78:79], v[110:111], v[62:63]
	v_pk_fma_f32 v[112:113], v[22:23], s[44:45], v[64:65] op_sel_hi:[0, 1, 1]
	v_pk_mul_f32 v[64:65], v[70:71], v[102:103]
	v_pk_mul_f32 v[70:71], v[18:19], v[4:5] op_sel_hi:[0,1]
	v_pk_fma_f32 v[102:103], v[22:23], s[46:47], v[64:65] op_sel_hi:[0, 1, 1]
	v_pk_mul_f32 v[64:65], v[18:19], v[2:3] op_sel_hi:[0,1]
	v_exp_f32_e32 v64, v64
	v_exp_f32_e32 v65, v65
	v_exp_f32_e32 v70, v70
	v_exp_f32_e32 v71, v71
	v_pk_fma_f32 v[62:63], s[80:81], v[112:113], v[62:63]
	v_pk_mul_f32 v[64:65], v[64:65], v[104:105]
	v_pk_fma_f32 v[62:63], s[82:83], v[102:103], v[62:63]
	v_pk_fma_f32 v[104:105], v[22:23], s[48:49], v[64:65] op_sel_hi:[0, 1, 1]
	v_pk_mul_f32 v[64:65], v[70:71], v[98:99]
	v_pk_fma_f32 v[62:63], s[84:85], v[104:105], v[62:63]
	v_pk_fma_f32 v[98:99], v[22:23], s[50:51], v[64:65] op_sel_hi:[0, 1, 1]
	v_pk_fma_f32 v[62:63], s[86:87], v[98:99], v[62:63]
	s_waitcnt lgkmcnt(0)
	s_load_dwordx16 s[36:51], s[54:55], 0xe00
	s_load_dwordx16 s[72:87], s[54:55], 0xe40
	s_nop 0
	v_add_f32_e32 v18, v62, v63
	v_fma_mix_f32 v18, v1, v19, v18 op_sel_hi:[0,1,0]
	v_fma_mixlo_f16 v18, v18, v23, 0 op_sel_hi:[0,1,0]
	ds_write_b16 v68, v18 offset:31136
	v_cvt_f32_f16_sdwa v18, v27 dst_sel:DWORD dst_unused:UNUSED_PAD src0_sel:WORD_1
	v_pk_mul_f32 v[26:27], v[18:19], v[14:15] op_sel_hi:[0,1]
	v_exp_f32_e32 v26, v26
	v_exp_f32_e32 v27, v27
	v_pk_mul_f32 v[114:115], v[18:19], v[16:17] op_sel_hi:[0,1]
	v_exp_f32_e32 v114, v114
	v_exp_f32_e32 v115, v115
	v_fma_mix_f32 v22, v18, v19, 0 op_sel:[0,1,0] op_sel_hi:[0,1,0]
	v_pk_mul_f32 v[26:27], v[26:27], v[100:101]
	v_pk_fma_f32 v[26:27], v[22:23], s[56:57], v[26:27] op_sel_hi:[0, 1, 1]
	v_pk_fma_f32 v[30:31], s[88:89], v[26:27], 0 op_sel_hi:[1, 1, 0]
	v_pk_mul_f32 v[46:47], v[114:115], v[106:107]
	s_nop 0
	v_pk_fma_f32 v[100:101], v[22:23], s[58:59], v[46:47] op_sel_hi:[0, 1, 1]
	v_pk_mul_f32 v[32:33], v[18:19], v[10:11] op_sel_hi:[0,1]
	v_exp_f32_e32 v32, v32
	v_exp_f32_e32 v33, v33
	v_pk_mul_f32 v[46:47], v[18:19], v[12:13] op_sel_hi:[0,1]
	v_exp_f32_e32 v46, v46
	v_exp_f32_e32 v47, v47
	v_pk_mul_f32 v[32:33], v[32:33], v[108:109]
	v_pk_fma_f32 v[30:31], s[90:91], v[100:101], v[30:31]
	v_pk_fma_f32 v[106:107], v[22:23], s[60:61], v[32:33] op_sel_hi:[0, 1, 1]
	v_pk_mul_f32 v[32:33], v[46:47], v[110:111]
	v_pk_mul_f32 v[34:35], v[18:19], v[8:9] op_sel_hi:[0,1]
	v_pk_fma_f32 v[108:109], v[22:23], s[62:63], v[32:33] op_sel_hi:[0, 1, 1]
	v_pk_mul_f32 v[32:33], v[18:19], v[6:7] op_sel_hi:[0,1]
	v_exp_f32_e32 v32, v32
	v_exp_f32_e32 v33, v33
	v_exp_f32_e32 v34, v34
	v_exp_f32_e32 v35, v35
	v_pk_fma_f32 v[30:31], s[92:93], v[106:107], v[30:31]
	v_pk_mul_f32 v[32:33], v[32:33], v[112:113]
	v_pk_fma_f32 v[30:31], s[94:95], v[108:109], v[30:31]
	v_pk_fma_f32 v[110:111], v[22:23], s[64:65], v[32:33] op_sel_hi:[0, 1, 1]
	v_pk_mul_f32 v[32:33], v[34:35], v[102:103]
	v_pk_mul_f32 v[34:35], v[18:19], v[4:5] op_sel_hi:[0,1]
	v_pk_fma_f32 v[102:103], v[22:23], s[66:67], v[32:33] op_sel_hi:[0, 1, 1]
	v_pk_mul_f32 v[32:33], v[18:19], v[2:3] op_sel_hi:[0,1]
	v_exp_f32_e32 v32, v32
	v_exp_f32_e32 v33, v33
	v_exp_f32_e32 v34, v34
	v_exp_f32_e32 v35, v35
	v_pk_fma_f32 v[30:31], s[96:97], v[110:111], v[30:31]
	v_pk_mul_f32 v[32:33], v[32:33], v[104:105]
	v_pk_fma_f32 v[30:31], s[98:99], v[102:103], v[30:31]
	v_pk_fma_f32 v[104:105], v[22:23], s[68:69], v[32:33] op_sel_hi:[0, 1, 1]
	v_pk_mul_f32 v[32:33], v[34:35], v[98:99]
	v_pk_fma_f32 v[30:31], s[20:21], v[104:105], v[30:31]
	v_pk_fma_f32 v[98:99], v[22:23], s[70:71], v[32:33] op_sel_hi:[0, 1, 1]
	v_pk_fma_f32 v[30:31], s[22:23], v[98:99], v[30:31]
	s_waitcnt lgkmcnt(0)
	s_load_dwordx16 s[56:71], s[54:55], 0xe80
	s_load_dwordx8 s[88:95], s[54:55], 0xec0
	s_load_dwordx4 s[96:99], s[54:55], 0xee0
	s_load_dwordx4 s[20:23], s[54:55], 0xef0
	s_nop 0
	v_add_f32_e32 v18, v30, v31
	v_fma_mix_f32 v18, v1, v19, v18 op_sel:[0,1,0] op_sel_hi:[0,1,0]
	v_fma_mixlo_f16 v18, v18, v23, 0 op_sel:[0,1,0] op_sel_hi:[0,1,0]
	ds_write_b16 v68, v18 offset:32176
	v_cvt_f32_f16_e32 v18, v28
	v_pk_mul_f32 v[112:113], v[18:19], v[14:15] op_sel_hi:[0,1]
	v_exp_f32_e32 v112, v112
	v_exp_f32_e32 v113, v113
	v_pk_mul_f32 v[114:115], v[18:19], v[16:17] op_sel_hi:[0,1]
	v_exp_f32_e32 v114, v114
	v_exp_f32_e32 v115, v115
	v_fma_mix_f32 v22, v18, v20, 0 op_sel_hi:[0,1,0]
	v_pk_mul_f32 v[26:27], v[112:113], v[26:27]
	v_pk_fma_f32 v[26:27], v[22:23], s[36:37], v[26:27] op_sel_hi:[0, 1, 1]
	v_pk_fma_f32 v[62:63], s[72:73], v[26:27], 0 op_sel_hi:[1, 1, 0]
	v_pk_mul_f32 v[82:83], v[114:115], v[100:101]
	s_nop 0
	v_pk_fma_f32 v[100:101], v[22:23], s[38:39], v[82:83] op_sel_hi:[0, 1, 1]
	v_pk_mul_f32 v[64:65], v[18:19], v[10:11] op_sel_hi:[0,1]
	v_exp_f32_e32 v64, v64
	v_exp_f32_e32 v65, v65
	v_pk_mul_f32 v[82:83], v[18:19], v[12:13] op_sel_hi:[0,1]
	v_exp_f32_e32 v82, v82
	v_exp_f32_e32 v83, v83
	v_pk_mul_f32 v[64:65], v[64:65], v[106:107]
	v_pk_fma_f32 v[62:63], s[74:75], v[100:101], v[62:63]
	v_pk_fma_f32 v[106:107], v[22:23], s[40:41], v[64:65] op_sel_hi:[0, 1, 1]
	v_pk_mul_f32 v[64:65], v[82:83], v[108:109]
	v_pk_mul_f32 v[70:71], v[18:19], v[8:9] op_sel_hi:[0,1]
	v_pk_fma_f32 v[108:109], v[22:23], s[42:43], v[64:65] op_sel_hi:[0, 1, 1]
	v_pk_mul_f32 v[64:65], v[18:19], v[6:7] op_sel_hi:[0,1]
	v_exp_f32_e32 v64, v64
	v_exp_f32_e32 v65, v65
	v_exp_f32_e32 v70, v70
	v_exp_f32_e32 v71, v71
	v_pk_fma_f32 v[62:63], s[76:77], v[106:107], v[62:63]
	v_pk_mul_f32 v[64:65], v[64:65], v[110:111]
	v_pk_fma_f32 v[62:63], s[78:79], v[108:109], v[62:63]
	v_pk_fma_f32 v[110:111], v[22:23], s[44:45], v[64:65] op_sel_hi:[0, 1, 1]
	v_pk_mul_f32 v[64:65], v[70:71], v[102:103]
	v_pk_fma_f32 v[62:63], s[80:81], v[110:111], v[62:63]
	v_pk_fma_f32 v[102:103], v[22:23], s[46:47], v[64:65] op_sel_hi:[0, 1, 1]
	v_pk_mul_f32 v[64:65], v[18:19], v[2:3] op_sel_hi:[0,1]
	v_exp_f32_e32 v64, v64
	v_exp_f32_e32 v65, v65
	v_pk_mul_f32 v[18:19], v[18:19], v[4:5] op_sel_hi:[0,1]
	v_exp_f32_e32 v18, v18
	v_exp_f32_e32 v19, v19
	v_pk_mul_f32 v[64:65], v[64:65], v[104:105]
	v_pk_fma_f32 v[62:63], s[82:83], v[102:103], v[62:63]
	v_pk_fma_f32 v[104:105], v[22:23], s[48:49], v[64:65] op_sel_hi:[0, 1, 1]
	v_pk_mul_f32 v[18:19], v[18:19], v[98:99]
	v_pk_fma_f32 v[62:63], s[84:85], v[104:105], v[62:63]
	v_pk_fma_f32 v[18:19], v[22:23], s[50:51], v[18:19] op_sel_hi:[0, 1, 1]
	v_pk_fma_f32 v[22:23], s[86:87], v[18:19], v[62:63]
	s_waitcnt lgkmcnt(0)
	s_load_dwordx16 s[36:51], s[54:55], 0xf00
	s_load_dwordx16 s[72:87], s[54:55], 0xf40
	s_nop 0
	v_add_f32_e32 v22, v22, v23
	v_fma_mix_f32 v22, v1, v20, v22 op_sel_hi:[0,1,0]
	v_fma_mixlo_f16 v22, v22, v24, 0 op_sel_hi:[0,1,0]
	ds_write_b16 v68, v22 offset:33216
	v_cvt_f32_f16_sdwa v22, v28 dst_sel:DWORD dst_unused:UNUSED_PAD src0_sel:WORD_1
	v_pk_mul_f32 v[98:99], v[22:23], v[14:15] op_sel_hi:[0,1]
	v_exp_f32_e32 v98, v98
	v_exp_f32_e32 v99, v99
	v_pk_mul_f32 v[112:113], v[22:23], v[16:17] op_sel_hi:[0,1]
	v_exp_f32_e32 v112, v112
	v_exp_f32_e32 v113, v113
	v_fma_mix_f32 v28, v22, v20, 0 op_sel:[0,1,0] op_sel_hi:[0,1,0]
	v_pk_mul_f32 v[26:27], v[98:99], v[26:27]
	v_pk_fma_f32 v[26:27], v[28:29], s[56:57], v[26:27] op_sel_hi:[0, 1, 1]
	v_pk_fma_f32 v[30:31], s[88:89], v[26:27], 0 op_sel_hi:[1, 1, 0]
	v_pk_mul_f32 v[46:47], v[112:113], v[100:101]
	s_nop 0
	v_pk_fma_f32 v[98:99], v[28:29], s[58:59], v[46:47] op_sel_hi:[0, 1, 1]
	v_pk_mul_f32 v[32:33], v[22:23], v[10:11] op_sel_hi:[0,1]
	v_exp_f32_e32 v32, v32
	v_exp_f32_e32 v33, v33
	v_pk_mul_f32 v[46:47], v[22:23], v[12:13] op_sel_hi:[0,1]
	v_exp_f32_e32 v46, v46
	v_exp_f32_e32 v47, v47
	v_pk_mul_f32 v[32:33], v[32:33], v[106:107]
	v_pk_fma_f32 v[30:31], s[90:91], v[98:99], v[30:31]
	v_pk_fma_f32 v[100:101], v[28:29], s[60:61], v[32:33] op_sel_hi:[0, 1, 1]
	v_pk_mul_f32 v[32:33], v[46:47], v[108:109]
	v_pk_mul_f32 v[34:35], v[22:23], v[8:9] op_sel_hi:[0,1]
	v_pk_fma_f32 v[106:107], v[28:29], s[62:63], v[32:33] op_sel_hi:[0, 1, 1]
	v_pk_mul_f32 v[32:33], v[22:23], v[6:7] op_sel_hi:[0,1]
	v_exp_f32_e32 v32, v32
	v_exp_f32_e32 v33, v33
	v_exp_f32_e32 v34, v34
	v_exp_f32_e32 v35, v35
	v_pk_fma_f32 v[30:31], s[92:93], v[100:101], v[30:31]
	v_pk_mul_f32 v[32:33], v[32:33], v[110:111]
	v_pk_fma_f32 v[30:31], s[94:95], v[106:107], v[30:31]
	v_pk_fma_f32 v[108:109], v[28:29], s[64:65], v[32:33] op_sel_hi:[0, 1, 1]
	v_pk_mul_f32 v[32:33], v[34:35], v[102:103]
	v_pk_fma_f32 v[30:31], s[96:97], v[108:109], v[30:31]
	v_pk_fma_f32 v[102:103], v[28:29], s[66:67], v[32:33] op_sel_hi:[0, 1, 1]
	v_pk_mul_f32 v[32:33], v[22:23], v[2:3] op_sel_hi:[0,1]
	v_exp_f32_e32 v32, v32
	v_exp_f32_e32 v33, v33
	v_pk_mul_f32 v[22:23], v[22:23], v[4:5] op_sel_hi:[0,1]
	v_exp_f32_e32 v22, v22
	v_exp_f32_e32 v23, v23
	v_pk_mul_f32 v[32:33], v[32:33], v[104:105]
	v_pk_fma_f32 v[30:31], s[98:99], v[102:103], v[30:31]
	v_pk_fma_f32 v[104:105], v[28:29], s[68:69], v[32:33] op_sel_hi:[0, 1, 1]
	v_pk_mul_f32 v[18:19], v[22:23], v[18:19]
	v_pk_fma_f32 v[30:31], s[20:21], v[104:105], v[30:31]
	v_pk_fma_f32 v[18:19], v[28:29], s[70:71], v[18:19] op_sel_hi:[0, 1, 1]
	v_pk_fma_f32 v[22:23], s[22:23], v[18:19], v[30:31]
	s_waitcnt lgkmcnt(0)
	s_load_dwordx16 s[56:71], s[54:55], 0xf80
	s_load_dwordx8 s[88:95], s[54:55], 0xfc0
	s_load_dwordx4 s[96:99], s[54:55], 0xfe0
	s_load_dwordx4 s[20:23], s[54:55], 0xff0
	s_nop 0
	v_add_f32_e32 v22, v22, v23
	v_fma_mix_f32 v20, v1, v20, v22 op_sel:[0,1,0] op_sel_hi:[0,1,0]
	v_fma_mixlo_f16 v20, v20, v24, 0 op_sel:[0,1,0] op_sel_hi:[0,1,0]
	ds_write_b16 v68, v20 offset:34256
	v_cvt_f32_f16_e32 v20, v29
	v_pk_mul_f32 v[110:111], v[20:21], v[14:15] op_sel_hi:[0,1]
	v_exp_f32_e32 v110, v110
	v_exp_f32_e32 v111, v111
	v_pk_mul_f32 v[112:113], v[20:21], v[16:17] op_sel_hi:[0,1]
	v_exp_f32_e32 v112, v112
	v_exp_f32_e32 v113, v113
	v_fma_mix_f32 v22, v20, v21, 0 op_sel_hi:[0,1,0]
	v_pk_mul_f32 v[26:27], v[110:111], v[26:27]
	v_pk_fma_f32 v[26:27], v[22:23], s[36:37], v[26:27] op_sel_hi:[0, 1, 1]
	v_pk_fma_f32 v[62:63], s[72:73], v[26:27], 0 op_sel_hi:[1, 1, 0]
	v_pk_mul_f32 v[82:83], v[112:113], v[98:99]
	s_nop 0
	v_pk_fma_f32 v[64:65], v[22:23], s[38:39], v[82:83] op_sel_hi:[0, 1, 1]
	v_pk_mul_f32 v[82:83], v[20:21], v[10:11] op_sel_hi:[0,1]
	v_pk_fma_f32 v[62:63], s[74:75], v[64:65], v[62:63]
	v_exp_f32_e32 v82, v82
	v_exp_f32_e32 v83, v83
	v_pk_mul_f32 v[84:85], v[20:21], v[12:13] op_sel_hi:[0,1]
	v_exp_f32_e32 v84, v84
	v_exp_f32_e32 v85, v85
	v_pk_mul_f32 v[82:83], v[82:83], v[100:101]
	s_nop 0
	v_pk_fma_f32 v[70:71], v[22:23], s[40:41], v[82:83] op_sel_hi:[0, 1, 1]
	v_pk_mul_f32 v[82:83], v[84:85], v[106:107]
	v_pk_mul_f32 v[84:85], v[20:21], v[8:9] op_sel_hi:[0,1]
	v_pk_fma_f32 v[72:73], v[22:23], s[42:43], v[82:83] op_sel_hi:[0, 1, 1]
	v_pk_mul_f32 v[82:83], v[20:21], v[6:7] op_sel_hi:[0,1]
	v_exp_f32_e32 v82, v82
	v_exp_f32_e32 v83, v83
	v_exp_f32_e32 v84, v84
	v_exp_f32_e32 v85, v85
	v_pk_fma_f32 v[62:63], s[76:77], v[70:71], v[62:63]
	v_pk_mul_f32 v[82:83], v[82:83], v[108:109]
	v_pk_fma_f32 v[62:63], s[78:79], v[72:73], v[62:63]
	v_pk_fma_f32 v[74:75], v[22:23], s[44:45], v[82:83] op_sel_hi:[0, 1, 1]
	v_pk_mul_f32 v[82:83], v[84:85], v[102:103]
	v_pk_mul_f32 v[84:85], v[20:21], v[4:5] op_sel_hi:[0,1]
	v_pk_fma_f32 v[76:77], v[22:23], s[46:47], v[82:83] op_sel_hi:[0, 1, 1]
	v_pk_mul_f32 v[82:83], v[20:21], v[2:3] op_sel_hi:[0,1]
	v_exp_f32_e32 v82, v82
	v_exp_f32_e32 v83, v83
	v_exp_f32_e32 v84, v84
	v_exp_f32_e32 v85, v85
	v_pk_fma_f32 v[62:63], s[80:81], v[74:75], v[62:63]
	v_pk_mul_f32 v[82:83], v[82:83], v[104:105]
	v_pk_fma_f32 v[62:63], s[82:83], v[76:77], v[62:63]
	v_pk_fma_f32 v[78:79], v[22:23], s[48:49], v[82:83] op_sel_hi:[0, 1, 1]
	v_pk_mul_f32 v[18:19], v[84:85], v[18:19]
	v_pk_fma_f32 v[62:63], s[84:85], v[78:79], v[62:63]
	v_pk_fma_f32 v[18:19], v[22:23], s[50:51], v[18:19] op_sel_hi:[0, 1, 1]
	v_pk_fma_f32 v[22:23], s[86:87], v[18:19], v[62:63]
	s_waitcnt lgkmcnt(0)
	s_nop 0
	v_add_f32_e32 v20, v22, v23
	v_fma_mix_f32 v20, v1, v21, v20 op_sel_hi:[0,1,0]
	v_fma_mixlo_f16 v20, v20, v25, 0 op_sel_hi:[0,1,0]
	ds_write_b16 v68, v20 offset:35296
	v_cvt_f32_f16_sdwa v20, v29 dst_sel:DWORD dst_unused:UNUSED_PAD src0_sel:WORD_1
	v_pk_mul_f32 v[14:15], v[20:21], v[14:15] op_sel_hi:[0,1]
	v_exp_f32_e32 v14, v14
	v_exp_f32_e32 v15, v15
	v_pk_mul_f32 v[16:17], v[20:21], v[16:17] op_sel_hi:[0,1]
	v_exp_f32_e32 v16, v16
	v_exp_f32_e32 v17, v17
	v_pk_mul_f32 v[10:11], v[20:21], v[10:11] op_sel_hi:[0,1]
	v_exp_f32_e32 v10, v10
	v_exp_f32_e32 v11, v11
	v_pk_mul_f32 v[12:13], v[20:21], v[12:13] op_sel_hi:[0,1]
	v_exp_f32_e32 v12, v12
	v_exp_f32_e32 v13, v13
	v_pk_mul_f32 v[6:7], v[20:21], v[6:7] op_sel_hi:[0,1]
	v_fma_mix_f32 v22, v20, v21, 0 op_sel:[0,1,0] op_sel_hi:[0,1,0]
	v_pk_mul_f32 v[14:15], v[14:15], v[26:27]
	v_exp_f32_e32 v6, v6
	v_exp_f32_e32 v7, v7
	v_pk_mul_f32 v[8:9], v[20:21], v[8:9] op_sel_hi:[0,1]
	v_pk_fma_f32 v[14:15], v[22:23], s[56:57], v[14:15] op_sel_hi:[0, 1, 1]
	v_pk_mul_f32 v[16:17], v[16:17], v[64:65]
	v_exp_f32_e32 v8, v8
	v_exp_f32_e32 v9, v9
	v_pk_mul_f32 v[2:3], v[20:21], v[2:3] op_sel_hi:[0,1]
	v_pk_fma_f32 v[14:15], s[88:89], v[14:15], 0 op_sel_hi:[1, 1, 0]
	v_pk_fma_f32 v[16:17], v[22:23], s[58:59], v[16:17] op_sel_hi:[0, 1, 1]
	v_pk_mul_f32 v[10:11], v[10:11], v[70:71]
	v_exp_f32_e32 v2, v2
	v_exp_f32_e32 v3, v3
	v_pk_mul_f32 v[4:5], v[20:21], v[4:5] op_sel_hi:[0,1]
	v_pk_fma_f32 v[14:15], s[90:91], v[16:17], v[14:15]
	v_pk_fma_f32 v[10:11], v[22:23], s[60:61], v[10:11] op_sel_hi:[0, 1, 1]
	v_pk_mul_f32 v[12:13], v[12:13], v[72:73]
	v_exp_f32_e32 v4, v4
	v_exp_f32_e32 v5, v5
	v_pk_fma_f32 v[10:11], s[92:93], v[10:11], v[14:15]
	v_pk_fma_f32 v[12:13], v[22:23], s[62:63], v[12:13] op_sel_hi:[0, 1, 1]
	v_pk_mul_f32 v[6:7], v[6:7], v[74:75]
	v_pk_fma_f32 v[10:11], s[94:95], v[12:13], v[10:11]
	v_pk_fma_f32 v[6:7], v[22:23], s[64:65], v[6:7] op_sel_hi:[0, 1, 1]
	v_pk_mul_f32 v[8:9], v[8:9], v[76:77]
	v_pk_fma_f32 v[6:7], s[96:97], v[6:7], v[10:11]
	v_pk_fma_f32 v[8:9], v[22:23], s[66:67], v[8:9] op_sel_hi:[0, 1, 1]
	v_pk_mul_f32 v[2:3], v[2:3], v[78:79]
	v_pk_fma_f32 v[6:7], s[98:99], v[8:9], v[6:7]
	v_pk_fma_f32 v[2:3], v[22:23], s[68:69], v[2:3] op_sel_hi:[0, 1, 1]
	v_pk_mul_f32 v[4:5], v[4:5], v[18:19]
	v_pk_fma_f32 v[2:3], s[20:21], v[2:3], v[6:7]
	v_pk_fma_f32 v[4:5], v[22:23], s[70:71], v[4:5] op_sel_hi:[0, 1, 1]
	v_pk_fma_f32 v[2:3], s[22:23], v[4:5], v[2:3]
	s_nop 0
	v_add_f32_e32 v2, v2, v3
	v_fma_mix_f32 v1, v1, v21, v2 op_sel:[0,1,0] op_sel_hi:[0,1,0]
	v_fma_mixlo_f16 v1, v1, v25, 0 op_sel:[0,1,0] op_sel_hi:[0,1,0]
	ds_write_b16 v68, v1 offset:36336
	v_lshlrev_b32_e32 v1, 9, v0
	v_and_b32_e32 v2, 0x38000, v1
	v_mov_b32_e32 v3, v67
	v_and_b32_e32 v1, 63, v0
	s_bfe_u32 s14, s2, 0x40003
	v_lshl_add_u64 v[2:3], s[18:19], 0, v[2:3]
	v_lshlrev_b32_e32 v58, 4, v1
	v_mov_b32_e32 v59, v67
	s_lshl_b32 s13, s14, 6
	v_lshl_add_u64 v[20:21], v[2:3], 0, v[58:59]
	s_lshl_b32 s26, s14, 10
	s_add_i32 s12, s13, 64
	v_lshl_add_u64 v[2:3], v[20:21], 0, s[26:27]
	s_and_b32 s15, s12, 0x3c0
	v_add_co_u32_e32 v4, vcc, s52, v2
	s_lshl_b32 s26, s15, 4
	s_lshl_b32 s12, s12, 4
	v_addc_co_u32_e32 v5, vcc, 0, v3, vcc
	global_load_dwordx4 v[28:31], v[2:3], off
	global_load_dwordx4 v[32:35], v[4:5], off
	v_lshl_add_u64 v[2:3], v[20:21], 0, s[26:27]
	s_or_b32 s26, s12, 0x4000
	s_add_i32 s12, s13, 0x80
	s_and_b32 s15, s12, 0x3c0
	v_lshl_add_u64 v[4:5], v[20:21], 0, s[26:27]
	s_lshl_b32 s26, s15, 4
	s_lshl_b32 s12, s12, 4
	global_load_dwordx4 v[36:39], v[2:3], off
	global_load_dwordx4 v[40:43], v[4:5], off
	v_lshl_add_u64 v[2:3], v[20:21], 0, s[26:27]
	s_or_b32 s26, s12, 0x4000
	s_add_i32 s12, s13, 0xc0
	s_and_b32 s15, s12, 0x3c0
	v_lshl_add_u64 v[4:5], v[20:21], 0, s[26:27]
	s_lshl_b32 s26, s15, 4
	s_lshl_b32 s12, s12, 4
	global_load_dwordx4 v[44:47], v[2:3], off
	global_load_dwordx4 v[48:51], v[4:5], off
	v_lshl_add_u64 v[2:3], v[20:21], 0, s[26:27]
	s_or_b32 s26, s12, 0x4000
	s_add_i32 s12, s13, 0x100
	s_and_b32 s15, s12, 0x3c0
	v_lshl_add_u64 v[4:5], v[20:21], 0, s[26:27]
	s_lshl_b32 s26, s15, 4
	s_lshl_b32 s12, s12, 4
	global_load_dwordx4 v[52:55], v[2:3], off
	global_load_dwordx4 v[60:63], v[4:5], off
	v_lshl_add_u64 v[2:3], v[20:21], 0, s[26:27]
	s_or_b32 s26, s12, 0x4000
	s_add_i32 s12, s13, 0x140
	s_and_b32 s15, s12, 0x3c0
	v_lshl_add_u64 v[4:5], v[20:21], 0, s[26:27]
	s_lshl_b32 s26, s15, 4
	s_lshl_b32 s12, s12, 4
	global_load_dwordx4 v[68:71], v[2:3], off
	global_load_dwordx4 v[72:75], v[4:5], off
	v_lshl_add_u64 v[2:3], v[20:21], 0, s[26:27]
	s_or_b32 s26, s12, 0x4000
	s_add_i32 s12, s13, 0x180
	s_and_b32 s15, s12, 0x3c0
	v_lshl_add_u64 v[4:5], v[20:21], 0, s[26:27]
	s_lshl_b32 s26, s15, 4
	s_lshl_b32 s12, s12, 4
	global_load_dwordx4 v[76:79], v[2:3], off
	global_load_dwordx4 v[82:85], v[4:5], off
	v_lshl_add_u64 v[2:3], v[20:21], 0, s[26:27]
	s_or_b32 s26, s12, 0x4000
	s_add_i32 s12, s13, 0x1c0
	s_and_b32 s15, s12, 0x3c0
	v_lshl_add_u64 v[4:5], v[20:21], 0, s[26:27]
	s_lshl_b32 s26, s15, 4
	s_lshl_b32 s12, s12, 4
	v_lshl_add_u64 v[18:19], v[20:21], 0, s[26:27]
	s_or_b32 s26, s12, 0x4000
	s_xor_b32 s15, s13, 0x200
	v_lshl_add_u64 v[22:23], v[20:21], 0, s[26:27]
	s_lshl_b32 s26, s15, 4
	global_load_dwordx4 v[14:17], v[2:3], off
	global_load_dwordx4 v[10:13], v[4:5], off
	global_load_dwordx4 v[6:9], v[18:19], off
	s_nop 0
	global_load_dwordx4 v[2:5], v[22:23], off
	v_lshl_add_u64 v[18:19], v[20:21], 0, s[26:27]
	v_add_co_u32_e32 v22, vcc, s52, v18
	s_waitcnt lgkmcnt(0)
	s_barrier
	v_addc_co_u32_e32 v23, vcc, 0, v19, vcc
	global_load_dwordx4 v[86:89], v[18:19], off
	global_load_dwordx4 v[90:93], v[22:23], off
	v_lshrrev_b32_e32 v118, 6, v0
	v_lshlrev_b32_e32 v22, 7, v118
	v_mov_b32_e32 v23, v67
	v_and_b32_e32 v81, 15, v0
	v_lshl_add_u64 v[24:25], s[4:5], 0, v[22:23]
	v_and_b32_e32 v18, 48, v0
	v_mov_b32_e32 v19, v67
	s_movk_i32 s12, 0x410
	v_lshl_add_u64 v[56:57], v[24:25], 0, v[18:19]
	v_mad_u32_u24 v19, v81, s12, v18
	v_add_u32_e32 v23, s13, v19
	ds_read_b128 v[94:97], v23 offset:4096
	ds_read_b128 v[98:101], v23 offset:20736
	v_or_b32_e32 v26, s28, v81
	v_mov_b32_e32 v27, v67
	v_lshlrev_b64 v[24:25], 10, v[26:27]
	v_or_b32_e32 v26, 16, v26
	v_lshlrev_b64 v[26:27], 10, v[26:27]
	v_lshrrev_b32_e32 v23, 1, v0
	v_lshl_add_u64 v[24:25], v[56:57], 0, v[24:25]
	v_lshl_add_u64 v[26:27], v[56:57], 0, v[26:27]
	v_and_b32_e32 v80, 24, v23
	s_lshl_b32 s14, s14, 5
	s_setprio 1
	s_waitcnt vmcnt(17) lgkmcnt(1)
	v_mfma_f32_16x16x32_f16 v[102:105], v[28:31], v[94:97], 0
	s_waitcnt lgkmcnt(0)
	v_mfma_f32_16x16x32_f16 v[28:31], v[28:31], v[98:101], 0
	s_waitcnt vmcnt(16)
	v_mfma_f32_16x16x32_f16 v[94:97], v[32:35], v[94:97], 0
	v_mfma_f32_16x16x32_f16 v[32:35], v[32:35], v[98:101], 0
	s_setprio 0
	s_add_i32 s16, s13, 0x240
	s_and_b32 s17, s16, 0x3c0
	s_lshl_b32 s26, s17, 4
	s_lshl_b32 s16, s16, 4
	v_lshl_add_u64 v[56:57], v[20:21], 0, s[26:27]
	s_or_b32 s26, s16, 0x4000
	v_lshl_add_u64 v[64:65], v[20:21], 0, s[26:27]
	global_load_dwordx4 v[98:101], v[56:57], off
	global_load_dwordx4 v[106:109], v[64:65], off
	s_add_i32 s16, s14, 32
	s_and_b32 s16, s16, 0x1e0
	v_lshl_add_u32 v23, s16, 1, v19
	ds_read_b128 v[110:113], v23 offset:4096
	ds_read_b128 v[114:117], v23 offset:20736
	s_setprio 1
	s_waitcnt vmcnt(17) lgkmcnt(1)
	v_mfma_f32_16x16x32_f16 v[102:105], v[36:39], v[110:113], v[102:105]
	s_waitcnt lgkmcnt(0)
	v_mfma_f32_16x16x32_f16 v[28:31], v[36:39], v[114:117], v[28:31]
	s_waitcnt vmcnt(16)
	v_mfma_f32_16x16x32_f16 v[36:39], v[40:43], v[110:113], v[94:97]
	v_mfma_f32_16x16x32_f16 v[32:35], v[40:43], v[114:117], v[32:35]
	s_setprio 0
	s_add_i32 s16, s13, 0x280
	s_and_b32 s17, s16, 0x3c0
	s_lshl_b32 s26, s17, 4
	s_lshl_b32 s16, s16, 4
	v_lshl_add_u64 v[56:57], v[20:21], 0, s[26:27]
	s_or_b32 s26, s16, 0x4000
	v_lshl_add_u64 v[64:65], v[20:21], 0, s[26:27]
	global_load_dwordx4 v[40:43], v[56:57], off
	global_load_dwordx4 v[94:97], v[64:65], off
	s_add_i32 s16, s14, 64
	s_and_b32 s16, s16, 0x1e0
	v_lshl_add_u32 v23, s16, 1, v19
	ds_read_b128 v[110:113], v23 offset:4096
	ds_read_b128 v[114:117], v23 offset:20736
	s_setprio 1
	s_waitcnt vmcnt(17) lgkmcnt(1)
	v_mfma_f32_16x16x32_f16 v[102:105], v[44:47], v[110:113], v[102:105]
	s_waitcnt lgkmcnt(0)
	v_mfma_f32_16x16x32_f16 v[28:31], v[44:47], v[114:117], v[28:31]
	s_waitcnt vmcnt(16)
	v_mfma_f32_16x16x32_f16 v[36:39], v[48:51], v[110:113], v[36:39]
	v_mfma_f32_16x16x32_f16 v[32:35], v[48:51], v[114:117], v[32:35]
	s_setprio 0
	s_add_i32 s16, s13, 0x2c0
	s_and_b32 s17, s16, 0x3c0
	s_lshl_b32 s26, s17, 4
	s_lshl_b32 s16, s16, 4
	v_lshl_add_u64 v[56:57], v[20:21], 0, s[26:27]
	s_or_b32 s26, s16, 0x4000
	v_lshl_add_u64 v[64:65], v[20:21], 0, s[26:27]
	global_load_dwordx4 v[44:47], v[56:57], off
	global_load_dwordx4 v[48:51], v[64:65], off
	s_add_i32 s16, s14, 0x60
	s_and_b32 s16, s16, 0x1e0
	v_lshl_add_u32 v23, s16, 1, v19
	ds_read_b128 v[110:113], v23 offset:4096
	ds_read_b128 v[114:117], v23 offset:20736
	s_setprio 1
	s_waitcnt vmcnt(17) lgkmcnt(1)
	v_mfma_f32_16x16x32_f16 v[102:105], v[52:55], v[110:113], v[102:105]
	s_waitcnt lgkmcnt(0)
	v_mfma_f32_16x16x32_f16 v[28:31], v[52:55], v[114:117], v[28:31]
	s_waitcnt vmcnt(16)
	v_mfma_f32_16x16x32_f16 v[36:39], v[60:63], v[110:113], v[36:39]
	v_mfma_f32_16x16x32_f16 v[32:35], v[60:63], v[114:117], v[32:35]
	s_setprio 0
	s_add_i32 s16, s13, 0x300
	s_and_b32 s17, s16, 0x3c0
	s_lshl_b32 s26, s17, 4
	s_lshl_b32 s16, s16, 4
	v_lshl_add_u64 v[56:57], v[20:21], 0, s[26:27]
	s_or_b32 s26, s16, 0x4000
	v_lshl_add_u64 v[64:65], v[20:21], 0, s[26:27]
	global_load_dwordx4 v[52:55], v[56:57], off
	global_load_dwordx4 v[60:63], v[64:65], off
	s_add_i32 s16, s14, 0x80
	s_and_b32 s16, s16, 0x1e0
	v_lshl_add_u32 v23, s16, 1, v19
	ds_read_b128 v[110:113], v23 offset:4096
	ds_read_b128 v[114:117], v23 offset:20736
	s_setprio 1
	s_waitcnt vmcnt(17) lgkmcnt(1)
	v_mfma_f32_16x16x32_f16 v[102:105], v[68:71], v[110:113], v[102:105]
	s_waitcnt lgkmcnt(0)
	v_mfma_f32_16x16x32_f16 v[28:31], v[68:71], v[114:117], v[28:31]
	s_waitcnt vmcnt(16)
	v_mfma_f32_16x16x32_f16 v[36:39], v[72:75], v[110:113], v[36:39]
	v_mfma_f32_16x16x32_f16 v[32:35], v[72:75], v[114:117], v[32:35]
	s_setprio 0
	s_add_i32 s16, s13, 0x340
	s_and_b32 s17, s16, 0x3c0
	s_lshl_b32 s26, s17, 4
	s_lshl_b32 s16, s16, 4
	v_lshl_add_u64 v[56:57], v[20:21], 0, s[26:27]
	s_or_b32 s26, s16, 0x4000
	v_lshl_add_u64 v[64:65], v[20:21], 0, s[26:27]
	global_load_dwordx4 v[68:71], v[56:57], off
	global_load_dwordx4 v[72:75], v[64:65], off
	s_add_i32 s16, s14, 0xa0
	s_and_b32 s16, s16, 0x1e0
	v_lshl_add_u32 v23, s16, 1, v19
	ds_read_b128 v[110:113], v23 offset:4096
	ds_read_b128 v[114:117], v23 offset:20736
	s_setprio 1
	s_waitcnt vmcnt(17) lgkmcnt(1)
	v_mfma_f32_16x16x32_f16 v[102:105], v[76:79], v[110:113], v[102:105]
	s_waitcnt lgkmcnt(0)
	v_mfma_f32_16x16x32_f16 v[28:31], v[76:79], v[114:117], v[28:31]
	s_waitcnt vmcnt(16)
	v_mfma_f32_16x16x32_f16 v[36:39], v[82:85], v[110:113], v[36:39]
	v_mfma_f32_16x16x32_f16 v[32:35], v[82:85], v[114:117], v[32:35]
	s_setprio 0
	s_add_i32 s16, s13, 0x380
	s_and_b32 s17, s16, 0x3c0
	s_lshl_b32 s26, s17, 4
	s_lshl_b32 s16, s16, 4
	v_lshl_add_u64 v[56:57], v[20:21], 0, s[26:27]
	s_or_b32 s26, s16, 0x4000
	v_lshl_add_u64 v[64:65], v[20:21], 0, s[26:27]
	global_load_dwordx4 v[76:79], v[56:57], off
	global_load_dwordx4 v[82:85], v[64:65], off
	s_add_i32 s16, s14, 0xc0
	s_and_b32 s16, s16, 0x1e0
	v_lshl_add_u32 v23, s16, 1, v19
	ds_read_b128 v[110:113], v23 offset:4096
	ds_read_b128 v[114:117], v23 offset:20736
	s_setprio 1
	s_waitcnt vmcnt(17) lgkmcnt(1)
	v_mfma_f32_16x16x32_f16 v[102:105], v[14:17], v[110:113], v[102:105]
	s_waitcnt lgkmcnt(0)
	v_mfma_f32_16x16x32_f16 v[14:17], v[14:17], v[114:117], v[28:31]
	s_waitcnt vmcnt(16)
	v_mfma_f32_16x16x32_f16 v[28:31], v[10:13], v[110:113], v[36:39]
	v_mfma_f32_16x16x32_f16 v[10:13], v[10:13], v[114:117], v[32:35]
	s_setprio 0
	s_addk_i32 s13, 0x3c0
	s_and_b32 s16, s13, 0x3c0
	s_lshl_b32 s26, s16, 4
	s_lshl_b32 s13, s13, 4
	v_lshl_add_u64 v[56:57], v[20:21], 0, s[26:27]
	s_or_b32 s26, s13, 0x4000
	v_lshl_add_u64 v[20:21], v[20:21], 0, s[26:27]
	global_load_dwordx4 v[32:35], v[56:57], off
	global_load_dwordx4 v[36:39], v[20:21], off
	s_add_i32 s13, s14, 0xe0
	s_and_b32 s13, s13, 0x1e0
	v_lshl_add_u32 v20, s13, 1, v19
	ds_read_b128 v[110:113], v20 offset:4096
	ds_read_b128 v[114:117], v20 offset:20736
	s_setprio 1
	s_waitcnt vmcnt(17) lgkmcnt(1)
	v_mfma_f32_16x16x32_f16 v[102:105], v[6:9], v[110:113], v[102:105]
	s_waitcnt lgkmcnt(0)
	v_mfma_f32_16x16x32_f16 v[6:9], v[6:9], v[114:117], v[14:17]
	s_waitcnt vmcnt(16)
	v_mfma_f32_16x16x32_f16 v[14:17], v[2:5], v[110:113], v[28:31]
	v_mfma_f32_16x16x32_f16 v[2:5], v[2:5], v[114:117], v[10:13]
	s_setprio 0
	v_add_u32_e32 v20, s15, v19
	s_nop 0
	ds_read_b128 v[10:13], v20 offset:4096
	ds_read_b128 v[28:31], v20 offset:20736
	s_setprio 1
	s_waitcnt vmcnt(15) lgkmcnt(1)
	v_mfma_f32_16x16x32_f16 v[102:105], v[86:89], v[10:13], v[102:105]
	s_waitcnt lgkmcnt(0)
	v_mfma_f32_16x16x32_f16 v[6:9], v[86:89], v[28:31], v[6:9]
	s_waitcnt vmcnt(14)
	v_mfma_f32_16x16x32_f16 v[10:13], v[90:93], v[10:13], v[14:17]
	v_mfma_f32_16x16x32_f16 v[2:5], v[90:93], v[28:31], v[2:5]
	s_setprio 0
	s_add_i32 s13, s14, 0x120
	s_and_b32 s13, s13, 0x1e0
	v_lshl_add_u32 v20, s13, 1, v19
	ds_read_b128 v[14:17], v20 offset:4096
	ds_read_b128 v[28:31], v20 offset:20736
	s_setprio 1
	s_waitcnt vmcnt(13) lgkmcnt(1)
	v_mfma_f32_16x16x32_f16 v[86:89], v[98:101], v[14:17], v[102:105]
	s_waitcnt lgkmcnt(0)
	v_mfma_f32_16x16x32_f16 v[6:9], v[98:101], v[28:31], v[6:9]
	s_waitcnt vmcnt(12)
	v_mfma_f32_16x16x32_f16 v[10:13], v[106:109], v[14:17], v[10:13]
	v_mfma_f32_16x16x32_f16 v[2:5], v[106:109], v[28:31], v[2:5]
	s_setprio 0
	s_add_i32 s13, s14, 0x140
	s_and_b32 s13, s13, 0x1e0
	v_lshl_add_u32 v20, s13, 1, v19
	ds_read_b128 v[14:17], v20 offset:4096
	ds_read_b128 v[28:31], v20 offset:20736
	s_setprio 1
	s_waitcnt vmcnt(11) lgkmcnt(1)
	v_mfma_f32_16x16x32_f16 v[86:89], v[40:43], v[14:17], v[86:89]
	s_waitcnt lgkmcnt(0)
	v_mfma_f32_16x16x32_f16 v[6:9], v[40:43], v[28:31], v[6:9]
	s_waitcnt vmcnt(10)
	v_mfma_f32_16x16x32_f16 v[10:13], v[94:97], v[14:17], v[10:13]
	v_mfma_f32_16x16x32_f16 v[2:5], v[94:97], v[28:31], v[2:5]
	s_setprio 0
	s_add_i32 s13, s14, 0x160
	s_and_b32 s13, s13, 0x1e0
	v_lshl_add_u32 v20, s13, 1, v19
	ds_read_b128 v[14:17], v20 offset:4096
	ds_read_b128 v[28:31], v20 offset:20736
	s_setprio 1
	s_waitcnt vmcnt(9) lgkmcnt(1)
	v_mfma_f32_16x16x32_f16 v[40:43], v[44:47], v[14:17], v[86:89]
	s_waitcnt lgkmcnt(0)
	v_mfma_f32_16x16x32_f16 v[6:9], v[44:47], v[28:31], v[6:9]
	s_waitcnt vmcnt(8)
	v_mfma_f32_16x16x32_f16 v[10:13], v[48:51], v[14:17], v[10:13]
	v_mfma_f32_16x16x32_f16 v[2:5], v[48:51], v[28:31], v[2:5]
	s_setprio 0
	s_add_i32 s13, s14, 0x180
	s_and_b32 s13, s13, 0x1e0
	v_lshl_add_u32 v20, s13, 1, v19
	ds_read_b128 v[14:17], v20 offset:4096
	ds_read_b128 v[28:31], v20 offset:20736
	s_setprio 1
	s_waitcnt vmcnt(7) lgkmcnt(1)
	v_mfma_f32_16x16x32_f16 v[40:43], v[52:55], v[14:17], v[40:43]
	s_waitcnt lgkmcnt(0)
	v_mfma_f32_16x16x32_f16 v[6:9], v[52:55], v[28:31], v[6:9]
	s_waitcnt vmcnt(6)
	v_mfma_f32_16x16x32_f16 v[10:13], v[60:63], v[14:17], v[10:13]
	v_mfma_f32_16x16x32_f16 v[2:5], v[60:63], v[28:31], v[2:5]
	s_setprio 0
	s_add_i32 s13, s14, 0x1a0
	s_and_b32 s13, s13, 0x1e0
	v_lshl_add_u32 v20, s13, 1, v19
	ds_read_b128 v[14:17], v20 offset:4096
	ds_read_b128 v[28:31], v20 offset:20736
	s_setprio 1
	s_waitcnt vmcnt(5) lgkmcnt(1)
	v_mfma_f32_16x16x32_f16 v[40:43], v[68:71], v[14:17], v[40:43]
	s_waitcnt lgkmcnt(0)
	v_mfma_f32_16x16x32_f16 v[6:9], v[68:71], v[28:31], v[6:9]
	s_waitcnt vmcnt(4)
	v_mfma_f32_16x16x32_f16 v[10:13], v[72:75], v[14:17], v[10:13]
	v_mfma_f32_16x16x32_f16 v[2:5], v[72:75], v[28:31], v[2:5]
	s_setprio 0
	s_add_i32 s13, s14, 0x1c0
	s_and_b32 s13, s13, 0x1e0
	v_lshl_add_u32 v20, s13, 1, v19
	ds_read_b128 v[14:17], v20 offset:4096
	ds_read_b128 v[28:31], v20 offset:20736
	s_setprio 1
	s_waitcnt vmcnt(3) lgkmcnt(1)
	v_mfma_f32_16x16x32_f16 v[40:43], v[76:79], v[14:17], v[40:43]
	s_waitcnt lgkmcnt(0)
	v_mfma_f32_16x16x32_f16 v[6:9], v[76:79], v[28:31], v[6:9]
	s_waitcnt vmcnt(2)
	v_mfma_f32_16x16x32_f16 v[10:13], v[82:85], v[14:17], v[10:13]
	v_mfma_f32_16x16x32_f16 v[2:5], v[82:85], v[28:31], v[2:5]
	s_setprio 0
	s_addk_i32 s14, 0x1e0
	s_and_b32 s13, s14, 0x1e0
	v_lshl_add_u32 v20, s13, 1, v19
	ds_read_b128 v[14:17], v20 offset:4096
	ds_read_b128 v[28:31], v20 offset:20736
	s_setprio 1
	s_waitcnt vmcnt(1) lgkmcnt(1)
	v_mfma_f32_16x16x32_f16 v[40:43], v[32:35], v[14:17], v[40:43]
	s_waitcnt lgkmcnt(0)
	v_mfma_f32_16x16x32_f16 v[6:9], v[32:35], v[28:31], v[6:9]
	s_waitcnt vmcnt(0)
	v_mfma_f32_16x16x32_f16 v[10:13], v[36:39], v[14:17], v[10:13]
	v_mfma_f32_16x16x32_f16 v[2:5], v[36:39], v[28:31], v[2:5]
	s_setprio 0
	v_add_u32_e32 v19, v19, v22
	v_lshlrev_b32_e32 v20, 15, v118
	v_mov_b32_e32 v21, v67
	s_bfe_u32 s22, s2, 0x30003
	v_lshl_add_u64 v[20:21], s[10:11], 0, v[20:21]
	s_lshl_b32 s26, s22, 10
	v_lshl_add_u64 v[64:65], v[20:21], 0, v[58:59]
	v_lshl_add_u64 v[52:53], v[64:65], 0, s[26:27]
	v_add_co_u32_e32 v76, vcc, s29, v52
	s_lshl_b32 s53, s22, 6
	s_nop 0
	v_addc_co_u32_e32 v77, vcc, 0, v53, vcc
	s_mov_b32 s14, 0x14000
	v_mov_b32_e32 v22, 0x14000
	v_mul_u32_u24_e32 v23, 0x210, v81
	s_add_i32 s38, s53, 64
	v_lshlrev_b32_e32 v83, 2, v118
	s_movk_i32 s16, 0x1040
	s_movk_i32 s18, 0x840
	v_lshl_or_b32 v1, v1, 3, v22
	v_add3_u32 v84, v23, v18, s14
	s_and_b32 s14, s38, 0x1c0
	s_movk_i32 s20, 0x210
	s_mov_b32 s19, s27
	v_mad_u32_u24 v56, v118, s16, v58
	v_or_b32_e32 v22, 1, v83
	v_mad_u32_u24 v98, v118, s18, v1
	s_lshl_b32 s18, s14, 4
	v_mad_u32_u24 v99, v22, s12, v58
	v_mad_u32_u24 v85, v22, s20, v1
	v_lshl_add_u64 v[54:55], v[64:65], 0, s[18:19]
	s_add_i32 s12, s53, 0xc0
	s_and_b32 s2, s3, 0x7ffffff
	s_lshl_b32 s3, s22, 5
	s_and_b32 s39, s12, 0x1c0
	s_lshl_b32 s14, s39, 4
	s_add_i32 s39, s3, 32
	s_and_b32 s39, s39, 0xe0
	v_lshl_add_u32 v82, s39, 1, v84
	s_add_i32 s11, s53, 0x80
	s_lshl_b32 s16, s38, 4
	s_mov_b32 s21, s27
	s_and_b32 s30, s11, 0x1c0
	s_lshl_b32 s11, s11, 4
	s_or_b32 s20, s16, 0x2000
	s_mov_b32 s23, s27
	s_mov_b32 s31, s27
	s_mov_b32 s35, s27
	s_or_b32 s22, s16, 0x6000
	s_lshl_b32 s30, s30, 4
	s_or_b32 s34, s11, 0x2000
	v_lshl_add_u64 v[26:27], v[64:65], 0, s[20:21]
	v_lshl_add_u64 v[28:29], v[64:65], 0, s[22:23]
	v_lshl_add_u64 v[30:31], v[64:65], 0, s[30:31]
	v_lshl_add_u64 v[32:33], v[64:65], 0, s[34:35]
	s_mov_b64 s[40:41], 0x40000
	v_lshl_add_u64 v[60:61], v[64:65], 0, s[40:41]
	s_mov_b32 s37, s27
	s_or_b32 s36, s11, 0x6000
	v_lshl_add_u64 v[74:75], v[64:65], 0, s[36:37]
	s_mov_b32 s15, s27
	s_lshl_b32 s12, s12, 4
	v_lshl_add_u64 v[70:71], v[64:65], 0, s[14:15]
	s_mov_b32 s17, s27
	s_or_b32 s16, s12, 0x2000
	s_mov_b32 s13, s27
	s_or_b32 s12, s12, 0x6000
	v_lshl_add_u64 v[72:73], v[64:65], 0, s[16:17]
	v_lshl_add_u64 v[68:69], v[64:65], 0, s[12:13]
	v_add_u32_e32 v1, s53, v84
	s_xor_b32 s10, s26, 0x1000
	s_mov_b32 s11, s27
	s_mov_b32 s49, s27
	s_mov_b32 s51, s27
	s_mov_b32 s47, s27
	v_pk_add_f32 v[14:15], v[180:181], v[40:41]
	v_pk_add_f32 v[16:17], v[182:183], v[42:43]
	v_pk_add_f32 v[10:11], v[184:185], v[10:11]
	v_pk_add_f32 v[12:13], v[186:187], v[12:13]
	v_pk_add_f32 v[6:7], v[188:189], v[6:7]
	v_pk_add_f32 v[8:9], v[190:191], v[8:9]
	v_pk_add_f32 v[2:3], v[192:193], v[2:3]
	v_pk_add_f32 v[4:5], v[194:195], v[4:5]
	ds_write_b128 v19, v[14:17] offset:37376
	ds_write_b128 v19, v[10:13] offset:37440
	ds_write_b128 v19, v[6:9] offset:54016
	ds_write_b128 v19, v[2:5] offset:54080
	v_mov_b64_e32 v[34:35], v[204:205]
	v_mov_b64_e32 v[36:37], v[206:207]
	v_mov_b64_e32 v[38:39], v[208:209]
	v_mov_b64_e32 v[40:41], v[210:211]
	v_add_co_u32_e32 v2, vcc, s52, v52
	s_waitcnt lgkmcnt(0)
	s_nop 0
	v_addc_co_u32_e32 v3, vcc, 0, v53, vcc
	v_add_co_u32_e32 v4, vcc, s33, v52
	s_barrier
	s_nop 0
	v_addc_co_u32_e32 v5, vcc, 0, v53, vcc
	global_load_dwordx4 v[14:17], v[2:3], off
	global_load_dwordx4 v[18:21], v[4:5], off
	global_load_dwordx4 v[22:25], v[52:53], off
	global_load_dwordx4 v[10:13], v[54:55], off
	ds_read_b128 v[2:5], v56 offset:37376
	ds_read_b128 v[6:9], v99 offset:37376
	v_add_co_u32_e32 v78, vcc, s52, v54
	s_mov_b32 s43, s27
	s_waitcnt lgkmcnt(1)
	v_add_f32_e32 v42, v2, v3
	v_add_f32_e32 v42, v42, v4
	v_add_f32_e32 v42, v42, v5
	v_addc_co_u32_e32 v79, vcc, 0, v55, vcc
	s_nop 0
	v_add_f32_dpp v42, v42, v42 quad_perm:[1,0,3,2] row_mask:0xf bank_mask:0xf bound_ctrl:1
	s_mov_b32 s45, s27
	s_mov_b32 s41, s27
	v_add_f32_dpp v42, v42, v42 quad_perm:[2,3,0,1] row_mask:0xf bank_mask:0xf bound_ctrl:1
	v_lshl_add_u64 v[62:63], v[64:65], 0, s[10:11]
	v_lshl_add_u64 v[58:59], s[4:5], 0, v[58:59]
	v_add_f32_dpp v42, v42, v42 row_half_mirror row_mask:0xf bank_mask:0xf bound_ctrl:1
	v_lshl_add_u64 v[152:153], v[60:61], 0, s[26:27]
	v_lshl_add_u64 v[154:155], v[60:61], 0, s[18:19]
	v_add_f32_dpp v42, v42, v42 row_mirror row_mask:0xf bank_mask:0xf bound_ctrl:1
	v_lshl_add_u64 v[156:157], v[60:61], 0, s[20:21]
	v_readlane_b32 s8, v42, 16
	v_readlane_b32 s9, v42, 48
	v_readlane_b32 s6, v42, 0
	v_readlane_b32 s7, v42, 32
	v_mov_b32_e32 v42, s8
	v_mov_b32_e32 v43, s9
	v_pk_add_f32 v[42:43], s[6:7], v[42:43]
	s_mov_b32 s6, 0x3b800000
	v_add_f32_e32 v42, v42, v43
	v_mul_f32_e32 v42, 0x3b800000, v42
	v_pk_add_f32 v[86:87], v[2:3], v[42:43] op_sel_hi:[1,0] neg_lo:[0,1] neg_hi:[0,1]
	v_pk_add_f32 v[88:89], v[4:5], v[42:43] op_sel_hi:[1,0] neg_lo:[0,1] neg_hi:[0,1]
	v_pk_mul_f32 v[42:43], v[86:87], v[86:87]
	v_pk_mul_f32 v[44:45], v[88:89], v[88:89]
	v_add_f32_e32 v42, v42, v43
	v_add_f32_e32 v42, v44, v42
	s_waitcnt lgkmcnt(0)
	v_add_f32_e32 v44, v6, v7
	v_add_f32_e32 v42, v45, v42
	v_add_f32_e32 v44, v44, v8
	v_add_f32_e32 v44, v44, v9
	v_add_f32_dpp v42, v42, v42 quad_perm:[1,0,3,2] row_mask:0xf bank_mask:0xf bound_ctrl:1
	v_lshl_add_u64 v[158:159], v[60:61], 0, s[22:23]
	v_add_f32_dpp v44, v44, v44 quad_perm:[1,0,3,2] row_mask:0xf bank_mask:0xf bound_ctrl:1
	v_add_f32_dpp v42, v42, v42 quad_perm:[2,3,0,1] row_mask:0xf bank_mask:0xf bound_ctrl:1
	v_lshl_add_u64 v[160:161], v[60:61], 0, s[30:31]
	v_add_f32_dpp v44, v44, v44 quad_perm:[2,3,0,1] row_mask:0xf bank_mask:0xf bound_ctrl:1
	v_add_f32_dpp v42, v42, v42 row_half_mirror row_mask:0xf bank_mask:0xf bound_ctrl:1
	v_lshl_add_u64 v[162:163], v[60:61], 0, s[34:35]
	v_add_f32_dpp v44, v44, v44 row_half_mirror row_mask:0xf bank_mask:0xf bound_ctrl:1
	v_add_f32_dpp v42, v42, v42 row_mirror row_mask:0xf bank_mask:0xf bound_ctrl:1
	v_lshl_add_u64 v[164:165], v[60:61], 0, s[36:37]
	v_readlane_b32 s7, v42, 16
	v_readlane_b32 s39, v42, 48
	v_add_f32_dpp v44, v44, v44 row_mirror row_mask:0xf bank_mask:0xf bound_ctrl:1
	v_readlane_b32 s8, v42, 0
	v_readlane_b32 s9, v42, 32
	v_mov_b32_e32 v42, s7
	v_mov_b32_e32 v43, s39
	v_readlane_b32 s7, v44, 16
	v_readlane_b32 s39, v44, 48
	v_pk_add_f32 v[42:43], s[8:9], v[42:43]
	v_readlane_b32 s8, v44, 0
	v_readlane_b32 s9, v44, 32
	v_mov_b32_e32 v44, s7
	v_mov_b32_e32 v45, s39
	v_pk_add_f32 v[44:45], s[8:9], v[44:45]
	s_nop 0
	v_add_f32_e32 v44, v44, v45
	v_mul_f32_e32 v44, 0x3b800000, v44
	v_pk_add_f32 v[90:91], v[6:7], v[44:45] op_sel_hi:[1,0] neg_lo:[0,1] neg_hi:[0,1]
	v_pk_add_f32 v[92:93], v[8:9], v[44:45] op_sel_hi:[1,0] neg_lo:[0,1] neg_hi:[0,1]
	v_pk_mul_f32 v[46:47], v[90:91], v[90:91]
	v_pk_mul_f32 v[44:45], v[92:93], v[92:93]
	v_add_f32_e32 v46, v46, v47
	v_add_f32_e32 v44, v44, v46
	v_add_f32_e32 v44, v45, v44
	v_mov_b32_e32 v47, v42
	s_nop 0
	v_add_f32_dpp v44, v44, v44 quad_perm:[1,0,3,2] row_mask:0xf bank_mask:0xf bound_ctrl:1
	s_nop 1
	v_add_f32_dpp v44, v44, v44 quad_perm:[2,3,0,1] row_mask:0xf bank_mask:0xf bound_ctrl:1
	s_nop 1
	v_add_f32_dpp v44, v44, v44 row_half_mirror row_mask:0xf bank_mask:0xf bound_ctrl:1
	s_nop 1
	v_add_f32_dpp v44, v44, v44 row_mirror row_mask:0xf bank_mask:0xf bound_ctrl:1
	s_nop 0
	v_readlane_b32 s7, v44, 16
	v_readlane_b32 s39, v44, 48
	v_readlane_b32 s8, v44, 0
	v_readlane_b32 s9, v44, 32
	v_mov_b32_e32 v44, s7
	v_mov_b32_e32 v45, s39
	v_pk_add_f32 v[44:45], s[8:9], v[44:45]
	s_mov_b32 s8, 0x3727c5ac
	v_mov_b32_e32 v46, v44
	v_mov_b32_e32 v42, v45
	v_pk_add_f32 v[42:43], v[46:47], v[42:43]
	v_mov_b64_e32 v[94:95], s[8:9]
	v_pk_fma_f32 v[96:97], v[42:43], s[6:7], v[94:95] op_sel_hi:[1,0,0]
	s_mov_b32 s7, 0x800000
	v_mul_f32_e32 v42, 0x4b800000, v97
	v_cmp_gt_f32_e32 vcc, s7, v97
	s_nop 1
	v_cndmask_b32_e32 v42, v97, v42, vcc
	v_rsq_f32_e32 v97, v42
	global_load_dwordx4 v[54:57], v[26:27], off
	global_load_dwordx4 v[50:53], v[28:29], off
	global_load_dwordx4 v[46:49], v[30:31], off
	global_load_dwordx4 v[42:45], v[32:33], off
	v_mul_f32_e32 v26, 0x45800000, v97
	v_cndmask_b32_e32 v26, v97, v26, vcc
	v_pk_mul_f32 v[28:29], v[86:87], v[26:27] op_sel_hi:[1,0]
	v_cmp_gt_f32_e32 vcc, s7, v96
	s_waitcnt vmcnt(8)
	v_pk_fma_f32 v[28:29], v[34:35], v[28:29], v[38:39]
	v_pk_mul_f32 v[26:27], v[88:89], v[26:27] op_sel_hi:[1,0]
	v_cvt_pk_f16_f32 v28, v28, v29
	v_mul_f32_e32 v29, 0x4b800000, v96
	v_cndmask_b32_e32 v29, v96, v29, vcc
	v_rsq_f32_e32 v32, v29
	v_pk_fma_f32 v[26:27], v[36:37], v[26:27], v[40:41]
	s_nop 0
	v_cvt_pk_f16_f32 v29, v26, v27
	v_mul_f32_e32 v26, 0x45800000, v32
	v_cndmask_b32_e32 v26, v32, v26, vcc
	ds_write_b64 v98, v[28:29]
	v_pk_mul_f32 v[28:29], v[90:91], v[26:27] op_sel_hi:[1,0]
	v_pk_mul_f32 v[26:27], v[92:93], v[26:27] op_sel_hi:[1,0]
	v_pk_fma_f32 v[28:29], v[34:35], v[28:29], v[38:39]
	v_pk_fma_f32 v[26:27], v[36:37], v[26:27], v[40:41]
	v_cvt_pk_f16_f32 v28, v28, v29
	v_cvt_pk_f16_f32 v29, v26, v27
	ds_write_b64 v85, v[28:29]
	ds_read_b128 v[26:29], v99 offset:38416
	v_add_co_u32_e32 v102, vcc, s52, v30
	s_nop 1
	v_addc_co_u32_e32 v103, vcc, 0, v31, vcc
	ds_read_b128 v[30:33], v99 offset:39456
	s_waitcnt lgkmcnt(1)
	v_add_f32_e32 v86, v26, v27
	v_add_f32_e32 v86, v86, v28
	v_add_f32_e32 v86, v86, v29
	s_nop 1
	v_add_f32_dpp v86, v86, v86 quad_perm:[1,0,3,2] row_mask:0xf bank_mask:0xf bound_ctrl:1
	s_nop 1
	v_add_f32_dpp v86, v86, v86 quad_perm:[2,3,0,1] row_mask:0xf bank_mask:0xf bound_ctrl:1
	s_nop 1
	v_add_f32_dpp v86, v86, v86 row_half_mirror row_mask:0xf bank_mask:0xf bound_ctrl:1
	s_nop 1
	v_add_f32_dpp v86, v86, v86 row_mirror row_mask:0xf bank_mask:0xf bound_ctrl:1
	s_nop 0
	v_readlane_b32 s39, v86, 16
	v_readlane_b32 s40, v86, 48
	v_readlane_b32 s8, v86, 0
	v_readlane_b32 s9, v86, 32
	v_mov_b32_e32 v86, s39
	v_mov_b32_e32 v87, s40
	v_pk_add_f32 v[86:87], s[8:9], v[86:87]
	s_nop 0
	v_add_f32_e32 v86, v86, v87
	v_mul_f32_e32 v86, 0x3b800000, v86
	v_pk_add_f32 v[104:105], v[26:27], v[86:87] op_sel_hi:[1,0] neg_lo:[0,1] neg_hi:[0,1]
	v_pk_add_f32 v[106:107], v[28:29], v[86:87] op_sel_hi:[1,0] neg_lo:[0,1] neg_hi:[0,1]
	v_pk_mul_f32 v[88:89], v[104:105], v[104:105]
	v_pk_mul_f32 v[86:87], v[106:107], v[106:107]
	v_add_f32_e32 v88, v88, v89
	v_add_f32_e32 v86, v86, v88
	s_waitcnt lgkmcnt(0)
	v_add_f32_e32 v88, v30, v31
	v_add_f32_e32 v86, v87, v86
	v_add_f32_e32 v88, v88, v32
	v_add_f32_e32 v88, v88, v33
	v_add_f32_dpp v86, v86, v86 quad_perm:[1,0,3,2] row_mask:0xf bank_mask:0xf bound_ctrl:1
	s_nop 0
	v_add_f32_dpp v88, v88, v88 quad_perm:[1,0,3,2] row_mask:0xf bank_mask:0xf bound_ctrl:1
	v_add_f32_dpp v86, v86, v86 quad_perm:[2,3,0,1] row_mask:0xf bank_mask:0xf bound_ctrl:1
	s_nop 0
	v_add_f32_dpp v88, v88, v88 quad_perm:[2,3,0,1] row_mask:0xf bank_mask:0xf bound_ctrl:1
	v_add_f32_dpp v86, v86, v86 row_half_mirror row_mask:0xf bank_mask:0xf bound_ctrl:1
	s_nop 0
	v_add_f32_dpp v88, v88, v88 row_half_mirror row_mask:0xf bank_mask:0xf bound_ctrl:1
	v_add_f32_dpp v86, v86, v86 row_mirror row_mask:0xf bank_mask:0xf bound_ctrl:1
	s_nop 0
	v_readlane_b32 s39, v86, 16
	v_readlane_b32 s40, v86, 48
	v_add_f32_dpp v88, v88, v88 row_mirror row_mask:0xf bank_mask:0xf bound_ctrl:1
	v_readlane_b32 s8, v86, 0
	v_readlane_b32 s9, v86, 32
	v_mov_b32_e32 v86, s39
	v_mov_b32_e32 v87, s40
	v_readlane_b32 s39, v88, 16
	v_readlane_b32 s40, v88, 48
	v_pk_add_f32 v[86:87], s[8:9], v[86:87]
	v_readlane_b32 s8, v88, 0
	v_readlane_b32 s9, v88, 32
	v_mov_b32_e32 v88, s39
	v_mov_b32_e32 v89, s40
	v_pk_add_f32 v[88:89], s[8:9], v[88:89]
	s_nop 0
	v_add_f32_e32 v88, v88, v89
	v_mul_f32_e32 v88, 0x3b800000, v88
	v_pk_add_f32 v[108:109], v[30:31], v[88:89] op_sel_hi:[1,0] neg_lo:[0,1] neg_hi:[0,1]
	v_pk_add_f32 v[110:111], v[32:33], v[88:89] op_sel_hi:[1,0] neg_lo:[0,1] neg_hi:[0,1]
	v_pk_mul_f32 v[90:91], v[108:109], v[108:109]
	v_pk_mul_f32 v[88:89], v[110:111], v[110:111]
	v_add_f32_e32 v90, v90, v91
	v_add_f32_e32 v88, v88, v90
	v_add_f32_e32 v88, v89, v88
	v_mov_b32_e32 v91, v86
	s_nop 0
	v_add_f32_dpp v88, v88, v88 quad_perm:[1,0,3,2] row_mask:0xf bank_mask:0xf bound_ctrl:1
	s_nop 1
	v_add_f32_dpp v88, v88, v88 quad_perm:[2,3,0,1] row_mask:0xf bank_mask:0xf bound_ctrl:1
	s_nop 1
	v_add_f32_dpp v88, v88, v88 row_half_mirror row_mask:0xf bank_mask:0xf bound_ctrl:1
	s_nop 1
	v_add_f32_dpp v88, v88, v88 row_mirror row_mask:0xf bank_mask:0xf bound_ctrl:1
	s_nop 0
	v_readlane_b32 s39, v88, 16
	v_readlane_b32 s40, v88, 48
	v_readlane_b32 s8, v88, 0
	v_readlane_b32 s9, v88, 32
	v_mov_b32_e32 v88, s39
	v_mov_b32_e32 v89, s40
	v_pk_add_f32 v[88:89], s[8:9], v[88:89]
	s_mov_b32 s9, s27
	v_mov_b32_e32 v90, v88
	v_mov_b32_e32 v86, v89
	v_pk_add_f32 v[86:87], v[90:91], v[86:87]
	s_mov_b32 s39, s27
	v_pk_fma_f32 v[112:113], v[86:87], s[6:7], v[94:95] op_sel_hi:[1,0,0]
	s_add_i32 s6, s53, 0x140
	v_mul_f32_e32 v86, 0x4b800000, v113
	v_cmp_gt_f32_e32 vcc, s7, v113
	s_nop 1
	v_cndmask_b32_e32 v86, v113, v86, vcc
	v_rsq_f32_e32 v113, v86
	global_load_dwordx4 v[86:89], v[78:79], off
	global_load_dwordx4 v[90:93], v[102:103], off
	global_load_dwordx4 v[94:97], v[76:77], off
	global_load_dwordx4 v[98:101], v[74:75], off
	v_mul_f32_e32 v74, 0x45800000, v113
	v_cndmask_b32_e32 v74, v113, v74, vcc
	v_pk_mul_f32 v[76:77], v[104:105], v[74:75] op_sel_hi:[1,0]
	v_mul_f32_e32 v75, 0x4b800000, v112
	v_cmp_gt_f32_e32 vcc, s7, v112
	v_pk_fma_f32 v[76:77], v[34:35], v[76:77], v[38:39]
	s_and_b32 s7, s6, 0x1c0
	v_cndmask_b32_e32 v75, v112, v75, vcc
	v_rsq_f32_e32 v78, v75
	v_pk_mul_f32 v[74:75], v[106:107], v[74:75] op_sel_hi:[1,0]
	v_cvt_pk_f16_f32 v76, v76, v77
	v_pk_fma_f32 v[74:75], v[36:37], v[74:75], v[40:41]
	s_lshl_b32 s6, s6, 4
	v_cvt_pk_f16_f32 v77, v74, v75
	v_mul_f32_e32 v74, 0x45800000, v78
	v_cndmask_b32_e32 v74, v78, v74, vcc
	v_pk_mul_f32 v[78:79], v[108:109], v[74:75] op_sel_hi:[1,0]
	s_or_b32 s50, s6, 0x2000
	v_pk_fma_f32 v[34:35], v[34:35], v[78:79], v[38:39]
	v_pk_mul_f32 v[38:39], v[110:111], v[74:75] op_sel_hi:[1,0]
	v_add_co_u32_e32 v78, vcc, s52, v70
	v_pk_fma_f32 v[36:37], v[36:37], v[38:39], v[40:41]
	v_cvt_pk_f16_f32 v34, v34, v35
	v_cvt_pk_f16_f32 v35, v36, v37
	v_addc_co_u32_e32 v79, vcc, 0, v71, vcc
	ds_write2_b64 v85, v[76:77], v[34:35] offset0:66 offset1:132
	s_waitcnt lgkmcnt(0)
	s_barrier
	global_load_dwordx4 v[34:37], v[70:71], off
	global_load_dwordx4 v[38:41], v[72:73], off
	s_nop 0
	global_load_dwordx4 v[70:73], v[78:79], off
	global_load_dwordx4 v[74:77], v[68:69], off
	s_or_b32 s46, s6, 0x6000
	s_sub_i32 s6, s38, s3
	s_and_b32 s6, s6, 0xe0
	v_lshl_add_u32 v172, s6, 1, v84
	s_add_i32 s6, s53, 0x180
	s_lshl_b32 s48, s7, 4
	s_and_b32 s7, s6, 0x1c0
	s_lshl_b32 s6, s6, 4
	s_or_b32 s44, s6, 0x2000
	s_or_b32 s40, s6, 0x6000
	s_add_i32 s6, s3, 0x60
	s_and_b32 s6, s6, 0xe0
	v_lshl_add_u32 v173, s6, 1, v84
	s_add_i32 s6, s53, 0x1c0
	s_xor_b32 s53, s53, 0x100
	v_add_u32_e32 v174, s53, v84
	s_add_i32 s53, s3, 0xa0
	s_lshl_b32 s42, s7, 4
	s_and_b32 s7, s6, 0x1c0
	s_lshl_b32 s6, s6, 4
	s_and_b32 s53, s53, 0xe0
	s_lshl_b32 s8, s7, 4
	s_or_b32 s38, s6, 0x2000
	s_or_b32 s6, s6, 0x6000
	s_mov_b32 s7, s27
	v_lshl_add_u32 v175, s53, 1, v84
	s_add_i32 s53, s3, 0xc0
	s_addk_i32 s3, 0xe0
	v_lshl_add_u64 v[68:69], v[64:65], 0, s[48:49]
	v_lshl_add_u64 v[78:79], v[64:65], 0, s[50:51]
	v_lshl_add_u64 v[138:139], v[64:65], 0, s[46:47]
	v_lshl_add_u64 v[140:141], v[64:65], 0, s[42:43]
	v_lshl_add_u64 v[142:143], v[64:65], 0, s[44:45]
	v_lshl_add_u64 v[144:145], v[64:65], 0, s[40:41]
	v_lshl_add_u64 v[146:147], v[64:65], 0, s[8:9]
	v_lshl_add_u64 v[148:149], v[64:65], 0, s[38:39]
	v_lshl_add_u64 v[150:151], v[64:65], 0, s[6:7]
	s_and_b32 s53, s53, 0xe0
	s_and_b32 s3, s3, 0xe0
	v_add_u32_e32 v64, s28, v83
	v_mov_b32_e32 v65, v67
	v_lshl_add_u32 v176, s53, 1, v84
	v_lshl_add_u32 v177, s3, 1, v84
	v_lshlrev_b64 v[84:85], 10, v[64:65]
	ds_read_b128 v[102:105], v1
	ds_read_b128 v[106:109], v1 offset:8448
	v_lshl_add_u64 v[166:167], v[58:59], 0, v[84:85]
	v_or_b32_e32 v84, 1, v64
	v_mov_b32_e32 v85, v67
	v_lshlrev_b64 v[84:85], 10, v[84:85]
	v_lshl_add_u64 v[168:169], v[58:59], 0, v[84:85]
	v_or_b32_e32 v84, 2, v64
	v_mov_b32_e32 v85, v67
	v_or_b32_e32 v64, 3, v64
	v_lshlrev_b64 v[84:85], 10, v[84:85]
	v_lshlrev_b64 v[64:65], 10, v[64:65]
	v_lshl_add_u64 v[170:171], v[58:59], 0, v[84:85]
	v_lshl_add_u64 v[58:59], v[58:59], 0, v[64:65]
	s_setprio 1
	s_waitcnt vmcnt(13) lgkmcnt(1)
	v_mfma_f32_16x16x32_f16 v[110:113], v[102:105], v[22:25], 0
	s_waitcnt lgkmcnt(0)
	v_mfma_f32_16x16x32_f16 v[22:25], v[106:109], v[22:25], 0
	s_waitcnt vmcnt(5)
	v_mfma_f32_16x16x32_f16 v[114:117], v[102:105], v[94:97], 0
	v_mfma_f32_16x16x32_f16 v[94:97], v[106:109], v[94:97], 0
	v_mfma_f32_16x16x32_f16 v[118:121], v[102:105], v[14:17], 0
	v_mfma_f32_16x16x32_f16 v[14:17], v[106:109], v[14:17], 0
	v_mfma_f32_16x16x32_f16 v[102:105], v[102:105], v[18:21], 0
	v_mfma_f32_16x16x32_f16 v[18:21], v[106:109], v[18:21], 0
	s_setprio 0
	v_add_co_u32_e32 v64, vcc, s29, v62
	global_load_dwordx4 v[106:109], v[62:63], off
	s_nop 0
	v_addc_co_u32_e32 v65, vcc, 0, v63, vcc
	v_add_co_u32_e32 v84, vcc, s52, v62
	s_nop 1
	v_addc_co_u32_e32 v85, vcc, 0, v63, vcc
	v_add_co_u32_e32 v62, vcc, s33, v62
	global_load_dwordx4 v[122:125], v[64:65], off
	global_load_dwordx4 v[126:129], v[84:85], off
	v_addc_co_u32_e32 v63, vcc, 0, v63, vcc
	global_load_dwordx4 v[62:65], v[62:63], off
	ds_read_b128 v[130:133], v82
	ds_read_b128 v[134:137], v82 offset:8448
	s_setprio 1
	s_waitcnt lgkmcnt(1)
	v_mfma_f32_16x16x32_f16 v[110:113], v[130:133], v[10:13], v[110:113]
	s_waitcnt lgkmcnt(0)
	v_mfma_f32_16x16x32_f16 v[10:13], v[134:137], v[10:13], v[22:25]
	v_mfma_f32_16x16x32_f16 v[22:25], v[130:133], v[54:57], v[114:117]
	v_mfma_f32_16x16x32_f16 v[54:57], v[134:137], v[54:57], v[94:97]
	v_mfma_f32_16x16x32_f16 v[94:97], v[130:133], v[86:89], v[118:121]
	v_mfma_f32_16x16x32_f16 v[14:17], v[134:137], v[86:89], v[14:17]
	v_mfma_f32_16x16x32_f16 v[84:87], v[130:133], v[50:53], v[102:105]
	v_mfma_f32_16x16x32_f16 v[18:21], v[134:137], v[50:53], v[18:21]
	s_setprio 0
	global_load_dwordx4 v[50:53], v[68:69], off
	global_load_dwordx4 v[102:105], v[78:79], off
	v_add_co_u32_e32 v68, vcc, s52, v68
	s_nop 1
	v_addc_co_u32_e32 v69, vcc, 0, v69, vcc
	global_load_dwordx4 v[114:117], v[68:69], off
	global_load_dwordx4 v[118:121], v[138:139], off
	ds_read_b128 v[130:133], v172
	ds_read_b128 v[134:137], v172 offset:8448
	s_setprio 1
	s_waitcnt lgkmcnt(1)
	v_mfma_f32_16x16x32_f16 v[110:113], v[130:133], v[46:49], v[110:113]
	s_waitcnt lgkmcnt(0)
	v_mfma_f32_16x16x32_f16 v[10:13], v[134:137], v[46:49], v[10:13]
	v_mfma_f32_16x16x32_f16 v[22:25], v[130:133], v[42:45], v[22:25]
	v_mfma_f32_16x16x32_f16 v[42:45], v[134:137], v[42:45], v[54:57]
	v_mfma_f32_16x16x32_f16 v[46:49], v[130:133], v[90:93], v[94:97]
	v_mfma_f32_16x16x32_f16 v[14:17], v[134:137], v[90:93], v[14:17]
	s_waitcnt vmcnt(12)
	v_mfma_f32_16x16x32_f16 v[54:57], v[130:133], v[98:101], v[84:87]
	v_mfma_f32_16x16x32_f16 v[18:21], v[134:137], v[98:101], v[18:21]
	s_setprio 0
	v_add_co_u32_e32 v68, vcc, s52, v140
	global_load_dwordx4 v[84:87], v[140:141], off
	global_load_dwordx4 v[88:91], v[142:143], off
	v_addc_co_u32_e32 v69, vcc, 0, v141, vcc
	global_load_dwordx4 v[92:95], v[68:69], off
	global_load_dwordx4 v[96:99], v[144:145], off
	ds_read_b128 v[130:133], v173
	ds_read_b128 v[134:137], v173 offset:8448
	s_setprio 1
	s_waitcnt vmcnt(15) lgkmcnt(1)
	v_mfma_f32_16x16x32_f16 v[110:113], v[130:133], v[34:37], v[110:113]
	s_waitcnt lgkmcnt(0)
	v_mfma_f32_16x16x32_f16 v[10:13], v[134:137], v[34:37], v[10:13]
	s_waitcnt vmcnt(14)
	v_mfma_f32_16x16x32_f16 v[22:25], v[130:133], v[38:41], v[22:25]
	v_mfma_f32_16x16x32_f16 v[34:37], v[134:137], v[38:41], v[42:45]
	s_waitcnt vmcnt(13)
	v_mfma_f32_16x16x32_f16 v[38:41], v[130:133], v[70:73], v[46:49]
	v_mfma_f32_16x16x32_f16 v[14:17], v[134:137], v[70:73], v[14:17]
	s_waitcnt vmcnt(12)
	v_mfma_f32_16x16x32_f16 v[42:45], v[130:133], v[74:77], v[54:57]
	v_mfma_f32_16x16x32_f16 v[18:21], v[134:137], v[74:77], v[18:21]
	s_setprio 0
	v_add_co_u32_e32 v68, vcc, s52, v146
	global_load_dwordx4 v[46:49], v[146:147], off
	global_load_dwordx4 v[54:57], v[148:149], off
	v_addc_co_u32_e32 v69, vcc, 0, v147, vcc
	global_load_dwordx4 v[68:71], v[68:69], off
	s_nop 0
	global_load_dwordx4 v[72:75], v[150:151], off
	ds_read_b128 v[76:79], v174
	ds_read_b128 v[130:133], v174 offset:8448
	s_setprio 1
	s_waitcnt vmcnt(15) lgkmcnt(1)
	v_mfma_f32_16x16x32_f16 v[110:113], v[76:79], v[106:109], v[110:113]
	s_waitcnt lgkmcnt(0)
	v_mfma_f32_16x16x32_f16 v[10:13], v[130:133], v[106:109], v[10:13]
	s_waitcnt vmcnt(14)
	v_mfma_f32_16x16x32_f16 v[22:25], v[76:79], v[122:125], v[22:25]
	v_mfma_f32_16x16x32_f16 v[34:37], v[130:133], v[122:125], v[34:37]
	s_waitcnt vmcnt(13)
	v_mfma_f32_16x16x32_f16 v[38:41], v[76:79], v[126:129], v[38:41]
	v_mfma_f32_16x16x32_f16 v[14:17], v[130:133], v[126:129], v[14:17]
	s_waitcnt vmcnt(12)
	v_mfma_f32_16x16x32_f16 v[42:45], v[76:79], v[62:65], v[42:45]
	v_mfma_f32_16x16x32_f16 v[18:21], v[130:133], v[62:65], v[18:21]
	s_setprio 0
	ds_read_b128 v[62:65], v175
	ds_read_b128 v[76:79], v175 offset:8448
	s_setprio 1
	s_waitcnt vmcnt(11) lgkmcnt(1)
	v_mfma_f32_16x16x32_f16 v[106:109], v[62:65], v[50:53], v[110:113]
	s_waitcnt lgkmcnt(0)
	v_mfma_f32_16x16x32_f16 v[10:13], v[76:79], v[50:53], v[10:13]
	s_waitcnt vmcnt(10)
	v_mfma_f32_16x16x32_f16 v[22:25], v[62:65], v[102:105], v[22:25]
	v_mfma_f32_16x16x32_f16 v[34:37], v[76:79], v[102:105], v[34:37]
	s_waitcnt vmcnt(9)
	v_mfma_f32_16x16x32_f16 v[38:41], v[62:65], v[114:117], v[38:41]
	v_mfma_f32_16x16x32_f16 v[14:17], v[76:79], v[114:117], v[14:17]
	s_waitcnt vmcnt(8)
	v_mfma_f32_16x16x32_f16 v[42:45], v[62:65], v[118:121], v[42:45]
	v_mfma_f32_16x16x32_f16 v[18:21], v[76:79], v[118:121], v[18:21]
	s_setprio 0
	ds_read_b128 v[50:53], v176
	ds_read_b128 v[62:65], v176 offset:8448
	s_setprio 1
	s_waitcnt vmcnt(7) lgkmcnt(1)
	v_mfma_f32_16x16x32_f16 v[76:79], v[50:53], v[84:87], v[106:109]
	s_waitcnt lgkmcnt(0)
	v_mfma_f32_16x16x32_f16 v[10:13], v[62:65], v[84:87], v[10:13]
	s_waitcnt vmcnt(6)
	v_mfma_f32_16x16x32_f16 v[22:25], v[50:53], v[88:91], v[22:25]
	v_mfma_f32_16x16x32_f16 v[34:37], v[62:65], v[88:91], v[34:37]
	s_waitcnt vmcnt(5)
	v_mfma_f32_16x16x32_f16 v[38:41], v[50:53], v[92:95], v[38:41]
	v_mfma_f32_16x16x32_f16 v[14:17], v[62:65], v[92:95], v[14:17]
	s_waitcnt vmcnt(4)
	v_mfma_f32_16x16x32_f16 v[42:45], v[50:53], v[96:99], v[42:45]
	v_mfma_f32_16x16x32_f16 v[18:21], v[62:65], v[96:99], v[18:21]
	s_setprio 0
	ds_read_b128 v[50:53], v177
	ds_read_b128 v[62:65], v177 offset:8448
	s_setprio 1
	s_waitcnt vmcnt(3) lgkmcnt(1)
	v_mfma_f32_16x16x32_f16 v[76:79], v[50:53], v[46:49], v[76:79]
	s_waitcnt lgkmcnt(0)
	v_mfma_f32_16x16x32_f16 v[10:13], v[62:65], v[46:49], v[10:13]
	s_waitcnt vmcnt(2)
	v_mfma_f32_16x16x32_f16 v[22:25], v[50:53], v[54:57], v[22:25]
	v_mfma_f32_16x16x32_f16 v[34:37], v[62:65], v[54:57], v[34:37]
	s_waitcnt vmcnt(1)
	v_mfma_f32_16x16x32_f16 v[38:41], v[50:53], v[68:71], v[38:41]
	v_mfma_f32_16x16x32_f16 v[14:17], v[62:65], v[68:71], v[14:17]
	s_waitcnt vmcnt(0)
	v_mfma_f32_16x16x32_f16 v[42:45], v[50:53], v[72:75], v[42:45]
	v_mfma_f32_16x16x32_f16 v[18:21], v[62:65], v[72:75], v[18:21]
	s_setprio 0
	v_add_co_u32_e32 v108, vcc, s29, v152
	v_and_b32_e32 v67, 0x1c0, v0
	s_nop 0
	v_addc_co_u32_e32 v109, vcc, 0, v153, vcc
	v_add_co_u32_e32 v46, vcc, s52, v152
	s_movk_i32 s4, 0x50
	s_nop 0
	v_addc_co_u32_e32 v47, vcc, 0, v153, vcc
	v_add_co_u32_e32 v68, vcc, s33, v152
	v_or_b32_e32 v116, 16, v67
	s_nop 0
	v_addc_co_u32_e32 v69, vcc, 0, v153, vcc
	v_add_co_u32_e32 v110, vcc, s52, v154
	global_load_dwordx4 v[46:49], v[46:47], off
	s_nop 0
	global_load_dwordx4 v[50:53], v[68:69], off
	global_load_dwordx4 v[54:57], v[152:153], off
	global_load_dwordx4 v[62:65], v[154:155], off
	v_addc_co_u32_e32 v111, vcc, 0, v155, vcc
	v_add_co_u32_e32 v112, vcc, s52, v160
	global_load_dwordx4 v[68:71], v[156:157], off
	global_load_dwordx4 v[72:75], v[158:159], off
	global_load_dwordx4 v[84:87], v[160:161], off
	global_load_dwordx4 v[88:91], v[162:163], off
	v_addc_co_u32_e32 v113, vcc, 0, v161, vcc
	global_load_dwordx4 v[92:95], v[110:111], off
	global_load_dwordx4 v[96:99], v[112:113], off
	global_load_dwordx4 v[100:103], v[108:109], off
	global_load_dwordx4 v[104:107], v[164:165], off
	s_nop 0
	global_store_dwordx4 v[166:167], v[2:5], off sc0 sc1
	global_store_dwordx4 v[168:169], v[6:9], off sc0 sc1
	global_store_dwordx4 v[170:171], v[26:29], off sc0 sc1
	global_store_dwordx4 v[58:59], v[30:33], off sc0 sc1
	v_and_b32_e32 v4, 0x1cf, v0
	v_cvt_pk_f16_f32 v3, v78, v79
	v_cvt_pk_f16_f32 v2, v76, v77
	v_mad_u32_u24 v4, v4, s4, v80
	v_or_b32_e32 v5, v116, v81
	v_or_b32_e32 v117, 32, v67
	ds_write_b64 v4, v[2:3]
	v_cvt_pk_f16_f32 v3, v24, v25
	v_cvt_pk_f16_f32 v2, v22, v23
	v_mad_u32_u24 v5, v5, s4, v80
	v_or_b32_e32 v6, v117, v81
	v_or_b32_e32 v118, 48, v67
	ds_write_b64 v5, v[2:3]
	v_cvt_pk_f16_f32 v3, v40, v41
	v_cvt_pk_f16_f32 v2, v38, v39
	v_mad_u32_u24 v6, v6, s4, v80
	v_or_b32_e32 v7, v118, v81
	ds_write_b64 v6, v[2:3]
	v_cvt_pk_f16_f32 v3, v44, v45
	v_cvt_pk_f16_f32 v2, v42, v43
	v_mad_u32_u24 v7, v7, s4, v80
	ds_write_b64 v7, v[2:3]
	v_cvt_pk_f16_f32 v3, v12, v13
	v_cvt_pk_f16_f32 v2, v10, v11
	ds_write_b64 v4, v[2:3] offset:32
	v_cvt_pk_f16_f32 v3, v36, v37
	v_cvt_pk_f16_f32 v2, v34, v35
	ds_write_b64 v5, v[2:3] offset:32
	v_cvt_pk_f16_f32 v3, v16, v17
	v_cvt_pk_f16_f32 v2, v14, v15
	v_lshl_add_u64 v[10:11], v[60:61], 0, s[14:15]
	ds_write_b64 v6, v[2:3] offset:32
	v_cvt_pk_f16_f32 v2, v18, v19
	v_add_co_u32_e32 v18, vcc, s52, v10
	v_cvt_pk_f16_f32 v3, v20, v21
	v_lshl_add_u64 v[12:13], v[60:61], 0, s[16:17]
	v_addc_co_u32_e32 v19, vcc, 0, v11, vcc
	ds_write_b64 v7, v[2:3] offset:32
	s_waitcnt lgkmcnt(0)
	s_barrier
	global_load_dwordx4 v[2:5], v[10:11], off
	global_load_dwordx4 v[6:9], v[12:13], off
	v_lshl_add_u64 v[20:21], v[60:61], 0, s[12:13]
	global_load_dwordx4 v[10:13], v[18:19], off
	global_load_dwordx4 v[14:17], v[20:21], off
	ds_read_b128 v[18:21], v1
	ds_read_b128 v[22:25], v1 offset:8448
	s_mov_b32 s3, s27
	s_setprio 1
	s_waitcnt vmcnt(17) lgkmcnt(1)
	v_mfma_f32_16x16x32_f16 v[26:29], v[18:21], v[54:57], 0
	s_waitcnt lgkmcnt(0)
	v_mfma_f32_16x16x32_f16 v[30:33], v[22:25], v[54:57], 0
	s_waitcnt vmcnt(9)
	v_mfma_f32_16x16x32_f16 v[34:37], v[18:21], v[100:103], 0
	v_mfma_f32_16x16x32_f16 v[38:41], v[22:25], v[100:103], 0
	v_mfma_f32_16x16x32_f16 v[42:45], v[18:21], v[46:49], 0
	v_mfma_f32_16x16x32_f16 v[46:49], v[22:25], v[46:49], 0
	v_mfma_f32_16x16x32_f16 v[18:21], v[18:21], v[50:53], 0
	v_mfma_f32_16x16x32_f16 v[22:25], v[22:25], v[50:53], 0
	s_setprio 0
	v_lshl_add_u64 v[58:59], v[60:61], 0, s[10:11]
	v_add_co_u32_e32 v76, vcc, s29, v58
	s_nop 1
	v_addc_co_u32_e32 v77, vcc, 0, v59, vcc
	v_add_co_u32_e32 v108, vcc, s52, v58
	global_load_dwordx4 v[50:53], v[58:59], off
	global_load_dwordx4 v[54:57], v[76:77], off
	v_addc_co_u32_e32 v109, vcc, 0, v59, vcc
	v_add_co_u32_e32 v58, vcc, s33, v58
	s_nop 1
	v_addc_co_u32_e32 v59, vcc, 0, v59, vcc
	global_load_dwordx4 v[76:79], v[108:109], off
	global_load_dwordx4 v[100:103], v[58:59], off
	ds_read_b128 v[108:111], v82
	ds_read_b128 v[112:115], v82 offset:8448
	s_setprio 1
	s_waitcnt lgkmcnt(1)
	v_mfma_f32_16x16x32_f16 v[26:29], v[108:111], v[62:65], v[26:29]
	s_waitcnt lgkmcnt(0)
	v_mfma_f32_16x16x32_f16 v[30:33], v[112:115], v[62:65], v[30:33]
	v_mfma_f32_16x16x32_f16 v[34:37], v[108:111], v[68:71], v[34:37]
	v_mfma_f32_16x16x32_f16 v[38:41], v[112:115], v[68:71], v[38:41]
	v_mfma_f32_16x16x32_f16 v[42:45], v[108:111], v[92:95], v[42:45]
	v_mfma_f32_16x16x32_f16 v[46:49], v[112:115], v[92:95], v[46:49]
	v_mfma_f32_16x16x32_f16 v[18:21], v[108:111], v[72:75], v[18:21]
	v_mfma_f32_16x16x32_f16 v[22:25], v[112:115], v[72:75], v[22:25]
	s_setprio 0
	v_lshl_add_u64 v[58:59], v[60:61], 0, s[48:49]
	v_lshl_add_u64 v[72:73], v[60:61], 0, s[50:51]
	global_load_dwordx4 v[62:65], v[58:59], off
	global_load_dwordx4 v[68:71], v[72:73], off
	v_add_co_u32_e32 v58, vcc, s52, v58
	v_lshl_add_u64 v[82:83], v[60:61], 0, s[46:47]
	s_nop 0
	v_addc_co_u32_e32 v59, vcc, 0, v59, vcc
	global_load_dwordx4 v[72:75], v[58:59], off
	global_load_dwordx4 v[92:95], v[82:83], off
	ds_read_b128 v[108:111], v172
	ds_read_b128 v[112:115], v172 offset:8448
	s_setprio 1
	s_waitcnt lgkmcnt(1)
	v_mfma_f32_16x16x32_f16 v[26:29], v[108:111], v[84:87], v[26:29]
	s_waitcnt lgkmcnt(0)
	v_mfma_f32_16x16x32_f16 v[30:33], v[112:115], v[84:87], v[30:33]
	v_mfma_f32_16x16x32_f16 v[34:37], v[108:111], v[88:91], v[34:37]
	v_mfma_f32_16x16x32_f16 v[38:41], v[112:115], v[88:91], v[38:41]
	v_mfma_f32_16x16x32_f16 v[42:45], v[108:111], v[96:99], v[42:45]
	v_mfma_f32_16x16x32_f16 v[46:49], v[112:115], v[96:99], v[46:49]
	s_waitcnt vmcnt(16)
	v_mfma_f32_16x16x32_f16 v[18:21], v[108:111], v[104:107], v[18:21]
	v_mfma_f32_16x16x32_f16 v[22:25], v[112:115], v[104:107], v[22:25]
	s_setprio 0
	v_lshl_add_u64 v[58:59], v[60:61], 0, s[42:43]
	v_lshl_add_u64 v[90:91], v[60:61], 0, s[44:45]
	global_load_dwordx4 v[82:85], v[58:59], off
	global_load_dwordx4 v[86:89], v[90:91], off
	v_add_co_u32_e32 v58, vcc, s52, v58
	v_lshl_add_u64 v[90:91], v[60:61], 0, s[40:41]
	s_nop 0
	v_addc_co_u32_e32 v59, vcc, 0, v59, vcc
	global_load_dwordx4 v[96:99], v[58:59], off
	global_load_dwordx4 v[104:107], v[90:91], off
	ds_read_b128 v[108:111], v173
	ds_read_b128 v[112:115], v173 offset:8448
	s_setprio 1
	s_waitcnt vmcnt(15) lgkmcnt(1)
	v_mfma_f32_16x16x32_f16 v[26:29], v[108:111], v[2:5], v[26:29]
	s_waitcnt lgkmcnt(0)
	v_mfma_f32_16x16x32_f16 v[2:5], v[112:115], v[2:5], v[30:33]
	s_waitcnt vmcnt(14)
	v_mfma_f32_16x16x32_f16 v[30:33], v[108:111], v[6:9], v[34:37]
	v_mfma_f32_16x16x32_f16 v[6:9], v[112:115], v[6:9], v[38:41]
	s_waitcnt vmcnt(13)
	v_mfma_f32_16x16x32_f16 v[34:37], v[108:111], v[10:13], v[42:45]
	v_mfma_f32_16x16x32_f16 v[10:13], v[112:115], v[10:13], v[46:49]
	s_waitcnt vmcnt(12)
	v_mfma_f32_16x16x32_f16 v[18:21], v[108:111], v[14:17], v[18:21]
	v_mfma_f32_16x16x32_f16 v[14:17], v[112:115], v[14:17], v[22:25]
	s_setprio 0
	v_lshl_add_u64 v[42:43], v[60:61], 0, s[8:9]
	v_add_co_u32_e32 v58, vcc, s52, v42
	v_lshl_add_u64 v[44:45], v[60:61], 0, s[38:39]
	s_nop 0
	v_addc_co_u32_e32 v59, vcc, 0, v43, vcc
	global_load_dwordx4 v[22:25], v[42:43], off
	global_load_dwordx4 v[38:41], v[44:45], off
	v_lshl_add_u64 v[60:61], v[60:61], 0, s[6:7]
	global_load_dwordx4 v[42:45], v[58:59], off
	global_load_dwordx4 v[46:49], v[60:61], off
	ds_read_b128 v[58:61], v174
	ds_read_b128 v[108:111], v174 offset:8448
	s_setprio 1
	s_waitcnt vmcnt(15) lgkmcnt(1)
	v_mfma_f32_16x16x32_f16 v[26:29], v[58:61], v[50:53], v[26:29]
	s_waitcnt lgkmcnt(0)
	v_mfma_f32_16x16x32_f16 v[2:5], v[108:111], v[50:53], v[2:5]
	s_waitcnt vmcnt(14)
	v_mfma_f32_16x16x32_f16 v[30:33], v[58:61], v[54:57], v[30:33]
	v_mfma_f32_16x16x32_f16 v[6:9], v[108:111], v[54:57], v[6:9]
	s_waitcnt vmcnt(13)
	v_mfma_f32_16x16x32_f16 v[34:37], v[58:61], v[76:79], v[34:37]
	v_mfma_f32_16x16x32_f16 v[10:13], v[108:111], v[76:79], v[10:13]
	s_waitcnt vmcnt(12)
	v_mfma_f32_16x16x32_f16 v[18:21], v[58:61], v[100:103], v[18:21]
	v_mfma_f32_16x16x32_f16 v[14:17], v[108:111], v[100:103], v[14:17]
	s_setprio 0
	ds_read_b128 v[50:53], v175
	ds_read_b128 v[54:57], v175 offset:8448
	s_setprio 1
	s_waitcnt vmcnt(11) lgkmcnt(1)
	v_mfma_f32_16x16x32_f16 v[26:29], v[50:53], v[62:65], v[26:29]
	s_waitcnt lgkmcnt(0)
	v_mfma_f32_16x16x32_f16 v[2:5], v[54:57], v[62:65], v[2:5]
	s_waitcnt vmcnt(10)
	v_mfma_f32_16x16x32_f16 v[30:33], v[50:53], v[68:71], v[30:33]
	v_mfma_f32_16x16x32_f16 v[6:9], v[54:57], v[68:71], v[6:9]
	s_waitcnt vmcnt(9)
	v_mfma_f32_16x16x32_f16 v[34:37], v[50:53], v[72:75], v[34:37]
	v_mfma_f32_16x16x32_f16 v[10:13], v[54:57], v[72:75], v[10:13]
	s_waitcnt vmcnt(8)
	v_mfma_f32_16x16x32_f16 v[18:21], v[50:53], v[92:95], v[18:21]
	v_mfma_f32_16x16x32_f16 v[14:17], v[54:57], v[92:95], v[14:17]
	s_setprio 0
	ds_read_b128 v[50:53], v176
	ds_read_b128 v[54:57], v176 offset:8448
	s_setprio 1
	s_waitcnt vmcnt(7) lgkmcnt(1)
	v_mfma_f32_16x16x32_f16 v[26:29], v[50:53], v[82:85], v[26:29]
	s_waitcnt lgkmcnt(0)
	v_mfma_f32_16x16x32_f16 v[2:5], v[54:57], v[82:85], v[2:5]
	s_waitcnt vmcnt(6)
	v_mfma_f32_16x16x32_f16 v[30:33], v[50:53], v[86:89], v[30:33]
	v_mfma_f32_16x16x32_f16 v[6:9], v[54:57], v[86:89], v[6:9]
	s_waitcnt vmcnt(5)
	v_mfma_f32_16x16x32_f16 v[34:37], v[50:53], v[96:99], v[34:37]
	v_mfma_f32_16x16x32_f16 v[58:61], v[54:57], v[96:99], v[10:13]
	s_waitcnt vmcnt(4)
	v_mfma_f32_16x16x32_f16 v[18:21], v[50:53], v[104:107], v[18:21]
	v_mfma_f32_16x16x32_f16 v[50:53], v[54:57], v[104:107], v[14:17]
	s_setprio 0
	ds_read_b128 v[54:57], v177
	ds_read_b128 v[62:65], v177 offset:8448
	s_setprio 1
	s_waitcnt vmcnt(3) lgkmcnt(1)
	v_mfma_f32_16x16x32_f16 v[26:29], v[54:57], v[22:25], v[26:29]
	s_waitcnt lgkmcnt(0)
	v_mfma_f32_16x16x32_f16 v[14:17], v[62:65], v[22:25], v[2:5]
	s_waitcnt vmcnt(2)
	v_mfma_f32_16x16x32_f16 v[22:25], v[54:57], v[38:41], v[30:33]
	v_mfma_f32_16x16x32_f16 v[10:13], v[62:65], v[38:41], v[6:9]
	s_waitcnt vmcnt(1)
	v_mfma_f32_16x16x32_f16 v[30:33], v[54:57], v[42:45], v[34:37]
	v_mfma_f32_16x16x32_f16 v[6:9], v[62:65], v[42:45], v[58:61]
	s_waitcnt vmcnt(0)
	v_mfma_f32_16x16x32_f16 v[34:37], v[54:57], v[46:49], v[18:21]
	v_mfma_f32_16x16x32_f16 v[2:5], v[62:65], v[46:49], v[50:53]
	s_setprio 0
	s_nop 1
	v_mul_u32_u24_e32 v52, 0x50, v0
	ds_read_b128 v[18:21], v52
	s_lshl_b64 s[2:3], s[2:3], 15
	v_or_b32_e32 v0, s2, v66
	v_mov_b32_e32 v1, s3
	v_lshl_add_u64 v[50:51], s[24:25], 0, v[0:1]
	ds_read_b128 v[38:41], v52 offset:16
	ds_read_b128 v[42:45], v52 offset:32
	ds_read_b128 v[46:49], v52 offset:48
	s_waitcnt lgkmcnt(3)
	global_store_dwordx4 v[50:51], v[18:21], off sc0 sc1
	s_nop 1
	v_add_co_u32_e32 v18, vcc, s29, v50
	s_nop 1
	v_addc_co_u32_e32 v19, vcc, 0, v51, vcc
	s_waitcnt lgkmcnt(2)
	global_store_dwordx4 v[18:19], v[38:41], off sc0 sc1
	v_or_b32_e32 v18, 0x4000, v0
	v_mov_b32_e32 v19, s3
	v_lshl_add_u64 v[20:21], s[24:25], 0, v[18:19]
	s_waitcnt lgkmcnt(1)
	global_store_dwordx4 v[20:21], v[42:45], off sc0 sc1
	v_add_co_u32_e32 v20, vcc, s33, v50
	v_or_b32_e32 v39, 0x200, v81
	s_nop 0
	v_addc_co_u32_e32 v21, vcc, 0, v51, vcc
	s_waitcnt lgkmcnt(0)
	global_store_dwordx4 v[20:21], v[46:49], off sc0 sc1
	v_lshl_add_u64 v[0:1], s[0:1], 0, v[0:1]
	v_mov_b32_e32 v180, 0xbfb8aa3b
	v_mov_b32_e32 v181, 0xbfb8aa3b
	v_mov_b32_e32 v182, 1.0
	v_mov_b32_e32 v183, 1.0
	v_or_b32_e32 v184, v39, v67
	v_mad_u32_u24 v184, v184, s4, v80
	v_or_b32_e32 v185, v116, v39
	v_mad_u32_u24 v185, v185, s4, v80
	v_or_b32_e32 v186, v117, v39
	v_mad_u32_u24 v186, v186, s4, v80
	v_or_b32_e32 v187, v118, v39
	v_mad_u32_u24 v187, v187, s4, v80
	v_pk_mul_f32 v[188:189], v[26:27], v[180:181]
	v_pk_mul_f32 v[190:191], v[28:29], v[180:181]
	v_pk_mul_f32 v[196:197], v[22:23], v[180:181]
	v_pk_mul_f32 v[198:199], v[24:25], v[180:181]
	v_pk_mul_f32 v[204:205], v[30:31], v[180:181]
	v_pk_mul_f32 v[206:207], v[32:33], v[180:181]
	v_pk_mul_f32 v[212:213], v[34:35], v[180:181]
	v_pk_mul_f32 v[214:215], v[36:37], v[180:181]
	v_pk_mul_f32 v[220:221], v[14:15], v[180:181]
	v_pk_mul_f32 v[222:223], v[16:17], v[180:181]
	v_pk_mul_f32 v[228:229], v[10:11], v[180:181]
	v_pk_mul_f32 v[230:231], v[12:13], v[180:181]
	v_pk_mul_f32 v[236:237], v[6:7], v[180:181]
	v_pk_mul_f32 v[238:239], v[8:9], v[180:181]
	v_pk_mul_f32 v[244:245], v[2:3], v[180:181]
	v_pk_mul_f32 v[246:247], v[4:5], v[180:181]
	v_exp_f32_e32 v188, v188
	v_exp_f32_e32 v189, v189
	v_exp_f32_e32 v190, v190
	v_exp_f32_e32 v191, v191
	v_exp_f32_e32 v196, v196
	v_exp_f32_e32 v197, v197
	v_exp_f32_e32 v198, v198
	v_exp_f32_e32 v199, v199
	v_exp_f32_e32 v204, v204
	v_exp_f32_e32 v205, v205
	v_exp_f32_e32 v206, v206
	v_exp_f32_e32 v207, v207
	v_exp_f32_e32 v212, v212
	v_exp_f32_e32 v213, v213
	v_exp_f32_e32 v214, v214
	v_exp_f32_e32 v215, v215
	v_exp_f32_e32 v220, v220
	v_exp_f32_e32 v221, v221
	v_exp_f32_e32 v222, v222
	v_exp_f32_e32 v223, v223
	v_exp_f32_e32 v228, v228
	v_exp_f32_e32 v229, v229
	v_exp_f32_e32 v230, v230
	v_exp_f32_e32 v231, v231
	v_exp_f32_e32 v236, v236
	v_exp_f32_e32 v237, v237
	v_exp_f32_e32 v238, v238
	v_exp_f32_e32 v239, v239
	v_exp_f32_e32 v244, v244
	v_exp_f32_e32 v245, v245
	v_exp_f32_e32 v246, v246
	v_exp_f32_e32 v247, v247
	v_pk_add_f32 v[188:189], v[188:189], v[182:183]
	v_pk_add_f32 v[190:191], v[190:191], v[182:183]
	v_pk_add_f32 v[196:197], v[196:197], v[182:183]
	v_pk_add_f32 v[198:199], v[198:199], v[182:183]
	v_pk_add_f32 v[204:205], v[204:205], v[182:183]
	v_pk_add_f32 v[206:207], v[206:207], v[182:183]
	v_pk_add_f32 v[212:213], v[212:213], v[182:183]
	v_pk_add_f32 v[214:215], v[214:215], v[182:183]
	v_pk_add_f32 v[220:221], v[220:221], v[182:183]
	v_pk_add_f32 v[222:223], v[222:223], v[182:183]
	v_pk_add_f32 v[228:229], v[228:229], v[182:183]
	v_pk_add_f32 v[230:231], v[230:231], v[182:183]
	v_pk_add_f32 v[236:237], v[236:237], v[182:183]
	v_pk_add_f32 v[238:239], v[238:239], v[182:183]
	v_pk_add_f32 v[244:245], v[244:245], v[182:183]
	v_pk_add_f32 v[246:247], v[246:247], v[182:183]
	v_rcp_f32_e32 v188, v188
	v_rcp_f32_e32 v189, v189
	v_rcp_f32_e32 v190, v190
	v_rcp_f32_e32 v191, v191
	v_rcp_f32_e32 v196, v196
	v_rcp_f32_e32 v197, v197
	v_rcp_f32_e32 v198, v198
	v_rcp_f32_e32 v199, v199
	v_rcp_f32_e32 v204, v204
	v_rcp_f32_e32 v205, v205
	v_rcp_f32_e32 v206, v206
	v_rcp_f32_e32 v207, v207
	v_rcp_f32_e32 v212, v212
	v_rcp_f32_e32 v213, v213
	v_rcp_f32_e32 v214, v214
	v_rcp_f32_e32 v215, v215
	v_rcp_f32_e32 v220, v220
	v_rcp_f32_e32 v221, v221
	v_rcp_f32_e32 v222, v222
	v_rcp_f32_e32 v223, v223
	v_rcp_f32_e32 v228, v228
	v_rcp_f32_e32 v229, v229
	v_rcp_f32_e32 v230, v230
	v_rcp_f32_e32 v231, v231
	v_rcp_f32_e32 v236, v236
	v_rcp_f32_e32 v237, v237
	v_rcp_f32_e32 v238, v238
	v_rcp_f32_e32 v239, v239
	v_rcp_f32_e32 v244, v244
	v_rcp_f32_e32 v245, v245
	v_rcp_f32_e32 v246, v246
	v_rcp_f32_e32 v247, v247
	v_fma_mixlo_f16 v192, v26, v188, 0
	v_mul_f32_e32 v189, v27, v189
	v_mul_f32_e32 v190, v28, v190
	v_fma_mixlo_f16 v193, v29, v191, 0
	v_fma_mixlo_f16 v200, v22, v196, 0
	v_mul_f32_e32 v197, v23, v197
	v_mul_f32_e32 v198, v24, v198
	v_fma_mixlo_f16 v201, v25, v199, 0
	v_fma_mixlo_f16 v208, v30, v204, 0
	v_mul_f32_e32 v205, v31, v205
	v_mul_f32_e32 v206, v32, v206
	v_fma_mixlo_f16 v209, v33, v207, 0
	v_fma_mixlo_f16 v216, v34, v212, 0
	v_mul_f32_e32 v213, v35, v213
	v_mul_f32_e32 v214, v36, v214
	v_fma_mixlo_f16 v217, v37, v215, 0
	v_fma_mixlo_f16 v224, v14, v220, 0
	v_mul_f32_e32 v221, v15, v221
	v_mul_f32_e32 v222, v16, v222
	v_fma_mixlo_f16 v225, v17, v223, 0
	v_fma_mixlo_f16 v232, v10, v228, 0
	v_mul_f32_e32 v229, v11, v229
	v_mul_f32_e32 v230, v12, v230
	v_fma_mixlo_f16 v233, v13, v231, 0
	v_fma_mixlo_f16 v240, v6, v236, 0
	v_mul_f32_e32 v237, v7, v237
	v_mul_f32_e32 v238, v8, v238
	v_fma_mixlo_f16 v241, v9, v239, 0
	v_fma_mixlo_f16 v248, v2, v244, 0
	v_mul_f32_e32 v245, v3, v245
	v_mul_f32_e32 v246, v4, v246
	v_fma_mixlo_f16 v249, v5, v247, 0
	v_cvt_pk_f16_f32 v188, v189, v190
	v_cvt_pk_f16_f32 v196, v197, v198
	v_cvt_pk_f16_f32 v204, v205, v206
	v_cvt_pk_f16_f32 v212, v213, v214
	v_cvt_pk_f16_f32 v220, v221, v222
	v_cvt_pk_f16_f32 v228, v229, v230
	v_cvt_pk_f16_f32 v236, v237, v238
	v_cvt_pk_f16_f32 v244, v245, v246
	v_pack_b32_f16 v194, v192, v188
	v_alignbit_b32 v195, v193, v188, 16
	v_pack_b32_f16 v202, v200, v196
	v_alignbit_b32 v203, v201, v196, 16
	v_pack_b32_f16 v210, v208, v204
	v_alignbit_b32 v211, v209, v204, 16
	v_pack_b32_f16 v218, v216, v212
	v_alignbit_b32 v219, v217, v212, 16
	v_pack_b32_f16 v226, v224, v220
	v_alignbit_b32 v227, v225, v220, 16
	v_pack_b32_f16 v234, v232, v228
	v_alignbit_b32 v235, v233, v228, 16
	v_pack_b32_f16 v242, v240, v236
	v_alignbit_b32 v243, v241, v236, 16
	v_pack_b32_f16 v250, v248, v244
	v_alignbit_b32 v251, v249, v244, 16
	ds_write_b64 v184, v[194:195]
	ds_write_b64 v185, v[202:203]
	ds_write_b64 v186, v[210:211]
	ds_write_b64 v187, v[218:219]
	ds_write_b64 v184, v[226:227] offset:32
	ds_write_b64 v185, v[234:235] offset:32
	ds_write_b64 v186, v[242:243] offset:32
	ds_write_b64 v187, v[250:251] offset:32
	s_waitcnt lgkmcnt(0)
	s_barrier
	ds_read_b128 v[2:5], v52 offset:40960
	ds_read_b128 v[6:9], v52 offset:40976
	ds_read_b128 v[10:13], v52 offset:40992
	ds_read_b128 v[14:17], v52 offset:41008
	s_waitcnt lgkmcnt(3)
	global_store_dwordx4 v[0:1], v[2:5], off sc0 sc1
	s_nop 1
	v_add_co_u32_e32 v2, vcc, 0x2000, v0
	s_nop 1
	v_addc_co_u32_e32 v3, vcc, 0, v1, vcc
	v_add_co_u32_e32 v0, vcc, 0x6000, v0
	s_waitcnt lgkmcnt(2)
	global_store_dwordx4 v[2:3], v[6:9], off sc0 sc1
	v_lshl_add_u64 v[2:3], s[0:1], 0, v[18:19]
	v_addc_co_u32_e32 v1, vcc, 0, v1, vcc
	s_waitcnt lgkmcnt(1)
	global_store_dwordx4 v[2:3], v[10:13], off sc0 sc1
	s_waitcnt lgkmcnt(0)
	global_store_dwordx4 v[0:1], v[14:17], off sc0 sc1
	s_endpgm
	.p2align	8
